# speedup vs baseline: 1.0572x; 1.0464x over previous
_Z10qkv_kernelPKfPK15HIP_vector_typeIjLj4EEPDv8_DF16_S6_S6_:
	s_load_dwordx8 s[4:11], s[0:1], 0x0
	s_ashr_i32 s3, s2, 2
	s_and_b32 s3, s3, -8
	s_and_b32 s12, s2, 7
	s_bfe_u32 s2, s2, 0x20003
	s_or_b32 s12, s3, s12
	s_mul_i32 s3, s2, 0x36000
	s_waitcnt lgkmcnt(0)
	s_add_u32 s6, s6, s3
	s_addc_u32 s7, s7, 0
	s_mov_b64 s[22:23], s[6:7]
	s_cmp_eq_u32 s2, 3
	s_cbranch_scc1 .Lqkv_p1N
	v_mov_b32_e32 v211, 0
	v_lshlrev_b32_e32 v208, 4, v0
	v_mov_b32_e32 v209, v211
	v_lshl_add_u64 v[2:3], s[6:7], 0, v[208:209]
	s_movk_i32 s3, 0x2000
	v_add_co_u32_e32 v4, vcc, s3, v2
	v_lshrrev_b32_e32 v214, 6, v0
	s_nop 0
	v_addc_co_u32_e32 v5, vcc, 0, v3, vcc
	s_movk_i32 s3, 0x4000
	v_add_co_u32_e32 v6, vcc, s3, v2
	v_lshlrev_b32_e32 v1, 5, v214
	v_addc_co_u32_e32 v7, vcc, 0, v3, vcc
	v_lshl_or_b32 v1, s12, 8, v1
	s_movk_i32 s6, 0x600
	v_mov_b64_e32 v[4:5], s[4:5]
	v_mad_i64_i32 v[72:73], s[4:5], v1, s6, v[4:5]
	v_bfe_u32 v1, v0, 4, 2
	v_and_b32_e32 v80, 15, v0
	v_lshlrev_b32_e32 v210, 4, v80
	v_mul_u32_u24_e32 v4, 0x180, v1
	v_lshl_add_u64 v[40:41], v[72:73], 0, v[210:211]
	v_lshlrev_b32_e32 v48, 2, v4
	v_mov_b32_e32 v49, v211
	v_lshl_add_u64 v[12:13], v[40:41], 0, v[48:49]
	s_movk_i32 s4, 0x1000
	v_add_co_u32_e32 v14, vcc, s4, v12
	s_movk_i32 s4, 0x3000
	s_nop 0
	v_addc_co_u32_e32 v15, vcc, 0, v13, vcc
	v_add_co_u32_e32 v32, vcc, s4, v12
	global_load_dwordx4 v[4:7], v[12:13], off nt
	global_load_dwordx4 v[8:11], v[14:15], off offset:2048 nt
	v_addc_co_u32_e32 v33, vcc, 0, v13, vcc
	v_add_co_u32_e32 v34, vcc, s3, v12
	v_or_b32_e32 v64, 0x6000, v48
	v_mov_b32_e32 v65, v211
	v_addc_co_u32_e32 v35, vcc, 0, v13, vcc
	global_load_dwordx4 v[12:15], v[32:33], off nt
	global_load_dwordx4 v[28:31], v[34:35], off offset:2048 nt
	v_lshl_add_u64 v[42:43], v[40:41], 0, v[64:65]
	v_add_u32_e32 v66, 0x7800, v48
	v_mov_b32_e32 v67, v211
	v_add_u32_e32 v74, 0x9000, v48
	v_mov_b32_e32 v75, v211
	v_lshl_add_u64 v[44:45], v[40:41], 0, v[66:67]
	global_load_dwordx4 v[32:35], v[42:43], off nt
	global_load_dwordx4 v[36:39], v[44:45], off nt
	v_lshl_add_u64 v[50:51], v[40:41], 0, v[74:75]
	v_add_u32_e32 v76, 0xa800, v48
	v_mov_b32_e32 v77, v211
	v_lshl_add_u64 v[52:53], v[40:41], 0, v[76:77]
	global_load_dwordx4 v[40:43], v[50:51], off nt
	global_load_dwordx4 v[44:47], v[52:53], off nt
	v_lshl_add_u64 v[48:49], v[72:73], 0, v[48:49]
	v_lshl_add_u64 v[140:141], v[48:49], 0, v[210:211]
	s_mov_b64 s[4:5], 0x1800
	v_lshl_add_u64 v[142:143], v[140:141], 0, s[4:5]
	s_mov_b64 s[4:5], 0x3000
	v_lshl_add_u64 v[64:65], v[72:73], 0, v[64:65]
	v_lshl_add_u64 v[74:75], v[72:73], 0, v[74:75]
	v_lshl_add_u64 v[144:145], v[140:141], 0, s[4:5]
	s_mov_b64 s[4:5], 0x4800
	v_lshl_add_u64 v[148:149], v[64:65], 0, v[210:211]
	v_lshl_add_u64 v[64:65], v[72:73], 0, v[66:67]
	v_lshl_add_u64 v[152:153], v[74:75], 0, v[210:211]
	v_lshl_add_u64 v[72:73], v[72:73], 0, v[76:77]
	global_load_dwordx4 v[48:51], v[140:141], off offset:256 nt
	global_load_dwordx4 v[52:55], v[142:143], off offset:256 nt
	v_lshl_add_u64 v[146:147], v[140:141], 0, s[4:5]
	global_load_dwordx4 v[56:59], v[144:145], off offset:256 nt
	global_load_dwordx4 v[60:63], v[146:147], off offset:256 nt
	v_lshl_add_u64 v[150:151], v[64:65], 0, v[210:211]
	global_load_dwordx4 v[64:67], v[148:149], off offset:256 nt
	global_load_dwordx4 v[68:71], v[150:151], off offset:256 nt
	v_lshl_add_u64 v[154:155], v[72:73], 0, v[210:211]
	global_load_dwordx4 v[72:75], v[152:153], off offset:256 nt
	global_load_dwordx4 v[76:79], v[154:155], off offset:256 nt
	v_mov_b32_e32 v236, v208
	v_add_u32_e32 v237, 0x2000, v208
	v_add_u32_e32 v238, 0x4000, v208
	global_load_dwordx4 v[160:163], v236, s[22:23]
	global_load_dwordx4 v[164:167], v237, s[22:23]
	global_load_dwordx4 v[168:171], v238, s[22:23]
	s_add_u32 s20, s22, 24576
	s_addc_u32 s21, s23, 0
	global_load_dwordx4 v[172:175], v236, s[20:21]
	global_load_dwordx4 v[176:179], v237, s[20:21]
	global_load_dwordx4 v[180:183], v238, s[20:21]
	s_add_u32 s20, s22, 49152
	s_addc_u32 s21, s23, 0
	global_load_dwordx4 v[184:187], v236, s[20:21]
	global_load_dwordx4 v[188:191], v237, s[20:21]
	global_load_dwordx4 v[192:195], v238, s[20:21]
	s_add_u32 s20, s22, 73728
	s_addc_u32 s21, s23, 0
	global_load_dwordx4 v[196:199], v236, s[20:21]
	global_load_dwordx4 v[200:203], v237, s[20:21]
	global_load_dwordx4 v[204:207], v238, s[20:21]
	s_add_u32 s20, s22, 98304
	s_addc_u32 s21, s23, 0
	global_load_dwordx4 v[216:219], v236, s[20:21]
	global_load_dwordx4 v[220:223], v237, s[20:21]
	global_load_dwordx4 v[224:227], v238, s[20:21]
	v_mul_u32_u24_e32 v82, 0x1200, v214
	v_lshl_or_b32 v80, v80, 3, v82
	s_movk_i32 s3, 0x90
	v_mad_u32_u24 v1, v1, s3, v80
	v_add_u32_e32 v157, 0x1e000, v1
	v_and_b32_e32 v81, 31, v0
	v_lshrrev_b32_e32 v83, 1, v0
	v_add_u32_e32 v1, 0x1e800, v1
	v_mul_u32_u24_e32 v81, 0x90, v81
	v_and_b32_e32 v83, 16, v83
	v_add3_u32 v156, v82, v81, v83
	v_add_u32_e32 v156, 0x12000, v156
	s_load_dwordx2 s[0:1], s[0:1], 0x20
	s_mov_b32 s3, 0
	v_and_b32_e32 v0, 63, v0
	s_waitcnt vmcnt(30)
	v_cvt_pk_f16_f32 v7, v6, v7
	v_cvt_pk_f16_f32 v6, v4, v5
	s_waitcnt vmcnt(29)
	v_cvt_pk_f16_f32 v5, v10, v11
	v_cvt_pk_f16_f32 v4, v8, v9
	ds_write2_b64 v157, v[6:7], v[4:5] offset1:72
	s_waitcnt vmcnt(28)
	v_cvt_pk_f16_f32 v5, v14, v15
	v_cvt_pk_f16_f32 v4, v12, v13
	s_waitcnt vmcnt(27)
	v_cvt_pk_f16_f32 v7, v30, v31
	v_cvt_pk_f16_f32 v6, v28, v29
	ds_write2_b64 v157, v[4:5], v[6:7] offset0:144 offset1:216
	s_waitcnt vmcnt(26)
	v_cvt_pk_f16_f32 v5, v34, v35
	v_cvt_pk_f16_f32 v4, v32, v33
	s_waitcnt vmcnt(25)
	v_cvt_pk_f16_f32 v7, v38, v39
	v_cvt_pk_f16_f32 v6, v36, v37
	ds_write2_b64 v1, v[4:5], v[6:7] offset0:32 offset1:104
	s_waitcnt vmcnt(24)
	v_cvt_pk_f16_f32 v5, v42, v43
	v_cvt_pk_f16_f32 v4, v40, v41
	s_waitcnt vmcnt(23)
	v_cvt_pk_f16_f32 v7, v46, v47
	v_cvt_pk_f16_f32 v6, v44, v45
	ds_write2_b64 v1, v[4:5], v[6:7] offset0:176 offset1:248
	ds_read_b128 v[28:31], v156 offset:49152
	ds_read_b128 v[32:35], v156 offset:49184
	ds_read_b128 v[36:39], v156 offset:49216
	ds_read_b128 v[40:43], v156 offset:49248
	global_load_dwordx4 v[4:7], v[140:141], off offset:512 nt
	global_load_dwordx4 v[8:11], v[142:143], off offset:512 nt
	global_load_dwordx4 v[12:15], v[144:145], off offset:512 nt
	global_load_dwordx4 v[80:83], v[146:147], off offset:512 nt
	global_load_dwordx4 v[84:87], v[148:149], off offset:512 nt
	global_load_dwordx4 v[88:91], v[150:151], off offset:512 nt
	global_load_dwordx4 v[92:95], v[152:153], off offset:512 nt
	global_load_dwordx4 v[96:99], v[154:155], off offset:512 nt
	s_waitcnt vmcnt(15)
	v_cvt_pk_f16_f32 v45, v50, v51
	v_cvt_pk_f16_f32 v44, v48, v49
	s_waitcnt vmcnt(14)
	v_cvt_pk_f16_f32 v47, v54, v55
	v_cvt_pk_f16_f32 v46, v52, v53
	ds_write2_b64 v157, v[44:45], v[46:47] offset1:72
	s_waitcnt vmcnt(13)
	v_cvt_pk_f16_f32 v45, v58, v59
	v_cvt_pk_f16_f32 v44, v56, v57
	s_waitcnt vmcnt(12)
	v_cvt_pk_f16_f32 v47, v62, v63
	v_cvt_pk_f16_f32 v46, v60, v61
	ds_write2_b64 v157, v[44:45], v[46:47] offset0:144 offset1:216
	s_waitcnt vmcnt(11)
	v_cvt_pk_f16_f32 v45, v66, v67
	v_cvt_pk_f16_f32 v44, v64, v65
	s_waitcnt vmcnt(10)
	v_cvt_pk_f16_f32 v47, v70, v71
	v_cvt_pk_f16_f32 v46, v68, v69
	ds_write2_b64 v1, v[44:45], v[46:47] offset0:32 offset1:104
	s_waitcnt vmcnt(9)
	v_cvt_pk_f16_f32 v45, v74, v75
	v_cvt_pk_f16_f32 v44, v72, v73
	s_waitcnt vmcnt(8)
	v_cvt_pk_f16_f32 v47, v78, v79
	v_cvt_pk_f16_f32 v46, v76, v77
	ds_write2_b64 v1, v[44:45], v[46:47] offset0:176 offset1:248
	ds_read_b128 v[44:47], v156 offset:49152
	ds_read_b128 v[48:51], v156 offset:49184
	ds_read_b128 v[52:55], v156 offset:49216
	ds_read_b128 v[56:59], v156 offset:49248
	global_load_dwordx4 v[76:79], v[140:141], off offset:768 nt
	global_load_dwordx4 v[100:103], v[142:143], off offset:768 nt
	global_load_dwordx4 v[104:107], v[144:145], off offset:768 nt
	global_load_dwordx4 v[108:111], v[146:147], off offset:768 nt
	global_load_dwordx4 v[112:115], v[148:149], off offset:768 nt
	global_load_dwordx4 v[116:119], v[150:151], off offset:768 nt
	global_load_dwordx4 v[120:123], v[152:153], off offset:768 nt
	global_load_dwordx4 v[124:127], v[154:155], off offset:768 nt
	s_mul_i32 s14, s2, 9
	s_mul_i32 s15, s12, 6
	v_lshlrev_b32_e32 v239, 4, v0
	v_add_u32_e32 v240, 0xc000, v239
	v_add_u32_e32 v242, 0x18000, v239
	v_lshlrev_b32_e32 v241, 12, v214
	v_or_b32_e32 v241, v241, v239
	v_add_u32_e32 v252, 0x12000, v236
	v_add_u32_e32 v253, 0x12000, v237
	v_add_u32_e32 v254, 0x12000, v238
	ds_write_b128 v236, v[160:163] offset:0
	ds_write_b128 v237, v[164:167] offset:0
	ds_write_b128 v238, v[168:171] offset:0
	ds_write_b128 v236, v[172:175] offset:24576
	ds_write_b128 v237, v[176:179] offset:24576
	ds_write_b128 v238, v[180:183] offset:24576
	ds_write_b128 v236, v[184:187] offset:49152
	ds_write_b128 v237, v[188:191] offset:49152
	ds_write_b128 v238, v[192:195] offset:49152
	ds_write_b128 v252, v[196:199] offset:0
	ds_write_b128 v253, v[200:203] offset:0
	ds_write_b128 v254, v[204:207] offset:0
	ds_write_b128 v252, v[216:219] offset:24576
	ds_write_b128 v253, v[220:223] offset:24576
	ds_write_b128 v254, v[224:227] offset:24576
	s_waitcnt lgkmcnt(0)
	s_barrier
	ds_read_b128 v[216:219], v239 offset:0
	ds_read_b128 v[220:223], v239 offset:24576
	ds_read_b128 v[224:227], v240 offset:0
	ds_read_b128 v[228:231], v239 offset:1024
	s_waitcnt lgkmcnt(3)
	v_mfma_f32_32x32x16_f16 v[160:175], v[216:219], v[28:31], 0
	ds_read_b128 v[216:219], v239 offset:25600
	s_waitcnt lgkmcnt(3)
	v_mfma_f32_32x32x16_f16 v[176:191], v[220:223], v[28:31], 0
	ds_read_b128 v[220:223], v240 offset:1024
	s_waitcnt lgkmcnt(3)
	v_mfma_f32_32x32x16_f16 v[192:207], v[224:227], v[28:31], 0
	ds_read_b128 v[224:227], v239 offset:2048
	s_waitcnt lgkmcnt(3)
	v_mfma_f32_32x32x16_f16 v[160:175], v[228:231], v[32:35], v[160:175]
	ds_read_b128 v[228:231], v239 offset:26624
	s_waitcnt lgkmcnt(3)
	v_mfma_f32_32x32x16_f16 v[176:191], v[216:219], v[32:35], v[176:191]
	ds_read_b128 v[216:219], v240 offset:2048
	s_waitcnt lgkmcnt(3)
	v_mfma_f32_32x32x16_f16 v[192:207], v[220:223], v[32:35], v[192:207]
	ds_read_b128 v[220:223], v239 offset:3072
	s_waitcnt lgkmcnt(3)
	v_mfma_f32_32x32x16_f16 v[160:175], v[224:227], v[36:39], v[160:175]
	ds_read_b128 v[224:227], v239 offset:27648
	s_waitcnt lgkmcnt(3)
	v_mfma_f32_32x32x16_f16 v[176:191], v[228:231], v[36:39], v[176:191]
	ds_read_b128 v[228:231], v240 offset:3072
	s_waitcnt lgkmcnt(3)
	v_mfma_f32_32x32x16_f16 v[192:207], v[216:219], v[36:39], v[192:207]
	s_waitcnt lgkmcnt(2)
	v_mfma_f32_32x32x16_f16 v[160:175], v[220:223], v[40:43], v[160:175]
	s_waitcnt lgkmcnt(1)
	v_mfma_f32_32x32x16_f16 v[176:191], v[224:227], v[40:43], v[176:191]
	s_waitcnt lgkmcnt(0)
	v_mfma_f32_32x32x16_f16 v[192:207], v[228:231], v[40:43], v[192:207]
	ds_read_b128 v[216:219], v239 offset:4096
	ds_read_b128 v[220:223], v239 offset:28672
	ds_read_b128 v[224:227], v240 offset:4096
	ds_read_b128 v[228:231], v239 offset:5120
	s_waitcnt lgkmcnt(3)
	v_mfma_f32_32x32x16_f16 v[160:175], v[216:219], v[44:47], v[160:175]
	ds_read_b128 v[216:219], v239 offset:29696
	s_waitcnt lgkmcnt(3)
	v_mfma_f32_32x32x16_f16 v[176:191], v[220:223], v[44:47], v[176:191]
	ds_read_b128 v[220:223], v240 offset:5120
	s_waitcnt lgkmcnt(3)
	v_mfma_f32_32x32x16_f16 v[192:207], v[224:227], v[44:47], v[192:207]
	ds_read_b128 v[224:227], v239 offset:6144
	s_waitcnt lgkmcnt(3)
	v_mfma_f32_32x32x16_f16 v[160:175], v[228:231], v[48:51], v[160:175]
	ds_read_b128 v[228:231], v239 offset:30720
	s_waitcnt lgkmcnt(3)
	v_mfma_f32_32x32x16_f16 v[176:191], v[216:219], v[48:51], v[176:191]
	ds_read_b128 v[216:219], v240 offset:6144
	s_waitcnt lgkmcnt(3)
	v_mfma_f32_32x32x16_f16 v[192:207], v[220:223], v[48:51], v[192:207]
	ds_read_b128 v[220:223], v239 offset:7168
	s_waitcnt lgkmcnt(3)
	v_mfma_f32_32x32x16_f16 v[160:175], v[224:227], v[52:55], v[160:175]
	ds_read_b128 v[224:227], v239 offset:31744
	s_waitcnt lgkmcnt(3)
	v_mfma_f32_32x32x16_f16 v[176:191], v[228:231], v[52:55], v[176:191]
	ds_read_b128 v[228:231], v240 offset:7168
	s_waitcnt lgkmcnt(3)
	v_mfma_f32_32x32x16_f16 v[192:207], v[216:219], v[52:55], v[192:207]
	s_waitcnt lgkmcnt(2)
	v_mfma_f32_32x32x16_f16 v[160:175], v[220:223], v[56:59], v[160:175]
	s_waitcnt lgkmcnt(1)
	v_mfma_f32_32x32x16_f16 v[176:191], v[224:227], v[56:59], v[176:191]
	s_waitcnt lgkmcnt(0)
	v_mfma_f32_32x32x16_f16 v[192:207], v[228:231], v[56:59], v[192:207]
	s_waitcnt vmcnt(15)
	v_cvt_pk_f16_f32 v7, v6, v7
	v_cvt_pk_f16_f32 v6, v4, v5
	s_waitcnt vmcnt(14)
	v_cvt_pk_f16_f32 v5, v10, v11
	v_cvt_pk_f16_f32 v4, v8, v9
	ds_write2_b64 v157, v[6:7], v[4:5] offset1:72
	s_waitcnt vmcnt(13)
	v_cvt_pk_f16_f32 v5, v14, v15
	v_cvt_pk_f16_f32 v4, v12, v13
	s_waitcnt vmcnt(12)
	v_cvt_pk_f16_f32 v7, v82, v83
	v_cvt_pk_f16_f32 v6, v80, v81
	ds_write2_b64 v157, v[4:5], v[6:7] offset0:144 offset1:216
	s_waitcnt vmcnt(11)
	v_cvt_pk_f16_f32 v5, v86, v87
	v_cvt_pk_f16_f32 v4, v84, v85
	s_waitcnt vmcnt(10)
	v_cvt_pk_f16_f32 v7, v90, v91
	v_cvt_pk_f16_f32 v6, v88, v89
	ds_write2_b64 v1, v[4:5], v[6:7] offset0:32 offset1:104
	s_waitcnt vmcnt(9)
	v_cvt_pk_f16_f32 v5, v94, v95
	v_cvt_pk_f16_f32 v4, v92, v93
	s_waitcnt vmcnt(8)
	v_cvt_pk_f16_f32 v7, v98, v99
	v_cvt_pk_f16_f32 v6, v96, v97
	ds_write2_b64 v1, v[4:5], v[6:7] offset0:176 offset1:248
	ds_read_b128 v[60:63], v156 offset:49152
	ds_read_b128 v[64:67], v156 offset:49184
	ds_read_b128 v[68:71], v156 offset:49216
	ds_read_b128 v[72:75], v156 offset:49248
	global_load_dwordx4 v[4:7], v[140:141], off offset:1024 nt
	global_load_dwordx4 v[8:11], v[142:143], off offset:1024 nt
	global_load_dwordx4 v[12:15], v[144:145], off offset:1024 nt
	global_load_dwordx4 v[92:95], v[146:147], off offset:1024 nt
	global_load_dwordx4 v[96:99], v[148:149], off offset:1024 nt
	global_load_dwordx4 v[128:131], v[150:151], off offset:1024 nt
	global_load_dwordx4 v[132:135], v[152:153], off offset:1024 nt
	global_load_dwordx4 v[136:139], v[154:155], off offset:1024 nt
	ds_read_b128 v[216:219], v239 offset:8192
	ds_read_b128 v[220:223], v239 offset:32768
	ds_read_b128 v[224:227], v240 offset:8192
	ds_read_b128 v[228:231], v239 offset:9216
	s_waitcnt lgkmcnt(3)
	v_mfma_f32_32x32x16_f16 v[160:175], v[216:219], v[60:63], v[160:175]
	ds_read_b128 v[216:219], v239 offset:33792
	s_waitcnt lgkmcnt(3)
	v_mfma_f32_32x32x16_f16 v[176:191], v[220:223], v[60:63], v[176:191]
	ds_read_b128 v[220:223], v240 offset:9216
	s_waitcnt lgkmcnt(3)
	v_mfma_f32_32x32x16_f16 v[192:207], v[224:227], v[60:63], v[192:207]
	ds_read_b128 v[224:227], v239 offset:10240
	s_waitcnt lgkmcnt(3)
	v_mfma_f32_32x32x16_f16 v[160:175], v[228:231], v[64:67], v[160:175]
	ds_read_b128 v[228:231], v239 offset:34816
	s_waitcnt lgkmcnt(3)
	v_mfma_f32_32x32x16_f16 v[176:191], v[216:219], v[64:67], v[176:191]
	ds_read_b128 v[216:219], v240 offset:10240
	s_waitcnt lgkmcnt(3)
	v_mfma_f32_32x32x16_f16 v[192:207], v[220:223], v[64:67], v[192:207]
	ds_read_b128 v[220:223], v239 offset:11264
	s_waitcnt lgkmcnt(3)
	v_mfma_f32_32x32x16_f16 v[160:175], v[224:227], v[68:71], v[160:175]
	ds_read_b128 v[224:227], v239 offset:35840
	s_waitcnt lgkmcnt(3)
	v_mfma_f32_32x32x16_f16 v[176:191], v[228:231], v[68:71], v[176:191]
	ds_read_b128 v[228:231], v240 offset:11264
	s_waitcnt lgkmcnt(3)
	v_mfma_f32_32x32x16_f16 v[192:207], v[216:219], v[68:71], v[192:207]
	s_waitcnt lgkmcnt(2)
	v_mfma_f32_32x32x16_f16 v[160:175], v[220:223], v[72:75], v[160:175]
	s_waitcnt lgkmcnt(1)
	v_mfma_f32_32x32x16_f16 v[176:191], v[224:227], v[72:75], v[176:191]
	s_waitcnt lgkmcnt(0)
	v_mfma_f32_32x32x16_f16 v[192:207], v[228:231], v[72:75], v[192:207]
	s_waitcnt vmcnt(15)
	v_cvt_pk_f16_f32 v79, v78, v79
	v_cvt_pk_f16_f32 v78, v76, v77
	s_waitcnt vmcnt(14)
	v_cvt_pk_f16_f32 v77, v102, v103
	v_cvt_pk_f16_f32 v76, v100, v101
	ds_write2_b64 v157, v[78:79], v[76:77] offset1:72
	s_waitcnt vmcnt(13)
	v_cvt_pk_f16_f32 v77, v106, v107
	v_cvt_pk_f16_f32 v76, v104, v105
	s_waitcnt vmcnt(12)
	v_cvt_pk_f16_f32 v79, v110, v111
	v_cvt_pk_f16_f32 v78, v108, v109
	ds_write2_b64 v157, v[76:77], v[78:79] offset0:144 offset1:216
	s_waitcnt vmcnt(11)
	v_cvt_pk_f16_f32 v77, v114, v115
	v_cvt_pk_f16_f32 v76, v112, v113
	s_waitcnt vmcnt(10)
	v_cvt_pk_f16_f32 v79, v118, v119
	v_cvt_pk_f16_f32 v78, v116, v117
	ds_write2_b64 v1, v[76:77], v[78:79] offset0:32 offset1:104
	s_waitcnt vmcnt(9)
	v_cvt_pk_f16_f32 v77, v122, v123
	v_cvt_pk_f16_f32 v76, v120, v121
	s_waitcnt vmcnt(8)
	v_cvt_pk_f16_f32 v79, v126, v127
	v_cvt_pk_f16_f32 v78, v124, v125
	ds_write2_b64 v1, v[76:77], v[78:79] offset0:176 offset1:248
	ds_read_b128 v[76:79], v156 offset:49152
	ds_read_b128 v[80:83], v156 offset:49184
	ds_read_b128 v[84:87], v156 offset:49216
	ds_read_b128 v[88:91], v156 offset:49248
	global_load_dwordx4 v[108:111], v[140:141], off offset:1280 nt
	global_load_dwordx4 v[112:115], v[142:143], off offset:1280 nt
	global_load_dwordx4 v[116:119], v[144:145], off offset:1280 nt
	global_load_dwordx4 v[120:123], v[146:147], off offset:1280 nt
	global_load_dwordx4 v[124:127], v[148:149], off offset:1280 nt
	s_nop 0
	global_load_dwordx4 v[140:143], v[150:151], off offset:1280 nt
	global_load_dwordx4 v[144:147], v[152:153], off offset:1280 nt
	s_nop 0
	global_load_dwordx4 v[148:151], v[154:155], off offset:1280 nt
	ds_read_b128 v[216:219], v239 offset:12288
	ds_read_b128 v[220:223], v239 offset:36864
	ds_read_b128 v[224:227], v240 offset:12288
	ds_read_b128 v[228:231], v239 offset:13312
	s_waitcnt lgkmcnt(3)
	v_mfma_f32_32x32x16_f16 v[160:175], v[216:219], v[76:79], v[160:175]
	ds_read_b128 v[216:219], v239 offset:37888
	s_waitcnt lgkmcnt(3)
	v_mfma_f32_32x32x16_f16 v[176:191], v[220:223], v[76:79], v[176:191]
	ds_read_b128 v[220:223], v240 offset:13312
	s_waitcnt lgkmcnt(3)
	v_mfma_f32_32x32x16_f16 v[192:207], v[224:227], v[76:79], v[192:207]
	ds_read_b128 v[224:227], v239 offset:14336
	s_waitcnt lgkmcnt(3)
	v_mfma_f32_32x32x16_f16 v[160:175], v[228:231], v[80:83], v[160:175]
	ds_read_b128 v[228:231], v239 offset:38912
	s_waitcnt lgkmcnt(3)
	v_mfma_f32_32x32x16_f16 v[176:191], v[216:219], v[80:83], v[176:191]
	ds_read_b128 v[216:219], v240 offset:14336
	s_waitcnt lgkmcnt(3)
	v_mfma_f32_32x32x16_f16 v[192:207], v[220:223], v[80:83], v[192:207]
	ds_read_b128 v[220:223], v239 offset:15360
	s_waitcnt lgkmcnt(3)
	v_mfma_f32_32x32x16_f16 v[160:175], v[224:227], v[84:87], v[160:175]
	ds_read_b128 v[224:227], v239 offset:39936
	s_waitcnt lgkmcnt(3)
	v_mfma_f32_32x32x16_f16 v[176:191], v[228:231], v[84:87], v[176:191]
	ds_read_b128 v[228:231], v240 offset:15360
	s_waitcnt lgkmcnt(3)
	v_mfma_f32_32x32x16_f16 v[192:207], v[216:219], v[84:87], v[192:207]
	s_waitcnt lgkmcnt(2)
	v_mfma_f32_32x32x16_f16 v[160:175], v[220:223], v[88:91], v[160:175]
	s_waitcnt lgkmcnt(1)
	v_mfma_f32_32x32x16_f16 v[176:191], v[224:227], v[88:91], v[176:191]
	s_waitcnt lgkmcnt(0)
	v_mfma_f32_32x32x16_f16 v[192:207], v[228:231], v[88:91], v[192:207]
	s_waitcnt vmcnt(15)
	v_cvt_pk_f16_f32 v7, v6, v7
	v_cvt_pk_f16_f32 v6, v4, v5
	s_waitcnt vmcnt(14)
	v_cvt_pk_f16_f32 v5, v10, v11
	v_cvt_pk_f16_f32 v4, v8, v9
	ds_write2_b64 v157, v[6:7], v[4:5] offset1:72
	s_waitcnt vmcnt(13)
	v_cvt_pk_f16_f32 v5, v14, v15
	v_cvt_pk_f16_f32 v4, v12, v13
	s_waitcnt vmcnt(12)
	v_cvt_pk_f16_f32 v7, v94, v95
	v_cvt_pk_f16_f32 v6, v92, v93
	ds_write2_b64 v157, v[4:5], v[6:7] offset0:144 offset1:216
	s_waitcnt vmcnt(11)
	v_cvt_pk_f16_f32 v5, v98, v99
	v_cvt_pk_f16_f32 v4, v96, v97
	s_waitcnt vmcnt(10)
	v_cvt_pk_f16_f32 v7, v130, v131
	v_cvt_pk_f16_f32 v6, v128, v129
	ds_write2_b64 v1, v[4:5], v[6:7] offset0:32 offset1:104
	s_waitcnt vmcnt(9)
	v_cvt_pk_f16_f32 v5, v134, v135
	v_cvt_pk_f16_f32 v4, v132, v133
	s_waitcnt vmcnt(8)
	v_cvt_pk_f16_f32 v7, v138, v139
	v_cvt_pk_f16_f32 v6, v136, v137
	ds_write2_b64 v1, v[4:5], v[6:7] offset0:176 offset1:248
	ds_read_b128 v[92:95], v156 offset:49152
	ds_read_b128 v[96:99], v156 offset:49184
	ds_read_b128 v[100:103], v156 offset:49216
	ds_read_b128 v[104:107], v156 offset:49248
	ds_read_b128 v[216:219], v239 offset:16384
	ds_read_b128 v[220:223], v239 offset:40960
	ds_read_b128 v[224:227], v240 offset:16384
	ds_read_b128 v[228:231], v239 offset:17408
	s_waitcnt lgkmcnt(3)
	v_mfma_f32_32x32x16_f16 v[160:175], v[216:219], v[92:95], v[160:175]
	ds_read_b128 v[216:219], v239 offset:41984
	s_waitcnt lgkmcnt(3)
	v_mfma_f32_32x32x16_f16 v[176:191], v[220:223], v[92:95], v[176:191]
	ds_read_b128 v[220:223], v240 offset:17408
	s_waitcnt lgkmcnt(3)
	v_mfma_f32_32x32x16_f16 v[192:207], v[224:227], v[92:95], v[192:207]
	ds_read_b128 v[224:227], v239 offset:18432
	s_waitcnt lgkmcnt(3)
	v_mfma_f32_32x32x16_f16 v[160:175], v[228:231], v[96:99], v[160:175]
	ds_read_b128 v[228:231], v239 offset:43008
	s_waitcnt lgkmcnt(3)
	v_mfma_f32_32x32x16_f16 v[176:191], v[216:219], v[96:99], v[176:191]
	ds_read_b128 v[216:219], v240 offset:18432
	s_waitcnt lgkmcnt(3)
	v_mfma_f32_32x32x16_f16 v[192:207], v[220:223], v[96:99], v[192:207]
	ds_read_b128 v[220:223], v239 offset:19456
	s_waitcnt lgkmcnt(3)
	v_mfma_f32_32x32x16_f16 v[160:175], v[224:227], v[100:103], v[160:175]
	ds_read_b128 v[224:227], v239 offset:44032
	s_waitcnt lgkmcnt(3)
	v_mfma_f32_32x32x16_f16 v[176:191], v[228:231], v[100:103], v[176:191]
	ds_read_b128 v[228:231], v240 offset:19456
	s_waitcnt lgkmcnt(3)
	v_mfma_f32_32x32x16_f16 v[192:207], v[216:219], v[100:103], v[192:207]
	s_waitcnt lgkmcnt(2)
	v_mfma_f32_32x32x16_f16 v[160:175], v[220:223], v[104:107], v[160:175]
	s_waitcnt lgkmcnt(1)
	v_mfma_f32_32x32x16_f16 v[176:191], v[224:227], v[104:107], v[176:191]
	s_waitcnt lgkmcnt(0)
	v_mfma_f32_32x32x16_f16 v[192:207], v[228:231], v[104:107], v[192:207]
	s_waitcnt vmcnt(7)
	v_cvt_pk_f16_f32 v5, v110, v111
	v_cvt_pk_f16_f32 v4, v108, v109
	s_waitcnt vmcnt(6)
	v_cvt_pk_f16_f32 v7, v114, v115
	v_cvt_pk_f16_f32 v6, v112, v113
	ds_write2_b64 v157, v[4:5], v[6:7] offset1:72
	s_waitcnt vmcnt(5)
	v_cvt_pk_f16_f32 v5, v118, v119
	v_cvt_pk_f16_f32 v4, v116, v117
	s_waitcnt vmcnt(4)
	v_cvt_pk_f16_f32 v7, v122, v123
	v_cvt_pk_f16_f32 v6, v120, v121
	ds_write2_b64 v157, v[4:5], v[6:7] offset0:144 offset1:216
	s_waitcnt vmcnt(3)
	v_cvt_pk_f16_f32 v5, v126, v127
	v_cvt_pk_f16_f32 v4, v124, v125
	s_waitcnt vmcnt(2)
	v_cvt_pk_f16_f32 v7, v142, v143
	v_cvt_pk_f16_f32 v6, v140, v141
	ds_write2_b64 v1, v[4:5], v[6:7] offset0:32 offset1:104
	s_waitcnt vmcnt(1)
	v_cvt_pk_f16_f32 v5, v146, v147
	v_cvt_pk_f16_f32 v4, v144, v145
	s_waitcnt vmcnt(0)
	v_cvt_pk_f16_f32 v7, v150, v151
	v_cvt_pk_f16_f32 v6, v148, v149
	ds_write2_b64 v1, v[4:5], v[6:7] offset0:176 offset1:248
	ds_read_b128 v[108:111], v156 offset:49152
	ds_read_b128 v[112:115], v156 offset:49184
	ds_read_b128 v[116:119], v156 offset:49216
	ds_read_b128 v[120:123], v156 offset:49248
	ds_read_b128 v[216:219], v239 offset:20480
	ds_read_b128 v[220:223], v239 offset:45056
	ds_read_b128 v[224:227], v240 offset:20480
	ds_read_b128 v[228:231], v239 offset:21504
	s_waitcnt lgkmcnt(3)
	v_mfma_f32_32x32x16_f16 v[160:175], v[216:219], v[108:111], v[160:175]
	ds_read_b128 v[216:219], v239 offset:46080
	s_waitcnt lgkmcnt(3)
	v_mfma_f32_32x32x16_f16 v[176:191], v[220:223], v[108:111], v[176:191]
	ds_read_b128 v[220:223], v240 offset:21504
	s_waitcnt lgkmcnt(3)
	v_mfma_f32_32x32x16_f16 v[192:207], v[224:227], v[108:111], v[192:207]
	ds_read_b128 v[224:227], v239 offset:22528
	s_waitcnt lgkmcnt(3)
	v_mfma_f32_32x32x16_f16 v[160:175], v[228:231], v[112:115], v[160:175]
	ds_read_b128 v[228:231], v239 offset:47104
	s_waitcnt lgkmcnt(3)
	v_mfma_f32_32x32x16_f16 v[176:191], v[216:219], v[112:115], v[176:191]
	ds_read_b128 v[216:219], v240 offset:22528
	s_waitcnt lgkmcnt(3)
	v_mfma_f32_32x32x16_f16 v[192:207], v[220:223], v[112:115], v[192:207]
	ds_read_b128 v[220:223], v239 offset:23552
	s_waitcnt lgkmcnt(3)
	v_mfma_f32_32x32x16_f16 v[160:175], v[224:227], v[116:119], v[160:175]
	ds_read_b128 v[224:227], v239 offset:48128
	s_waitcnt lgkmcnt(3)
	v_mfma_f32_32x32x16_f16 v[176:191], v[228:231], v[116:119], v[176:191]
	ds_read_b128 v[228:231], v240 offset:23552
	s_waitcnt lgkmcnt(3)
	v_mfma_f32_32x32x16_f16 v[192:207], v[216:219], v[116:119], v[192:207]
	s_waitcnt lgkmcnt(2)
	v_mfma_f32_32x32x16_f16 v[160:175], v[220:223], v[120:123], v[160:175]
	s_waitcnt lgkmcnt(1)
	v_mfma_f32_32x32x16_f16 v[176:191], v[224:227], v[120:123], v[176:191]
	s_waitcnt lgkmcnt(0)
	v_mfma_f32_32x32x16_f16 v[192:207], v[228:231], v[120:123], v[192:207]
	s_add_i32 s20, s14, 0
	s_cmp_lt_u32 s20, 12
	s_cselect_b32 s26, s8, s10
	s_cselect_b32 s27, s9, s11
	s_cselect_b32 s21, 0, 12
	s_cmp_lt_u32 s20, 24
	s_cselect_b32 s26, s26, s0
	s_cselect_b32 s27, s27, s1
	s_cselect_b32 s21, s21, 24
	s_sub_i32 s20, s20, s21
	s_lshr_b32 s21, s20, 1
	s_and_b32 s20, s20, 1
	s_add_i32 s21, s21, s15
	s_lshl_b32 s21, s21, 15
	s_lshl_b32 s20, s20, 11
	s_add_i32 s21, s21, s20
	s_add_u32 s26, s26, s21
	s_addc_u32 s27, s27, 0
	s_mov_b64 s[28:29], s[26:27]
	s_add_i32 s20, s14, 1
	s_cmp_lt_u32 s20, 12
	s_cselect_b32 s26, s8, s10
	s_cselect_b32 s27, s9, s11
	s_cselect_b32 s21, 0, 12
	s_cmp_lt_u32 s20, 24
	s_cselect_b32 s26, s26, s0
	s_cselect_b32 s27, s27, s1
	s_cselect_b32 s21, s21, 24
	s_sub_i32 s20, s20, s21
	s_lshr_b32 s21, s20, 1
	s_and_b32 s20, s20, 1
	s_add_i32 s21, s21, s15
	s_lshl_b32 s21, s21, 15
	s_lshl_b32 s20, s20, 11
	s_add_i32 s21, s21, s20
	s_add_u32 s26, s26, s21
	s_addc_u32 s27, s27, 0
	s_mov_b64 s[30:31], s[26:27]
	s_add_i32 s20, s14, 2
	s_cmp_lt_u32 s20, 12
	s_cselect_b32 s26, s8, s10
	s_cselect_b32 s27, s9, s11
	s_cselect_b32 s21, 0, 12
	s_cmp_lt_u32 s20, 24
	s_cselect_b32 s26, s26, s0
	s_cselect_b32 s27, s27, s1
	s_cselect_b32 s21, s21, 24
	s_sub_i32 s20, s20, s21
	s_lshr_b32 s21, s20, 1
	s_and_b32 s20, s20, 1
	s_add_i32 s21, s21, s15
	s_lshl_b32 s21, s21, 15
	s_lshl_b32 s20, s20, 11
	s_add_i32 s21, s21, s20
	s_add_u32 s26, s26, s21
	s_addc_u32 s27, s27, 0
	v_cvt_pk_f16_f32 v244, v160, v161
	v_cvt_pk_f16_f32 v245, v162, v163
	v_cvt_pk_f16_f32 v246, v164, v165
	v_cvt_pk_f16_f32 v247, v166, v167
	v_cvt_pk_f16_f32 v248, v168, v169
	v_cvt_pk_f16_f32 v249, v170, v171
	v_cvt_pk_f16_f32 v250, v172, v173
	v_cvt_pk_f16_f32 v251, v174, v175
	global_store_dwordx4 v241, v[244:247], s[28:29]
	global_store_dwordx4 v241, v[248:251], s[28:29] offset:1024
	v_cvt_pk_f16_f32 v124, v176, v177
	v_cvt_pk_f16_f32 v125, v178, v179
	v_cvt_pk_f16_f32 v126, v180, v181
	v_cvt_pk_f16_f32 v127, v182, v183
	v_cvt_pk_f16_f32 v128, v184, v185
	v_cvt_pk_f16_f32 v129, v186, v187
	v_cvt_pk_f16_f32 v130, v188, v189
	v_cvt_pk_f16_f32 v131, v190, v191
	global_store_dwordx4 v241, v[124:127], s[30:31]
	global_store_dwordx4 v241, v[128:131], s[30:31] offset:1024
	v_cvt_pk_f16_f32 v132, v192, v193
	v_cvt_pk_f16_f32 v133, v194, v195
	v_cvt_pk_f16_f32 v134, v196, v197
	v_cvt_pk_f16_f32 v135, v198, v199
	v_cvt_pk_f16_f32 v136, v200, v201
	v_cvt_pk_f16_f32 v137, v202, v203
	v_cvt_pk_f16_f32 v138, v204, v205
	v_cvt_pk_f16_f32 v139, v206, v207
	global_store_dwordx4 v241, v[132:135], s[26:27]
	global_store_dwordx4 v241, v[136:139], s[26:27] offset:1024
	s_waitcnt lgkmcnt(0)
	s_barrier
	s_cmp_lt_u32 s2, 2
	s_cbranch_scc1 .Lqkv_p2S
.Lqkv_p2M:
	ds_read_b128 v[124:127], v240 offset:24576
	ds_read_b128 v[128:131], v240 offset:25600
	ds_read_b128 v[132:135], v240 offset:26624
	ds_read_b128 v[136:139], v240 offset:27648
	ds_read_b128 v[140:143], v240 offset:28672
	ds_read_b128 v[144:147], v240 offset:29696
	ds_read_b128 v[148:151], v240 offset:30720
	ds_read_b128 v[152:155], v240 offset:31744
	ds_read_b128 v[156:159], v240 offset:32768
	ds_read_b128 v[160:163], v240 offset:33792
	ds_read_b128 v[164:167], v240 offset:34816
	ds_read_b128 v[168:171], v240 offset:35840
	ds_read_b128 v[172:175], v240 offset:36864
	ds_read_b128 v[176:179], v240 offset:37888
	ds_read_b128 v[180:183], v240 offset:38912
	ds_read_b128 v[184:187], v240 offset:39936
	ds_read_b128 v[188:191], v240 offset:40960
	ds_read_b128 v[192:195], v240 offset:41984
	ds_read_b128 v[196:199], v240 offset:43008
	ds_read_b128 v[200:203], v240 offset:44032
	ds_read_b128 v[204:207], v240 offset:45056
	ds_read_b128 v[208:211], v240 offset:46080
	ds_read_b128 v[212:215], v240 offset:47104
	ds_read_b128 v[216:219], v240 offset:48128
	s_add_u32 s24, s22, 122880
	s_addc_u32 s25, s23, 0
	s_waitcnt lgkmcnt(14)
	v_mfma_f32_32x32x16_f16 v[0:15], v[124:127], v[28:31], 0
	ds_read_b128 v[124:127], v242 offset:0
	global_load_dwordx4 v[16:19], v236, s[24:25]
	global_load_dwordx4 v[20:23], v237, s[24:25]
	global_load_dwordx4 v[24:27], v238, s[24:25]
	s_waitcnt lgkmcnt(14)
	v_mfma_f32_32x32x16_f16 v[0:15], v[128:131], v[32:35], v[0:15]
	ds_read_b128 v[128:131], v242 offset:1024
	s_waitcnt lgkmcnt(14)
	v_mfma_f32_32x32x16_f16 v[0:15], v[132:135], v[36:39], v[0:15]
	ds_read_b128 v[132:135], v242 offset:2048
	s_waitcnt lgkmcnt(14)
	v_mfma_f32_32x32x16_f16 v[0:15], v[136:139], v[40:43], v[0:15]
	ds_read_b128 v[136:139], v242 offset:3072
	s_waitcnt lgkmcnt(14)
	v_mfma_f32_32x32x16_f16 v[0:15], v[140:143], v[44:47], v[0:15]
	ds_read_b128 v[140:143], v242 offset:4096
	s_waitcnt lgkmcnt(14)
	v_mfma_f32_32x32x16_f16 v[0:15], v[144:147], v[48:51], v[0:15]
	ds_read_b128 v[144:147], v242 offset:5120
	s_waitcnt lgkmcnt(14)
	v_mfma_f32_32x32x16_f16 v[0:15], v[148:151], v[52:55], v[0:15]
	ds_read_b128 v[148:151], v242 offset:6144
	s_waitcnt lgkmcnt(14)
	v_mfma_f32_32x32x16_f16 v[0:15], v[152:155], v[56:59], v[0:15]
	ds_read_b128 v[152:155], v242 offset:7168
	s_waitcnt lgkmcnt(14)
	v_mfma_f32_32x32x16_f16 v[0:15], v[156:159], v[60:63], v[0:15]
	ds_read_b128 v[156:159], v242 offset:8192
	s_waitcnt lgkmcnt(14)
	v_mfma_f32_32x32x16_f16 v[0:15], v[160:163], v[64:67], v[0:15]
	ds_read_b128 v[160:163], v242 offset:9216
	s_waitcnt lgkmcnt(14)
	v_mfma_f32_32x32x16_f16 v[0:15], v[164:167], v[68:71], v[0:15]
	ds_read_b128 v[164:167], v242 offset:10240
	s_waitcnt lgkmcnt(14)
	v_mfma_f32_32x32x16_f16 v[0:15], v[168:171], v[72:75], v[0:15]
	ds_read_b128 v[168:171], v242 offset:11264
	s_waitcnt lgkmcnt(14)
	v_mfma_f32_32x32x16_f16 v[0:15], v[172:175], v[76:79], v[0:15]
	ds_read_b128 v[172:175], v242 offset:12288
	s_waitcnt lgkmcnt(14)
	v_mfma_f32_32x32x16_f16 v[0:15], v[176:179], v[80:83], v[0:15]
	ds_read_b128 v[176:179], v242 offset:13312
	s_waitcnt lgkmcnt(14)
	v_mfma_f32_32x32x16_f16 v[0:15], v[180:183], v[84:87], v[0:15]
	ds_read_b128 v[180:183], v242 offset:14336
	s_waitcnt lgkmcnt(14)
	v_mfma_f32_32x32x16_f16 v[0:15], v[184:187], v[88:91], v[0:15]
	ds_read_b128 v[184:187], v242 offset:15360
	s_waitcnt lgkmcnt(14)
	v_mfma_f32_32x32x16_f16 v[0:15], v[188:191], v[92:95], v[0:15]
	ds_read_b128 v[188:191], v242 offset:16384
	s_waitcnt lgkmcnt(14)
	v_mfma_f32_32x32x16_f16 v[0:15], v[192:195], v[96:99], v[0:15]
	ds_read_b128 v[192:195], v242 offset:17408
	s_waitcnt lgkmcnt(14)
	v_mfma_f32_32x32x16_f16 v[0:15], v[196:199], v[100:103], v[0:15]
	ds_read_b128 v[196:199], v242 offset:18432
	s_waitcnt vmcnt(0)
	ds_write_b128 v252, v[16:19] offset:49152
	ds_write_b128 v253, v[20:23] offset:49152
	ds_write_b128 v254, v[24:27] offset:49152
	s_waitcnt lgkmcnt(14)
	v_mfma_f32_32x32x16_f16 v[0:15], v[200:203], v[104:107], v[0:15]
	ds_read_b128 v[200:203], v242 offset:19456
	s_waitcnt lgkmcnt(14)
	v_mfma_f32_32x32x16_f16 v[0:15], v[204:207], v[108:111], v[0:15]
	ds_read_b128 v[204:207], v242 offset:20480
	s_waitcnt lgkmcnt(14)
	v_mfma_f32_32x32x16_f16 v[0:15], v[208:211], v[112:115], v[0:15]
	ds_read_b128 v[208:211], v242 offset:21504
	s_waitcnt lgkmcnt(14)
	v_mfma_f32_32x32x16_f16 v[0:15], v[212:215], v[116:119], v[0:15]
	ds_read_b128 v[212:215], v242 offset:22528
	s_waitcnt lgkmcnt(14)
	v_mfma_f32_32x32x16_f16 v[0:15], v[216:219], v[120:123], v[0:15]
	ds_read_b128 v[216:219], v242 offset:23552
	s_waitcnt lgkmcnt(5)
	s_barrier
	s_add_u32 s24, s22, 147456
	s_addc_u32 s25, s23, 0
	s_waitcnt lgkmcnt(14)
	v_mfma_f32_32x32x16_f16 v[220:235], v[124:127], v[28:31], 0
	ds_read_b128 v[124:127], v242 offset:24576
	global_load_dwordx4 v[16:19], v236, s[24:25]
	global_load_dwordx4 v[20:23], v237, s[24:25]
	global_load_dwordx4 v[24:27], v238, s[24:25]
	s_waitcnt lgkmcnt(14)
	v_mfma_f32_32x32x16_f16 v[220:235], v[128:131], v[32:35], v[220:235]
	ds_read_b128 v[128:131], v242 offset:25600
	s_add_i32 s20, s14, 3
	s_cmp_lt_u32 s20, 12
	s_cselect_b32 s26, s8, s10
	s_cselect_b32 s27, s9, s11
	s_waitcnt lgkmcnt(14)
	v_mfma_f32_32x32x16_f16 v[220:235], v[132:135], v[36:39], v[220:235]
	ds_read_b128 v[132:135], v242 offset:26624
	s_cselect_b32 s21, 0, 12
	s_cmp_lt_u32 s20, 24
	s_cselect_b32 s26, s26, s0
	s_cselect_b32 s27, s27, s1
	s_waitcnt lgkmcnt(14)
	v_mfma_f32_32x32x16_f16 v[220:235], v[136:139], v[40:43], v[220:235]
	ds_read_b128 v[136:139], v242 offset:27648
	s_cselect_b32 s21, s21, 24
	s_sub_i32 s20, s20, s21
	s_lshr_b32 s21, s20, 1
	s_and_b32 s20, s20, 1
	s_waitcnt lgkmcnt(14)
	v_mfma_f32_32x32x16_f16 v[220:235], v[140:143], v[44:47], v[220:235]
	ds_read_b128 v[140:143], v242 offset:28672
	s_add_i32 s21, s21, s15
	s_lshl_b32 s21, s21, 15
	s_lshl_b32 s20, s20, 11
	s_add_i32 s21, s21, s20
	s_waitcnt lgkmcnt(14)
	v_mfma_f32_32x32x16_f16 v[220:235], v[144:147], v[48:51], v[220:235]
	ds_read_b128 v[144:147], v242 offset:29696
	s_add_u32 s26, s26, s21
	s_addc_u32 s27, s27, 0
	s_waitcnt lgkmcnt(14)
	v_mfma_f32_32x32x16_f16 v[220:235], v[148:151], v[52:55], v[220:235]
	ds_read_b128 v[148:151], v242 offset:30720
	v_cvt_pk_f16_f32 v244, v0, v1
	v_cvt_pk_f16_f32 v245, v2, v3
	s_waitcnt lgkmcnt(14)
	v_mfma_f32_32x32x16_f16 v[220:235], v[152:155], v[56:59], v[220:235]
	ds_read_b128 v[152:155], v242 offset:31744
	v_cvt_pk_f16_f32 v246, v4, v5
	v_cvt_pk_f16_f32 v247, v6, v7
	s_waitcnt lgkmcnt(14)
	v_mfma_f32_32x32x16_f16 v[220:235], v[156:159], v[60:63], v[220:235]
	ds_read_b128 v[156:159], v242 offset:32768
	v_cvt_pk_f16_f32 v248, v8, v9
	v_cvt_pk_f16_f32 v249, v10, v11
	s_waitcnt lgkmcnt(14)
	v_mfma_f32_32x32x16_f16 v[220:235], v[160:163], v[64:67], v[220:235]
	ds_read_b128 v[160:163], v242 offset:33792
	v_cvt_pk_f16_f32 v250, v12, v13
	v_cvt_pk_f16_f32 v251, v14, v15
	s_waitcnt lgkmcnt(14)
	v_mfma_f32_32x32x16_f16 v[220:235], v[164:167], v[68:71], v[220:235]
	ds_read_b128 v[164:167], v242 offset:34816
	global_store_dwordx4 v241, v[244:247], s[26:27]
	s_waitcnt lgkmcnt(14)
	v_mfma_f32_32x32x16_f16 v[220:235], v[168:171], v[72:75], v[220:235]
	ds_read_b128 v[168:171], v242 offset:35840
	global_store_dwordx4 v241, v[248:251], s[26:27] offset:1024
	s_waitcnt lgkmcnt(14)
	v_mfma_f32_32x32x16_f16 v[220:235], v[172:175], v[76:79], v[220:235]
	ds_read_b128 v[172:175], v242 offset:36864
	s_waitcnt lgkmcnt(14)
	v_mfma_f32_32x32x16_f16 v[220:235], v[176:179], v[80:83], v[220:235]
	ds_read_b128 v[176:179], v242 offset:37888
	s_waitcnt lgkmcnt(14)
	v_mfma_f32_32x32x16_f16 v[220:235], v[180:183], v[84:87], v[220:235]
	ds_read_b128 v[180:183], v242 offset:38912
	s_waitcnt lgkmcnt(14)
	v_mfma_f32_32x32x16_f16 v[220:235], v[184:187], v[88:91], v[220:235]
	ds_read_b128 v[184:187], v242 offset:39936
	s_waitcnt lgkmcnt(14)
	v_mfma_f32_32x32x16_f16 v[220:235], v[188:191], v[92:95], v[220:235]
	ds_read_b128 v[188:191], v242 offset:40960
	s_waitcnt lgkmcnt(14)
	v_mfma_f32_32x32x16_f16 v[220:235], v[192:195], v[96:99], v[220:235]
	ds_read_b128 v[192:195], v242 offset:41984
	s_waitcnt lgkmcnt(14)
	v_mfma_f32_32x32x16_f16 v[220:235], v[196:199], v[100:103], v[220:235]
	ds_read_b128 v[196:199], v242 offset:43008
	s_waitcnt vmcnt(2)
	ds_write_b128 v236, v[16:19] offset:0
	ds_write_b128 v237, v[20:23] offset:0
	ds_write_b128 v238, v[24:27] offset:0
	s_waitcnt lgkmcnt(14)
	v_mfma_f32_32x32x16_f16 v[220:235], v[200:203], v[104:107], v[220:235]
	ds_read_b128 v[200:203], v242 offset:44032
	s_waitcnt lgkmcnt(14)
	v_mfma_f32_32x32x16_f16 v[220:235], v[204:207], v[108:111], v[220:235]
	ds_read_b128 v[204:207], v242 offset:45056
	s_waitcnt lgkmcnt(14)
	v_mfma_f32_32x32x16_f16 v[220:235], v[208:211], v[112:115], v[220:235]
	ds_read_b128 v[208:211], v242 offset:46080
	s_waitcnt lgkmcnt(14)
	v_mfma_f32_32x32x16_f16 v[220:235], v[212:215], v[116:119], v[220:235]
	ds_read_b128 v[212:215], v242 offset:47104
	s_waitcnt lgkmcnt(14)
	v_mfma_f32_32x32x16_f16 v[220:235], v[216:219], v[120:123], v[220:235]
	ds_read_b128 v[216:219], v242 offset:48128
	s_waitcnt lgkmcnt(5)
	s_barrier
	s_add_u32 s24, s22, 172032
	s_addc_u32 s25, s23, 0
	s_waitcnt lgkmcnt(14)
	v_mfma_f32_32x32x16_f16 v[0:15], v[124:127], v[28:31], 0
	ds_read_b128 v[124:127], v239 offset:0
	global_load_dwordx4 v[16:19], v236, s[24:25]
	global_load_dwordx4 v[20:23], v237, s[24:25]
	global_load_dwordx4 v[24:27], v238, s[24:25]
	s_waitcnt lgkmcnt(14)
	v_mfma_f32_32x32x16_f16 v[0:15], v[128:131], v[32:35], v[0:15]
	ds_read_b128 v[128:131], v239 offset:1024
	s_add_i32 s20, s14, 4
	s_cmp_lt_u32 s20, 12
	s_cselect_b32 s26, s8, s10
	s_cselect_b32 s27, s9, s11
	s_waitcnt lgkmcnt(14)
	v_mfma_f32_32x32x16_f16 v[0:15], v[132:135], v[36:39], v[0:15]
	ds_read_b128 v[132:135], v239 offset:2048
	s_cselect_b32 s21, 0, 12
	s_cmp_lt_u32 s20, 24
	s_cselect_b32 s26, s26, s0
	s_cselect_b32 s27, s27, s1
	s_waitcnt lgkmcnt(14)
	v_mfma_f32_32x32x16_f16 v[0:15], v[136:139], v[40:43], v[0:15]
	ds_read_b128 v[136:139], v239 offset:3072
	s_cselect_b32 s21, s21, 24
	s_sub_i32 s20, s20, s21
	s_lshr_b32 s21, s20, 1
	s_and_b32 s20, s20, 1
	s_waitcnt lgkmcnt(14)
	v_mfma_f32_32x32x16_f16 v[0:15], v[140:143], v[44:47], v[0:15]
	ds_read_b128 v[140:143], v239 offset:4096
	s_add_i32 s21, s21, s15
	s_lshl_b32 s21, s21, 15
	s_lshl_b32 s20, s20, 11
	s_add_i32 s21, s21, s20
	s_waitcnt lgkmcnt(14)
	v_mfma_f32_32x32x16_f16 v[0:15], v[144:147], v[48:51], v[0:15]
	ds_read_b128 v[144:147], v239 offset:5120
	s_add_u32 s26, s26, s21
	s_addc_u32 s27, s27, 0
	s_waitcnt lgkmcnt(14)
	v_mfma_f32_32x32x16_f16 v[0:15], v[148:151], v[52:55], v[0:15]
	ds_read_b128 v[148:151], v239 offset:6144
	v_cvt_pk_f16_f32 v244, v220, v221
	v_cvt_pk_f16_f32 v245, v222, v223
	s_waitcnt lgkmcnt(14)
	v_mfma_f32_32x32x16_f16 v[0:15], v[152:155], v[56:59], v[0:15]
	ds_read_b128 v[152:155], v239 offset:7168
	v_cvt_pk_f16_f32 v246, v224, v225
	v_cvt_pk_f16_f32 v247, v226, v227
	s_waitcnt lgkmcnt(14)
	v_mfma_f32_32x32x16_f16 v[0:15], v[156:159], v[60:63], v[0:15]
	ds_read_b128 v[156:159], v239 offset:8192
	v_cvt_pk_f16_f32 v248, v228, v229
	v_cvt_pk_f16_f32 v249, v230, v231
	s_waitcnt lgkmcnt(14)
	v_mfma_f32_32x32x16_f16 v[0:15], v[160:163], v[64:67], v[0:15]
	ds_read_b128 v[160:163], v239 offset:9216
	v_cvt_pk_f16_f32 v250, v232, v233
	v_cvt_pk_f16_f32 v251, v234, v235
	s_waitcnt lgkmcnt(14)
	v_mfma_f32_32x32x16_f16 v[0:15], v[164:167], v[68:71], v[0:15]
	ds_read_b128 v[164:167], v239 offset:10240
	global_store_dwordx4 v241, v[244:247], s[26:27]
	s_waitcnt lgkmcnt(14)
	v_mfma_f32_32x32x16_f16 v[0:15], v[168:171], v[72:75], v[0:15]
	ds_read_b128 v[168:171], v239 offset:11264
	global_store_dwordx4 v241, v[248:251], s[26:27] offset:1024
	s_waitcnt lgkmcnt(14)
	v_mfma_f32_32x32x16_f16 v[0:15], v[172:175], v[76:79], v[0:15]
	ds_read_b128 v[172:175], v239 offset:12288
	s_waitcnt lgkmcnt(14)
	v_mfma_f32_32x32x16_f16 v[0:15], v[176:179], v[80:83], v[0:15]
	ds_read_b128 v[176:179], v239 offset:13312
	s_waitcnt lgkmcnt(14)
	v_mfma_f32_32x32x16_f16 v[0:15], v[180:183], v[84:87], v[0:15]
	ds_read_b128 v[180:183], v239 offset:14336
	s_waitcnt lgkmcnt(14)
	v_mfma_f32_32x32x16_f16 v[0:15], v[184:187], v[88:91], v[0:15]
	ds_read_b128 v[184:187], v239 offset:15360
	s_waitcnt lgkmcnt(14)
	v_mfma_f32_32x32x16_f16 v[0:15], v[188:191], v[92:95], v[0:15]
	ds_read_b128 v[188:191], v239 offset:16384
	s_waitcnt lgkmcnt(14)
	v_mfma_f32_32x32x16_f16 v[0:15], v[192:195], v[96:99], v[0:15]
	ds_read_b128 v[192:195], v239 offset:17408
	s_waitcnt lgkmcnt(14)
	v_mfma_f32_32x32x16_f16 v[0:15], v[196:199], v[100:103], v[0:15]
	ds_read_b128 v[196:199], v239 offset:18432
	s_waitcnt vmcnt(2)
	ds_write_b128 v236, v[16:19] offset:24576
	ds_write_b128 v237, v[20:23] offset:24576
	ds_write_b128 v238, v[24:27] offset:24576
	s_waitcnt lgkmcnt(14)
	v_mfma_f32_32x32x16_f16 v[0:15], v[200:203], v[104:107], v[0:15]
	ds_read_b128 v[200:203], v239 offset:19456
	s_waitcnt lgkmcnt(14)
	v_mfma_f32_32x32x16_f16 v[0:15], v[204:207], v[108:111], v[0:15]
	ds_read_b128 v[204:207], v239 offset:20480
	s_waitcnt lgkmcnt(14)
	v_mfma_f32_32x32x16_f16 v[0:15], v[208:211], v[112:115], v[0:15]
	ds_read_b128 v[208:211], v239 offset:21504
	s_waitcnt lgkmcnt(14)
	v_mfma_f32_32x32x16_f16 v[0:15], v[212:215], v[116:119], v[0:15]
	ds_read_b128 v[212:215], v239 offset:22528
	s_waitcnt lgkmcnt(14)
	v_mfma_f32_32x32x16_f16 v[0:15], v[216:219], v[120:123], v[0:15]
	ds_read_b128 v[216:219], v239 offset:23552
	s_waitcnt lgkmcnt(5)
	s_barrier
	s_add_u32 s24, s22, 196608
	s_addc_u32 s25, s23, 0
	s_waitcnt lgkmcnt(14)
	v_mfma_f32_32x32x16_f16 v[220:235], v[28:31], v[124:127], 0
	ds_read_b128 v[124:127], v239 offset:24576
	global_load_dwordx4 v[16:19], v236, s[24:25]
	global_load_dwordx4 v[20:23], v237, s[24:25]
	global_load_dwordx4 v[24:27], v238, s[24:25]
	s_waitcnt lgkmcnt(14)
	v_mfma_f32_32x32x16_f16 v[220:235], v[32:35], v[128:131], v[220:235]
	ds_read_b128 v[128:131], v239 offset:25600
	s_add_i32 s20, s14, 5
	s_cmp_lt_u32 s20, 12
	s_cselect_b32 s26, s8, s10
	s_cselect_b32 s27, s9, s11
	s_waitcnt lgkmcnt(14)
	v_mfma_f32_32x32x16_f16 v[220:235], v[36:39], v[132:135], v[220:235]
	ds_read_b128 v[132:135], v239 offset:26624
	s_cselect_b32 s21, 0, 12
	s_cmp_lt_u32 s20, 24
	s_cselect_b32 s26, s26, s0
	s_cselect_b32 s27, s27, s1
	s_waitcnt lgkmcnt(14)
	v_mfma_f32_32x32x16_f16 v[220:235], v[40:43], v[136:139], v[220:235]
	ds_read_b128 v[136:139], v239 offset:27648
	s_cselect_b32 s21, s21, 24
	s_sub_i32 s20, s20, s21
	s_lshr_b32 s21, s20, 1
	s_and_b32 s20, s20, 1
	s_waitcnt lgkmcnt(14)
	v_mfma_f32_32x32x16_f16 v[220:235], v[44:47], v[140:143], v[220:235]
	ds_read_b128 v[140:143], v239 offset:28672
	s_add_i32 s21, s21, s15
	s_lshl_b32 s21, s21, 15
	s_lshl_b32 s20, s20, 11
	s_add_i32 s21, s21, s20
	s_waitcnt lgkmcnt(14)
	v_mfma_f32_32x32x16_f16 v[220:235], v[48:51], v[144:147], v[220:235]
	ds_read_b128 v[144:147], v239 offset:29696
	s_add_u32 s26, s26, s21
	s_addc_u32 s27, s27, 0
	s_waitcnt lgkmcnt(14)
	v_mfma_f32_32x32x16_f16 v[220:235], v[52:55], v[148:151], v[220:235]
	ds_read_b128 v[148:151], v239 offset:30720
	v_cvt_pk_f16_f32 v244, v0, v1
	v_cvt_pk_f16_f32 v245, v2, v3
	s_waitcnt lgkmcnt(14)
	v_mfma_f32_32x32x16_f16 v[220:235], v[56:59], v[152:155], v[220:235]
	ds_read_b128 v[152:155], v239 offset:31744
	v_cvt_pk_f16_f32 v246, v4, v5
	v_cvt_pk_f16_f32 v247, v6, v7
	s_waitcnt lgkmcnt(14)
	v_mfma_f32_32x32x16_f16 v[220:235], v[60:63], v[156:159], v[220:235]
	ds_read_b128 v[156:159], v239 offset:32768
	v_cvt_pk_f16_f32 v248, v8, v9
	v_cvt_pk_f16_f32 v249, v10, v11
	s_waitcnt lgkmcnt(14)
	v_mfma_f32_32x32x16_f16 v[220:235], v[64:67], v[160:163], v[220:235]
	ds_read_b128 v[160:163], v239 offset:33792
	v_cvt_pk_f16_f32 v250, v12, v13
	v_cvt_pk_f16_f32 v251, v14, v15
	s_waitcnt lgkmcnt(14)
	v_mfma_f32_32x32x16_f16 v[220:235], v[68:71], v[164:167], v[220:235]
	ds_read_b128 v[164:167], v239 offset:34816
	global_store_dwordx4 v241, v[244:247], s[26:27]
	s_waitcnt lgkmcnt(14)
	v_mfma_f32_32x32x16_f16 v[220:235], v[72:75], v[168:171], v[220:235]
	ds_read_b128 v[168:171], v239 offset:35840
	global_store_dwordx4 v241, v[248:251], s[26:27] offset:1024
	s_waitcnt lgkmcnt(14)
	v_mfma_f32_32x32x16_f16 v[220:235], v[76:79], v[172:175], v[220:235]
	ds_read_b128 v[172:175], v239 offset:36864
	s_waitcnt lgkmcnt(14)
	v_mfma_f32_32x32x16_f16 v[220:235], v[80:83], v[176:179], v[220:235]
	ds_read_b128 v[176:179], v239 offset:37888
	s_waitcnt lgkmcnt(14)
	v_mfma_f32_32x32x16_f16 v[220:235], v[84:87], v[180:183], v[220:235]
	ds_read_b128 v[180:183], v239 offset:38912
	s_waitcnt lgkmcnt(14)
	v_mfma_f32_32x32x16_f16 v[220:235], v[88:91], v[184:187], v[220:235]
	ds_read_b128 v[184:187], v239 offset:39936
	s_waitcnt lgkmcnt(14)
	v_mfma_f32_32x32x16_f16 v[220:235], v[92:95], v[188:191], v[220:235]
	ds_read_b128 v[188:191], v239 offset:40960
	s_waitcnt lgkmcnt(14)
	v_mfma_f32_32x32x16_f16 v[220:235], v[96:99], v[192:195], v[220:235]
	ds_read_b128 v[192:195], v239 offset:41984
	s_waitcnt lgkmcnt(14)
	v_mfma_f32_32x32x16_f16 v[220:235], v[100:103], v[196:199], v[220:235]
	ds_read_b128 v[196:199], v239 offset:43008
	s_waitcnt vmcnt(2)
	ds_write_b128 v236, v[16:19] offset:49152
	ds_write_b128 v237, v[20:23] offset:49152
	ds_write_b128 v238, v[24:27] offset:49152
	s_waitcnt lgkmcnt(14)
	v_mfma_f32_32x32x16_f16 v[220:235], v[104:107], v[200:203], v[220:235]
	ds_read_b128 v[200:203], v239 offset:44032
	s_waitcnt lgkmcnt(14)
	v_mfma_f32_32x32x16_f16 v[220:235], v[108:111], v[204:207], v[220:235]
	ds_read_b128 v[204:207], v239 offset:45056
	s_waitcnt lgkmcnt(14)
	v_mfma_f32_32x32x16_f16 v[220:235], v[112:115], v[208:211], v[220:235]
	ds_read_b128 v[208:211], v239 offset:46080
	s_waitcnt lgkmcnt(14)
	v_mfma_f32_32x32x16_f16 v[220:235], v[116:119], v[212:215], v[220:235]
	ds_read_b128 v[212:215], v239 offset:47104
	s_waitcnt lgkmcnt(14)
	v_mfma_f32_32x32x16_f16 v[220:235], v[120:123], v[216:219], v[220:235]
	ds_read_b128 v[216:219], v239 offset:48128
	s_waitcnt lgkmcnt(5)
	s_barrier
	s_waitcnt lgkmcnt(14)
	v_mfma_f32_32x32x16_f16 v[0:15], v[28:31], v[124:127], 0
	ds_read_b128 v[124:127], v240 offset:0
	s_waitcnt lgkmcnt(14)
	v_mfma_f32_32x32x16_f16 v[0:15], v[32:35], v[128:131], v[0:15]
	ds_read_b128 v[128:131], v240 offset:1024
	s_add_i32 s20, s14, 6
	s_cmp_lt_u32 s20, 12
	s_cselect_b32 s26, s8, s10
	s_cselect_b32 s27, s9, s11
	s_waitcnt lgkmcnt(14)
	v_mfma_f32_32x32x16_f16 v[0:15], v[36:39], v[132:135], v[0:15]
	ds_read_b128 v[132:135], v240 offset:2048
	s_cselect_b32 s21, 0, 12
	s_cmp_lt_u32 s20, 24
	s_cselect_b32 s26, s26, s0
	s_cselect_b32 s27, s27, s1
	s_waitcnt lgkmcnt(14)
	v_mfma_f32_32x32x16_f16 v[0:15], v[40:43], v[136:139], v[0:15]
	ds_read_b128 v[136:139], v240 offset:3072
	s_cselect_b32 s21, s21, 24
	s_sub_i32 s20, s20, s21
	s_lshr_b32 s21, s20, 1
	s_and_b32 s20, s20, 1
	s_waitcnt lgkmcnt(14)
	v_mfma_f32_32x32x16_f16 v[0:15], v[44:47], v[140:143], v[0:15]
	ds_read_b128 v[140:143], v240 offset:4096
	s_add_i32 s21, s21, s15
	s_lshl_b32 s21, s21, 15
	s_lshl_b32 s20, s20, 11
	s_add_i32 s21, s21, s20
	s_waitcnt lgkmcnt(14)
	v_mfma_f32_32x32x16_f16 v[0:15], v[48:51], v[144:147], v[0:15]
	ds_read_b128 v[144:147], v240 offset:5120
	s_add_u32 s26, s26, s21
	s_addc_u32 s27, s27, 0
	s_waitcnt lgkmcnt(14)
	v_mfma_f32_32x32x16_f16 v[0:15], v[52:55], v[148:151], v[0:15]
	ds_read_b128 v[148:151], v240 offset:6144
	v_cvt_pk_f16_f32 v244, v220, v221
	v_cvt_pk_f16_f32 v245, v222, v223
	s_waitcnt lgkmcnt(14)
	v_mfma_f32_32x32x16_f16 v[0:15], v[56:59], v[152:155], v[0:15]
	ds_read_b128 v[152:155], v240 offset:7168
	v_cvt_pk_f16_f32 v246, v224, v225
	v_cvt_pk_f16_f32 v247, v226, v227
	s_waitcnt lgkmcnt(14)
	v_mfma_f32_32x32x16_f16 v[0:15], v[60:63], v[156:159], v[0:15]
	ds_read_b128 v[156:159], v240 offset:8192
	v_cvt_pk_f16_f32 v248, v228, v229
	v_cvt_pk_f16_f32 v249, v230, v231
	s_waitcnt lgkmcnt(14)
	v_mfma_f32_32x32x16_f16 v[0:15], v[64:67], v[160:163], v[0:15]
	ds_read_b128 v[160:163], v240 offset:9216
	v_cvt_pk_f16_f32 v250, v232, v233
	v_cvt_pk_f16_f32 v251, v234, v235
	s_waitcnt lgkmcnt(14)
	v_mfma_f32_32x32x16_f16 v[0:15], v[68:71], v[164:167], v[0:15]
	ds_read_b128 v[164:167], v240 offset:10240
	global_store_dwordx4 v241, v[244:247], s[26:27]
	s_waitcnt lgkmcnt(14)
	v_mfma_f32_32x32x16_f16 v[0:15], v[72:75], v[168:171], v[0:15]
	ds_read_b128 v[168:171], v240 offset:11264
	global_store_dwordx4 v241, v[248:251], s[26:27] offset:1024
	s_waitcnt lgkmcnt(14)
	v_mfma_f32_32x32x16_f16 v[0:15], v[76:79], v[172:175], v[0:15]
	ds_read_b128 v[172:175], v240 offset:12288
	s_waitcnt lgkmcnt(14)
	v_mfma_f32_32x32x16_f16 v[0:15], v[80:83], v[176:179], v[0:15]
	ds_read_b128 v[176:179], v240 offset:13312
	s_waitcnt lgkmcnt(14)
	v_mfma_f32_32x32x16_f16 v[0:15], v[84:87], v[180:183], v[0:15]
	ds_read_b128 v[180:183], v240 offset:14336
	s_waitcnt lgkmcnt(14)
	v_mfma_f32_32x32x16_f16 v[0:15], v[88:91], v[184:187], v[0:15]
	ds_read_b128 v[184:187], v240 offset:15360
	s_waitcnt lgkmcnt(14)
	v_mfma_f32_32x32x16_f16 v[0:15], v[92:95], v[188:191], v[0:15]
	ds_read_b128 v[188:191], v240 offset:16384
	s_waitcnt lgkmcnt(14)
	v_mfma_f32_32x32x16_f16 v[0:15], v[96:99], v[192:195], v[0:15]
	ds_read_b128 v[192:195], v240 offset:17408
	s_waitcnt lgkmcnt(14)
	v_mfma_f32_32x32x16_f16 v[0:15], v[100:103], v[196:199], v[0:15]
	ds_read_b128 v[196:199], v240 offset:18432
	s_waitcnt lgkmcnt(14)
	v_mfma_f32_32x32x16_f16 v[0:15], v[104:107], v[200:203], v[0:15]
	ds_read_b128 v[200:203], v240 offset:19456
	s_waitcnt lgkmcnt(14)
	v_mfma_f32_32x32x16_f16 v[0:15], v[108:111], v[204:207], v[0:15]
	ds_read_b128 v[204:207], v240 offset:20480
	s_waitcnt lgkmcnt(14)
	v_mfma_f32_32x32x16_f16 v[0:15], v[112:115], v[208:211], v[0:15]
	ds_read_b128 v[208:211], v240 offset:21504
	s_waitcnt lgkmcnt(14)
	v_mfma_f32_32x32x16_f16 v[0:15], v[116:119], v[212:215], v[0:15]
	ds_read_b128 v[212:215], v240 offset:22528
	s_waitcnt lgkmcnt(14)
	v_mfma_f32_32x32x16_f16 v[0:15], v[120:123], v[216:219], v[0:15]
	ds_read_b128 v[216:219], v240 offset:23552
	s_waitcnt lgkmcnt(14)
	v_mfma_f32_32x32x16_f16 v[220:235], v[28:31], v[124:127], 0
	s_waitcnt lgkmcnt(14)
	v_mfma_f32_32x32x16_f16 v[220:235], v[32:35], v[128:131], v[220:235]
	s_add_i32 s20, s14, 7
	s_cmp_lt_u32 s20, 12
	s_cselect_b32 s26, s8, s10
	s_cselect_b32 s27, s9, s11
	s_waitcnt lgkmcnt(14)
	v_mfma_f32_32x32x16_f16 v[220:235], v[36:39], v[132:135], v[220:235]
	s_cselect_b32 s21, 0, 12
	s_cmp_lt_u32 s20, 24
	s_cselect_b32 s26, s26, s0
	s_cselect_b32 s27, s27, s1
	s_waitcnt lgkmcnt(14)
	v_mfma_f32_32x32x16_f16 v[220:235], v[40:43], v[136:139], v[220:235]
	s_cselect_b32 s21, s21, 24
	s_sub_i32 s20, s20, s21
	s_lshr_b32 s21, s20, 1
	s_and_b32 s20, s20, 1
	s_waitcnt lgkmcnt(14)
	v_mfma_f32_32x32x16_f16 v[220:235], v[44:47], v[140:143], v[220:235]
	s_add_i32 s21, s21, s15
	s_lshl_b32 s21, s21, 15
	s_lshl_b32 s20, s20, 11
	s_add_i32 s21, s21, s20
	s_waitcnt lgkmcnt(14)
	v_mfma_f32_32x32x16_f16 v[220:235], v[48:51], v[144:147], v[220:235]
	s_add_u32 s26, s26, s21
	s_addc_u32 s27, s27, 0
	s_waitcnt lgkmcnt(14)
	v_mfma_f32_32x32x16_f16 v[220:235], v[52:55], v[148:151], v[220:235]
	v_cvt_pk_f16_f32 v244, v0, v1
	v_cvt_pk_f16_f32 v245, v2, v3
	s_waitcnt lgkmcnt(14)
	v_mfma_f32_32x32x16_f16 v[220:235], v[56:59], v[152:155], v[220:235]
	v_cvt_pk_f16_f32 v246, v4, v5
	v_cvt_pk_f16_f32 v247, v6, v7
	s_waitcnt lgkmcnt(14)
	v_mfma_f32_32x32x16_f16 v[220:235], v[60:63], v[156:159], v[220:235]
	v_cvt_pk_f16_f32 v248, v8, v9
	v_cvt_pk_f16_f32 v249, v10, v11
	s_waitcnt lgkmcnt(14)
	v_mfma_f32_32x32x16_f16 v[220:235], v[64:67], v[160:163], v[220:235]
	v_cvt_pk_f16_f32 v250, v12, v13
	v_cvt_pk_f16_f32 v251, v14, v15
	s_waitcnt lgkmcnt(13)
	v_mfma_f32_32x32x16_f16 v[220:235], v[68:71], v[164:167], v[220:235]
	global_store_dwordx4 v241, v[244:247], s[26:27]
	s_waitcnt lgkmcnt(12)
	v_mfma_f32_32x32x16_f16 v[220:235], v[72:75], v[168:171], v[220:235]
	global_store_dwordx4 v241, v[248:251], s[26:27] offset:1024
	s_waitcnt lgkmcnt(11)
	v_mfma_f32_32x32x16_f16 v[220:235], v[76:79], v[172:175], v[220:235]
	s_waitcnt lgkmcnt(10)
	v_mfma_f32_32x32x16_f16 v[220:235], v[80:83], v[176:179], v[220:235]
	s_waitcnt lgkmcnt(9)
	v_mfma_f32_32x32x16_f16 v[220:235], v[84:87], v[180:183], v[220:235]
	s_waitcnt lgkmcnt(8)
	v_mfma_f32_32x32x16_f16 v[220:235], v[88:91], v[184:187], v[220:235]
	s_waitcnt lgkmcnt(7)
	v_mfma_f32_32x32x16_f16 v[220:235], v[92:95], v[188:191], v[220:235]
	s_waitcnt lgkmcnt(6)
	v_mfma_f32_32x32x16_f16 v[220:235], v[96:99], v[192:195], v[220:235]
	s_waitcnt lgkmcnt(5)
	v_mfma_f32_32x32x16_f16 v[220:235], v[100:103], v[196:199], v[220:235]
	s_waitcnt lgkmcnt(4)
	v_mfma_f32_32x32x16_f16 v[220:235], v[104:107], v[200:203], v[220:235]
	s_waitcnt lgkmcnt(3)
	v_mfma_f32_32x32x16_f16 v[220:235], v[108:111], v[204:207], v[220:235]
	s_waitcnt lgkmcnt(2)
	v_mfma_f32_32x32x16_f16 v[220:235], v[112:115], v[208:211], v[220:235]
	s_waitcnt lgkmcnt(1)
	v_mfma_f32_32x32x16_f16 v[220:235], v[116:119], v[212:215], v[220:235]
	s_waitcnt lgkmcnt(0)
	v_mfma_f32_32x32x16_f16 v[220:235], v[120:123], v[216:219], v[220:235]
	s_add_i32 s20, s14, 8
	s_cmp_lt_u32 s20, 12
	s_cselect_b32 s26, s8, s10
	s_cselect_b32 s27, s9, s11
	s_cselect_b32 s21, 0, 12
	s_cmp_lt_u32 s20, 24
	s_cselect_b32 s26, s26, s0
	s_cselect_b32 s27, s27, s1
	s_cselect_b32 s21, s21, 24
	s_sub_i32 s20, s20, s21
	s_lshr_b32 s21, s20, 1
	s_and_b32 s20, s20, 1
	s_add_i32 s21, s21, s15
	s_lshl_b32 s21, s21, 15
	s_lshl_b32 s20, s20, 11
	s_add_i32 s21, s21, s20
	s_add_u32 s26, s26, s21
	s_addc_u32 s27, s27, 0
	s_nop 7
	v_cvt_pk_f16_f32 v244, v220, v221
	v_cvt_pk_f16_f32 v245, v222, v223
	v_cvt_pk_f16_f32 v246, v224, v225
	v_cvt_pk_f16_f32 v247, v226, v227
	v_cvt_pk_f16_f32 v248, v228, v229
	v_cvt_pk_f16_f32 v249, v230, v231
	v_cvt_pk_f16_f32 v250, v232, v233
	v_cvt_pk_f16_f32 v251, v234, v235
	global_store_dwordx4 v241, v[244:247], s[26:27]
	global_store_dwordx4 v241, v[248:251], s[26:27] offset:1024
	s_endpgm
.Lqkv_p2S:
	ds_read_b128 v[124:127], v240 offset:24576
	ds_read_b128 v[128:131], v240 offset:25600
	ds_read_b128 v[132:135], v240 offset:26624
	ds_read_b128 v[136:139], v240 offset:27648
	ds_read_b128 v[140:143], v240 offset:28672
	ds_read_b128 v[144:147], v240 offset:29696
	ds_read_b128 v[148:151], v240 offset:30720
	ds_read_b128 v[152:155], v240 offset:31744
	ds_read_b128 v[156:159], v240 offset:32768
	ds_read_b128 v[160:163], v240 offset:33792
	ds_read_b128 v[164:167], v240 offset:34816
	ds_read_b128 v[168:171], v240 offset:35840
	ds_read_b128 v[172:175], v240 offset:36864
	ds_read_b128 v[176:179], v240 offset:37888
	ds_read_b128 v[180:183], v240 offset:38912
	ds_read_b128 v[184:187], v240 offset:39936
	ds_read_b128 v[188:191], v240 offset:40960
	ds_read_b128 v[192:195], v240 offset:41984
	ds_read_b128 v[196:199], v240 offset:43008
	ds_read_b128 v[200:203], v240 offset:44032
	ds_read_b128 v[204:207], v240 offset:45056
	ds_read_b128 v[208:211], v240 offset:46080
	ds_read_b128 v[212:215], v240 offset:47104
	ds_read_b128 v[216:219], v240 offset:48128
	s_add_u32 s24, s22, 122880
	s_addc_u32 s25, s23, 0
	s_waitcnt lgkmcnt(14)
	v_mfma_f32_32x32x16_f16 v[0:15], v[124:127], v[28:31], 0
	ds_read_b128 v[124:127], v242 offset:0
	global_load_dwordx4 v[16:19], v236, s[24:25]
	global_load_dwordx4 v[20:23], v237, s[24:25]
	global_load_dwordx4 v[24:27], v238, s[24:25]
	s_waitcnt lgkmcnt(14)
	v_mfma_f32_32x32x16_f16 v[0:15], v[128:131], v[32:35], v[0:15]
	ds_read_b128 v[128:131], v242 offset:1024
	s_waitcnt lgkmcnt(14)
	v_mfma_f32_32x32x16_f16 v[0:15], v[132:135], v[36:39], v[0:15]
	ds_read_b128 v[132:135], v242 offset:2048
	s_waitcnt lgkmcnt(14)
	v_mfma_f32_32x32x16_f16 v[0:15], v[136:139], v[40:43], v[0:15]
	ds_read_b128 v[136:139], v242 offset:3072
	s_waitcnt lgkmcnt(14)
	v_mfma_f32_32x32x16_f16 v[0:15], v[140:143], v[44:47], v[0:15]
	ds_read_b128 v[140:143], v242 offset:4096
	s_waitcnt lgkmcnt(14)
	v_mfma_f32_32x32x16_f16 v[0:15], v[144:147], v[48:51], v[0:15]
	ds_read_b128 v[144:147], v242 offset:5120
	s_waitcnt lgkmcnt(14)
	v_mfma_f32_32x32x16_f16 v[0:15], v[148:151], v[52:55], v[0:15]
	ds_read_b128 v[148:151], v242 offset:6144
	s_waitcnt lgkmcnt(14)
	v_mfma_f32_32x32x16_f16 v[0:15], v[152:155], v[56:59], v[0:15]
	ds_read_b128 v[152:155], v242 offset:7168
	s_waitcnt lgkmcnt(14)
	v_mfma_f32_32x32x16_f16 v[0:15], v[156:159], v[60:63], v[0:15]
	ds_read_b128 v[156:159], v242 offset:8192
	s_waitcnt lgkmcnt(14)
	v_mfma_f32_32x32x16_f16 v[0:15], v[160:163], v[64:67], v[0:15]
	ds_read_b128 v[160:163], v242 offset:9216
	s_waitcnt lgkmcnt(14)
	v_mfma_f32_32x32x16_f16 v[0:15], v[164:167], v[68:71], v[0:15]
	ds_read_b128 v[164:167], v242 offset:10240
	s_waitcnt lgkmcnt(14)
	v_mfma_f32_32x32x16_f16 v[0:15], v[168:171], v[72:75], v[0:15]
	ds_read_b128 v[168:171], v242 offset:11264
	s_waitcnt lgkmcnt(14)
	v_mfma_f32_32x32x16_f16 v[0:15], v[172:175], v[76:79], v[0:15]
	ds_read_b128 v[172:175], v242 offset:12288
	s_waitcnt lgkmcnt(14)
	v_mfma_f32_32x32x16_f16 v[0:15], v[176:179], v[80:83], v[0:15]
	ds_read_b128 v[176:179], v242 offset:13312
	s_waitcnt lgkmcnt(14)
	v_mfma_f32_32x32x16_f16 v[0:15], v[180:183], v[84:87], v[0:15]
	ds_read_b128 v[180:183], v242 offset:14336
	s_waitcnt lgkmcnt(14)
	v_mfma_f32_32x32x16_f16 v[0:15], v[184:187], v[88:91], v[0:15]
	ds_read_b128 v[184:187], v242 offset:15360
	s_waitcnt lgkmcnt(14)
	v_mfma_f32_32x32x16_f16 v[0:15], v[188:191], v[92:95], v[0:15]
	ds_read_b128 v[188:191], v242 offset:16384
	s_waitcnt lgkmcnt(14)
	v_mfma_f32_32x32x16_f16 v[0:15], v[192:195], v[96:99], v[0:15]
	ds_read_b128 v[192:195], v242 offset:17408
	s_waitcnt lgkmcnt(14)
	v_mfma_f32_32x32x16_f16 v[0:15], v[196:199], v[100:103], v[0:15]
	ds_read_b128 v[196:199], v242 offset:18432
	s_waitcnt vmcnt(0)
	ds_write_b128 v252, v[16:19] offset:49152
	ds_write_b128 v253, v[20:23] offset:49152
	ds_write_b128 v254, v[24:27] offset:49152
	s_waitcnt lgkmcnt(14)
	v_mfma_f32_32x32x16_f16 v[0:15], v[200:203], v[104:107], v[0:15]
	ds_read_b128 v[200:203], v242 offset:19456
	s_waitcnt lgkmcnt(14)
	v_mfma_f32_32x32x16_f16 v[0:15], v[204:207], v[108:111], v[0:15]
	ds_read_b128 v[204:207], v242 offset:20480
	s_waitcnt lgkmcnt(14)
	v_mfma_f32_32x32x16_f16 v[0:15], v[208:211], v[112:115], v[0:15]
	ds_read_b128 v[208:211], v242 offset:21504
	s_waitcnt lgkmcnt(14)
	v_mfma_f32_32x32x16_f16 v[0:15], v[212:215], v[116:119], v[0:15]
	ds_read_b128 v[212:215], v242 offset:22528
	s_waitcnt lgkmcnt(14)
	v_mfma_f32_32x32x16_f16 v[0:15], v[216:219], v[120:123], v[0:15]
	ds_read_b128 v[216:219], v242 offset:23552
	s_waitcnt lgkmcnt(5)
	s_barrier
	s_add_u32 s24, s22, 147456
	s_addc_u32 s25, s23, 0
	s_waitcnt lgkmcnt(14)
	v_mfma_f32_32x32x16_f16 v[220:235], v[124:127], v[28:31], 0
	ds_read_b128 v[124:127], v242 offset:24576
	global_load_dwordx4 v[16:19], v236, s[24:25]
	global_load_dwordx4 v[20:23], v237, s[24:25]
	global_load_dwordx4 v[24:27], v238, s[24:25]
	s_waitcnt lgkmcnt(14)
	v_mfma_f32_32x32x16_f16 v[220:235], v[128:131], v[32:35], v[220:235]
	ds_read_b128 v[128:131], v242 offset:25600
	s_add_i32 s20, s14, 3
	s_cmp_lt_u32 s20, 12
	s_cselect_b32 s26, s8, s10
	s_cselect_b32 s27, s9, s11
	s_waitcnt lgkmcnt(14)
	v_mfma_f32_32x32x16_f16 v[220:235], v[132:135], v[36:39], v[220:235]
	ds_read_b128 v[132:135], v242 offset:26624
	s_cselect_b32 s21, 0, 12
	s_cmp_lt_u32 s20, 24
	s_cselect_b32 s26, s26, s0
	s_cselect_b32 s27, s27, s1
	s_waitcnt lgkmcnt(14)
	v_mfma_f32_32x32x16_f16 v[220:235], v[136:139], v[40:43], v[220:235]
	ds_read_b128 v[136:139], v242 offset:27648
	s_cselect_b32 s21, s21, 24
	s_sub_i32 s20, s20, s21
	s_lshr_b32 s21, s20, 1
	s_and_b32 s20, s20, 1
	s_waitcnt lgkmcnt(14)
	v_mfma_f32_32x32x16_f16 v[220:235], v[140:143], v[44:47], v[220:235]
	ds_read_b128 v[140:143], v242 offset:28672
	s_add_i32 s21, s21, s15
	s_lshl_b32 s21, s21, 15
	s_lshl_b32 s20, s20, 11
	s_add_i32 s21, s21, s20
	s_waitcnt lgkmcnt(14)
	v_mfma_f32_32x32x16_f16 v[220:235], v[144:147], v[48:51], v[220:235]
	ds_read_b128 v[144:147], v242 offset:29696
	s_add_u32 s26, s26, s21
	s_addc_u32 s27, s27, 0
	s_waitcnt lgkmcnt(14)
	v_mfma_f32_32x32x16_f16 v[220:235], v[148:151], v[52:55], v[220:235]
	ds_read_b128 v[148:151], v242 offset:30720
	v_cvt_pk_f16_f32 v244, v0, v1
	v_cvt_pk_f16_f32 v245, v2, v3
	s_waitcnt lgkmcnt(14)
	v_mfma_f32_32x32x16_f16 v[220:235], v[152:155], v[56:59], v[220:235]
	ds_read_b128 v[152:155], v242 offset:31744
	v_cvt_pk_f16_f32 v246, v4, v5
	v_cvt_pk_f16_f32 v247, v6, v7
	s_waitcnt lgkmcnt(14)
	v_mfma_f32_32x32x16_f16 v[220:235], v[156:159], v[60:63], v[220:235]
	ds_read_b128 v[156:159], v242 offset:32768
	v_cvt_pk_f16_f32 v248, v8, v9
	v_cvt_pk_f16_f32 v249, v10, v11
	s_waitcnt lgkmcnt(14)
	v_mfma_f32_32x32x16_f16 v[220:235], v[160:163], v[64:67], v[220:235]
	ds_read_b128 v[160:163], v242 offset:33792
	v_cvt_pk_f16_f32 v250, v12, v13
	v_cvt_pk_f16_f32 v251, v14, v15
	s_waitcnt lgkmcnt(14)
	v_mfma_f32_32x32x16_f16 v[220:235], v[164:167], v[68:71], v[220:235]
	ds_read_b128 v[164:167], v242 offset:34816
	global_store_dwordx4 v241, v[244:247], s[26:27]
	s_waitcnt lgkmcnt(14)
	v_mfma_f32_32x32x16_f16 v[220:235], v[168:171], v[72:75], v[220:235]
	ds_read_b128 v[168:171], v242 offset:35840
	global_store_dwordx4 v241, v[248:251], s[26:27] offset:1024
	s_waitcnt lgkmcnt(14)
	v_mfma_f32_32x32x16_f16 v[220:235], v[172:175], v[76:79], v[220:235]
	ds_read_b128 v[172:175], v242 offset:36864
	s_waitcnt lgkmcnt(14)
	v_mfma_f32_32x32x16_f16 v[220:235], v[176:179], v[80:83], v[220:235]
	ds_read_b128 v[176:179], v242 offset:37888
	s_waitcnt lgkmcnt(14)
	v_mfma_f32_32x32x16_f16 v[220:235], v[180:183], v[84:87], v[220:235]
	ds_read_b128 v[180:183], v242 offset:38912
	s_waitcnt lgkmcnt(14)
	v_mfma_f32_32x32x16_f16 v[220:235], v[184:187], v[88:91], v[220:235]
	ds_read_b128 v[184:187], v242 offset:39936
	s_waitcnt lgkmcnt(14)
	v_mfma_f32_32x32x16_f16 v[220:235], v[188:191], v[92:95], v[220:235]
	ds_read_b128 v[188:191], v242 offset:40960
	s_waitcnt lgkmcnt(14)
	v_mfma_f32_32x32x16_f16 v[220:235], v[192:195], v[96:99], v[220:235]
	ds_read_b128 v[192:195], v242 offset:41984
	s_waitcnt lgkmcnt(14)
	v_mfma_f32_32x32x16_f16 v[220:235], v[196:199], v[100:103], v[220:235]
	ds_read_b128 v[196:199], v242 offset:43008
	s_waitcnt vmcnt(2)
	ds_write_b128 v236, v[16:19] offset:0
	ds_write_b128 v237, v[20:23] offset:0
	ds_write_b128 v238, v[24:27] offset:0
	s_waitcnt lgkmcnt(14)
	v_mfma_f32_32x32x16_f16 v[220:235], v[200:203], v[104:107], v[220:235]
	ds_read_b128 v[200:203], v242 offset:44032
	s_waitcnt lgkmcnt(14)
	v_mfma_f32_32x32x16_f16 v[220:235], v[204:207], v[108:111], v[220:235]
	ds_read_b128 v[204:207], v242 offset:45056
	s_waitcnt lgkmcnt(14)
	v_mfma_f32_32x32x16_f16 v[220:235], v[208:211], v[112:115], v[220:235]
	ds_read_b128 v[208:211], v242 offset:46080
	s_waitcnt lgkmcnt(14)
	v_mfma_f32_32x32x16_f16 v[220:235], v[212:215], v[116:119], v[220:235]
	ds_read_b128 v[212:215], v242 offset:47104
	s_waitcnt lgkmcnt(14)
	v_mfma_f32_32x32x16_f16 v[220:235], v[216:219], v[120:123], v[220:235]
	ds_read_b128 v[216:219], v242 offset:48128
	s_waitcnt lgkmcnt(5)
	s_barrier
	s_add_u32 s24, s22, 172032
	s_addc_u32 s25, s23, 0
	s_waitcnt lgkmcnt(14)
	v_mfma_f32_32x32x16_f16 v[0:15], v[124:127], v[28:31], 0
	ds_read_b128 v[124:127], v239 offset:0
	global_load_dwordx4 v[16:19], v236, s[24:25]
	global_load_dwordx4 v[20:23], v237, s[24:25]
	global_load_dwordx4 v[24:27], v238, s[24:25]
	s_waitcnt lgkmcnt(14)
	v_mfma_f32_32x32x16_f16 v[0:15], v[128:131], v[32:35], v[0:15]
	ds_read_b128 v[128:131], v239 offset:1024
	s_add_i32 s20, s14, 4
	s_cmp_lt_u32 s20, 12
	s_cselect_b32 s26, s8, s10
	s_cselect_b32 s27, s9, s11
	s_waitcnt lgkmcnt(14)
	v_mfma_f32_32x32x16_f16 v[0:15], v[132:135], v[36:39], v[0:15]
	ds_read_b128 v[132:135], v239 offset:2048
	s_cselect_b32 s21, 0, 12
	s_cmp_lt_u32 s20, 24
	s_cselect_b32 s26, s26, s0
	s_cselect_b32 s27, s27, s1
	s_waitcnt lgkmcnt(14)
	v_mfma_f32_32x32x16_f16 v[0:15], v[136:139], v[40:43], v[0:15]
	ds_read_b128 v[136:139], v239 offset:3072
	s_cselect_b32 s21, s21, 24
	s_sub_i32 s20, s20, s21
	s_lshr_b32 s21, s20, 1
	s_and_b32 s20, s20, 1
	s_waitcnt lgkmcnt(14)
	v_mfma_f32_32x32x16_f16 v[0:15], v[140:143], v[44:47], v[0:15]
	ds_read_b128 v[140:143], v239 offset:4096
	s_add_i32 s21, s21, s15
	s_lshl_b32 s21, s21, 15
	s_lshl_b32 s20, s20, 11
	s_add_i32 s21, s21, s20
	s_waitcnt lgkmcnt(14)
	v_mfma_f32_32x32x16_f16 v[0:15], v[144:147], v[48:51], v[0:15]
	ds_read_b128 v[144:147], v239 offset:5120
	s_add_u32 s26, s26, s21
	s_addc_u32 s27, s27, 0
	s_waitcnt lgkmcnt(14)
	v_mfma_f32_32x32x16_f16 v[0:15], v[148:151], v[52:55], v[0:15]
	ds_read_b128 v[148:151], v239 offset:6144
	v_cvt_pk_f16_f32 v244, v220, v221
	v_cvt_pk_f16_f32 v245, v222, v223
	s_waitcnt lgkmcnt(14)
	v_mfma_f32_32x32x16_f16 v[0:15], v[152:155], v[56:59], v[0:15]
	ds_read_b128 v[152:155], v239 offset:7168
	v_cvt_pk_f16_f32 v246, v224, v225
	v_cvt_pk_f16_f32 v247, v226, v227
	s_waitcnt lgkmcnt(14)
	v_mfma_f32_32x32x16_f16 v[0:15], v[156:159], v[60:63], v[0:15]
	ds_read_b128 v[156:159], v239 offset:8192
	v_cvt_pk_f16_f32 v248, v228, v229
	v_cvt_pk_f16_f32 v249, v230, v231
	s_waitcnt lgkmcnt(14)
	v_mfma_f32_32x32x16_f16 v[0:15], v[160:163], v[64:67], v[0:15]
	ds_read_b128 v[160:163], v239 offset:9216
	v_cvt_pk_f16_f32 v250, v232, v233
	v_cvt_pk_f16_f32 v251, v234, v235
	s_waitcnt lgkmcnt(14)
	v_mfma_f32_32x32x16_f16 v[0:15], v[164:167], v[68:71], v[0:15]
	ds_read_b128 v[164:167], v239 offset:10240
	global_store_dwordx4 v241, v[244:247], s[26:27]
	s_waitcnt lgkmcnt(14)
	v_mfma_f32_32x32x16_f16 v[0:15], v[168:171], v[72:75], v[0:15]
	ds_read_b128 v[168:171], v239 offset:11264
	global_store_dwordx4 v241, v[248:251], s[26:27] offset:1024
	s_waitcnt lgkmcnt(14)
	v_mfma_f32_32x32x16_f16 v[0:15], v[172:175], v[76:79], v[0:15]
	ds_read_b128 v[172:175], v239 offset:12288
	s_waitcnt lgkmcnt(14)
	v_mfma_f32_32x32x16_f16 v[0:15], v[176:179], v[80:83], v[0:15]
	ds_read_b128 v[176:179], v239 offset:13312
	s_waitcnt lgkmcnt(14)
	v_mfma_f32_32x32x16_f16 v[0:15], v[180:183], v[84:87], v[0:15]
	ds_read_b128 v[180:183], v239 offset:14336
	s_waitcnt lgkmcnt(14)
	v_mfma_f32_32x32x16_f16 v[0:15], v[184:187], v[88:91], v[0:15]
	ds_read_b128 v[184:187], v239 offset:15360
	s_waitcnt lgkmcnt(14)
	v_mfma_f32_32x32x16_f16 v[0:15], v[188:191], v[92:95], v[0:15]
	ds_read_b128 v[188:191], v239 offset:16384
	s_waitcnt lgkmcnt(14)
	v_mfma_f32_32x32x16_f16 v[0:15], v[192:195], v[96:99], v[0:15]
	ds_read_b128 v[192:195], v239 offset:17408
	s_waitcnt lgkmcnt(14)
	v_mfma_f32_32x32x16_f16 v[0:15], v[196:199], v[100:103], v[0:15]
	ds_read_b128 v[196:199], v239 offset:18432
	s_waitcnt vmcnt(2)
	ds_write_b128 v236, v[16:19] offset:24576
	ds_write_b128 v237, v[20:23] offset:24576
	ds_write_b128 v238, v[24:27] offset:24576
	s_waitcnt lgkmcnt(14)
	v_mfma_f32_32x32x16_f16 v[0:15], v[200:203], v[104:107], v[0:15]
	ds_read_b128 v[200:203], v239 offset:19456
	s_waitcnt lgkmcnt(14)
	v_mfma_f32_32x32x16_f16 v[0:15], v[204:207], v[108:111], v[0:15]
	ds_read_b128 v[204:207], v239 offset:20480
	s_waitcnt lgkmcnt(14)
	v_mfma_f32_32x32x16_f16 v[0:15], v[208:211], v[112:115], v[0:15]
	ds_read_b128 v[208:211], v239 offset:21504
	s_waitcnt lgkmcnt(14)
	v_mfma_f32_32x32x16_f16 v[0:15], v[212:215], v[116:119], v[0:15]
	ds_read_b128 v[212:215], v239 offset:22528
	s_waitcnt lgkmcnt(14)
	v_mfma_f32_32x32x16_f16 v[0:15], v[216:219], v[120:123], v[0:15]
	ds_read_b128 v[216:219], v239 offset:23552
	s_waitcnt lgkmcnt(5)
	s_barrier
	s_add_u32 s24, s22, 196608
	s_addc_u32 s25, s23, 0
	s_waitcnt lgkmcnt(14)
	v_mfma_f32_32x32x16_f16 v[220:235], v[124:127], v[28:31], 0
	ds_read_b128 v[124:127], v239 offset:24576
	global_load_dwordx4 v[16:19], v236, s[24:25]
	global_load_dwordx4 v[20:23], v237, s[24:25]
	global_load_dwordx4 v[24:27], v238, s[24:25]
	s_waitcnt lgkmcnt(14)
	v_mfma_f32_32x32x16_f16 v[220:235], v[128:131], v[32:35], v[220:235]
	ds_read_b128 v[128:131], v239 offset:25600
	s_add_i32 s20, s14, 5
	s_cmp_lt_u32 s20, 12
	s_cselect_b32 s26, s8, s10
	s_cselect_b32 s27, s9, s11
	s_waitcnt lgkmcnt(14)
	v_mfma_f32_32x32x16_f16 v[220:235], v[132:135], v[36:39], v[220:235]
	ds_read_b128 v[132:135], v239 offset:26624
	s_cselect_b32 s21, 0, 12
	s_cmp_lt_u32 s20, 24
	s_cselect_b32 s26, s26, s0
	s_cselect_b32 s27, s27, s1
	s_waitcnt lgkmcnt(14)
	v_mfma_f32_32x32x16_f16 v[220:235], v[136:139], v[40:43], v[220:235]
	ds_read_b128 v[136:139], v239 offset:27648
	s_cselect_b32 s21, s21, 24
	s_sub_i32 s20, s20, s21
	s_lshr_b32 s21, s20, 1
	s_and_b32 s20, s20, 1
	s_waitcnt lgkmcnt(14)
	v_mfma_f32_32x32x16_f16 v[220:235], v[140:143], v[44:47], v[220:235]
	ds_read_b128 v[140:143], v239 offset:28672
	s_add_i32 s21, s21, s15
	s_lshl_b32 s21, s21, 15
	s_lshl_b32 s20, s20, 11
	s_add_i32 s21, s21, s20
	s_waitcnt lgkmcnt(14)
	v_mfma_f32_32x32x16_f16 v[220:235], v[144:147], v[48:51], v[220:235]
	ds_read_b128 v[144:147], v239 offset:29696
	s_add_u32 s26, s26, s21
	s_addc_u32 s27, s27, 0
	s_waitcnt lgkmcnt(14)
	v_mfma_f32_32x32x16_f16 v[220:235], v[148:151], v[52:55], v[220:235]
	ds_read_b128 v[148:151], v239 offset:30720
	v_cvt_pk_f16_f32 v244, v0, v1
	v_cvt_pk_f16_f32 v245, v2, v3
	s_waitcnt lgkmcnt(14)
	v_mfma_f32_32x32x16_f16 v[220:235], v[152:155], v[56:59], v[220:235]
	ds_read_b128 v[152:155], v239 offset:31744
	v_cvt_pk_f16_f32 v246, v4, v5
	v_cvt_pk_f16_f32 v247, v6, v7
	s_waitcnt lgkmcnt(14)
	v_mfma_f32_32x32x16_f16 v[220:235], v[156:159], v[60:63], v[220:235]
	ds_read_b128 v[156:159], v239 offset:32768
	v_cvt_pk_f16_f32 v248, v8, v9
	v_cvt_pk_f16_f32 v249, v10, v11
	s_waitcnt lgkmcnt(14)
	v_mfma_f32_32x32x16_f16 v[220:235], v[160:163], v[64:67], v[220:235]
	ds_read_b128 v[160:163], v239 offset:33792
	v_cvt_pk_f16_f32 v250, v12, v13
	v_cvt_pk_f16_f32 v251, v14, v15
	s_waitcnt lgkmcnt(14)
	v_mfma_f32_32x32x16_f16 v[220:235], v[164:167], v[68:71], v[220:235]
	ds_read_b128 v[164:167], v239 offset:34816
	global_store_dwordx4 v241, v[244:247], s[26:27]
	s_waitcnt lgkmcnt(14)
	v_mfma_f32_32x32x16_f16 v[220:235], v[168:171], v[72:75], v[220:235]
	ds_read_b128 v[168:171], v239 offset:35840
	global_store_dwordx4 v241, v[248:251], s[26:27] offset:1024
	s_waitcnt lgkmcnt(14)
	v_mfma_f32_32x32x16_f16 v[220:235], v[172:175], v[76:79], v[220:235]
	ds_read_b128 v[172:175], v239 offset:36864
	s_waitcnt lgkmcnt(14)
	v_mfma_f32_32x32x16_f16 v[220:235], v[176:179], v[80:83], v[220:235]
	ds_read_b128 v[176:179], v239 offset:37888
	s_waitcnt lgkmcnt(14)
	v_mfma_f32_32x32x16_f16 v[220:235], v[180:183], v[84:87], v[220:235]
	ds_read_b128 v[180:183], v239 offset:38912
	s_waitcnt lgkmcnt(14)
	v_mfma_f32_32x32x16_f16 v[220:235], v[184:187], v[88:91], v[220:235]
	ds_read_b128 v[184:187], v239 offset:39936
	s_waitcnt lgkmcnt(14)
	v_mfma_f32_32x32x16_f16 v[220:235], v[188:191], v[92:95], v[220:235]
	ds_read_b128 v[188:191], v239 offset:40960
	s_waitcnt lgkmcnt(14)
	v_mfma_f32_32x32x16_f16 v[220:235], v[192:195], v[96:99], v[220:235]
	ds_read_b128 v[192:195], v239 offset:41984
	s_waitcnt lgkmcnt(14)
	v_mfma_f32_32x32x16_f16 v[220:235], v[196:199], v[100:103], v[220:235]
	ds_read_b128 v[196:199], v239 offset:43008
	s_waitcnt vmcnt(2)
	ds_write_b128 v236, v[16:19] offset:49152
	ds_write_b128 v237, v[20:23] offset:49152
	ds_write_b128 v238, v[24:27] offset:49152
	s_waitcnt lgkmcnt(14)
	v_mfma_f32_32x32x16_f16 v[220:235], v[200:203], v[104:107], v[220:235]
	ds_read_b128 v[200:203], v239 offset:44032
	s_waitcnt lgkmcnt(14)
	v_mfma_f32_32x32x16_f16 v[220:235], v[204:207], v[108:111], v[220:235]
	ds_read_b128 v[204:207], v239 offset:45056
	s_waitcnt lgkmcnt(14)
	v_mfma_f32_32x32x16_f16 v[220:235], v[208:211], v[112:115], v[220:235]
	ds_read_b128 v[208:211], v239 offset:46080
	s_waitcnt lgkmcnt(14)
	v_mfma_f32_32x32x16_f16 v[220:235], v[212:215], v[116:119], v[220:235]
	ds_read_b128 v[212:215], v239 offset:47104
	s_waitcnt lgkmcnt(14)
	v_mfma_f32_32x32x16_f16 v[220:235], v[216:219], v[120:123], v[220:235]
	ds_read_b128 v[216:219], v239 offset:48128
	s_waitcnt lgkmcnt(5)
	s_barrier
	s_waitcnt lgkmcnt(14)
	v_mfma_f32_32x32x16_f16 v[0:15], v[124:127], v[28:31], 0
	ds_read_b128 v[124:127], v240 offset:0
	s_waitcnt lgkmcnt(14)
	v_mfma_f32_32x32x16_f16 v[0:15], v[128:131], v[32:35], v[0:15]
	ds_read_b128 v[128:131], v240 offset:1024
	s_add_i32 s20, s14, 6
	s_cmp_lt_u32 s20, 12
	s_cselect_b32 s26, s8, s10
	s_cselect_b32 s27, s9, s11
	s_waitcnt lgkmcnt(14)
	v_mfma_f32_32x32x16_f16 v[0:15], v[132:135], v[36:39], v[0:15]
	ds_read_b128 v[132:135], v240 offset:2048
	s_cselect_b32 s21, 0, 12
	s_cmp_lt_u32 s20, 24
	s_cselect_b32 s26, s26, s0
	s_cselect_b32 s27, s27, s1
	s_waitcnt lgkmcnt(14)
	v_mfma_f32_32x32x16_f16 v[0:15], v[136:139], v[40:43], v[0:15]
	ds_read_b128 v[136:139], v240 offset:3072
	s_cselect_b32 s21, s21, 24
	s_sub_i32 s20, s20, s21
	s_lshr_b32 s21, s20, 1
	s_and_b32 s20, s20, 1
	s_waitcnt lgkmcnt(14)
	v_mfma_f32_32x32x16_f16 v[0:15], v[140:143], v[44:47], v[0:15]
	ds_read_b128 v[140:143], v240 offset:4096
	s_add_i32 s21, s21, s15
	s_lshl_b32 s21, s21, 15
	s_lshl_b32 s20, s20, 11
	s_add_i32 s21, s21, s20
	s_waitcnt lgkmcnt(14)
	v_mfma_f32_32x32x16_f16 v[0:15], v[144:147], v[48:51], v[0:15]
	ds_read_b128 v[144:147], v240 offset:5120
	s_add_u32 s26, s26, s21
	s_addc_u32 s27, s27, 0
	s_waitcnt lgkmcnt(14)
	v_mfma_f32_32x32x16_f16 v[0:15], v[148:151], v[52:55], v[0:15]
	ds_read_b128 v[148:151], v240 offset:6144
	v_cvt_pk_f16_f32 v244, v220, v221
	v_cvt_pk_f16_f32 v245, v222, v223
	s_waitcnt lgkmcnt(14)
	v_mfma_f32_32x32x16_f16 v[0:15], v[152:155], v[56:59], v[0:15]
	ds_read_b128 v[152:155], v240 offset:7168
	v_cvt_pk_f16_f32 v246, v224, v225
	v_cvt_pk_f16_f32 v247, v226, v227
	s_waitcnt lgkmcnt(14)
	v_mfma_f32_32x32x16_f16 v[0:15], v[156:159], v[60:63], v[0:15]
	ds_read_b128 v[156:159], v240 offset:8192
	v_cvt_pk_f16_f32 v248, v228, v229
	v_cvt_pk_f16_f32 v249, v230, v231
	s_waitcnt lgkmcnt(14)
	v_mfma_f32_32x32x16_f16 v[0:15], v[160:163], v[64:67], v[0:15]
	ds_read_b128 v[160:163], v240 offset:9216
	v_cvt_pk_f16_f32 v250, v232, v233
	v_cvt_pk_f16_f32 v251, v234, v235
	s_waitcnt lgkmcnt(14)
	v_mfma_f32_32x32x16_f16 v[0:15], v[164:167], v[68:71], v[0:15]
	ds_read_b128 v[164:167], v240 offset:10240
	global_store_dwordx4 v241, v[244:247], s[26:27]
	s_waitcnt lgkmcnt(14)
	v_mfma_f32_32x32x16_f16 v[0:15], v[168:171], v[72:75], v[0:15]
	ds_read_b128 v[168:171], v240 offset:11264
	global_store_dwordx4 v241, v[248:251], s[26:27] offset:1024
	s_waitcnt lgkmcnt(14)
	v_mfma_f32_32x32x16_f16 v[0:15], v[172:175], v[76:79], v[0:15]
	ds_read_b128 v[172:175], v240 offset:12288
	s_waitcnt lgkmcnt(14)
	v_mfma_f32_32x32x16_f16 v[0:15], v[176:179], v[80:83], v[0:15]
	ds_read_b128 v[176:179], v240 offset:13312
	s_waitcnt lgkmcnt(14)
	v_mfma_f32_32x32x16_f16 v[0:15], v[180:183], v[84:87], v[0:15]
	ds_read_b128 v[180:183], v240 offset:14336
	s_waitcnt lgkmcnt(14)
	v_mfma_f32_32x32x16_f16 v[0:15], v[184:187], v[88:91], v[0:15]
	ds_read_b128 v[184:187], v240 offset:15360
	s_waitcnt lgkmcnt(14)
	v_mfma_f32_32x32x16_f16 v[0:15], v[188:191], v[92:95], v[0:15]
	ds_read_b128 v[188:191], v240 offset:16384
	s_waitcnt lgkmcnt(14)
	v_mfma_f32_32x32x16_f16 v[0:15], v[192:195], v[96:99], v[0:15]
	ds_read_b128 v[192:195], v240 offset:17408
	s_waitcnt lgkmcnt(14)
	v_mfma_f32_32x32x16_f16 v[0:15], v[196:199], v[100:103], v[0:15]
	ds_read_b128 v[196:199], v240 offset:18432
	s_waitcnt lgkmcnt(14)
	v_mfma_f32_32x32x16_f16 v[0:15], v[200:203], v[104:107], v[0:15]
	ds_read_b128 v[200:203], v240 offset:19456
	s_waitcnt lgkmcnt(14)
	v_mfma_f32_32x32x16_f16 v[0:15], v[204:207], v[108:111], v[0:15]
	ds_read_b128 v[204:207], v240 offset:20480
	s_waitcnt lgkmcnt(14)
	v_mfma_f32_32x32x16_f16 v[0:15], v[208:211], v[112:115], v[0:15]
	ds_read_b128 v[208:211], v240 offset:21504
	s_waitcnt lgkmcnt(14)
	v_mfma_f32_32x32x16_f16 v[0:15], v[212:215], v[116:119], v[0:15]
	ds_read_b128 v[212:215], v240 offset:22528
	s_waitcnt lgkmcnt(14)
	v_mfma_f32_32x32x16_f16 v[0:15], v[216:219], v[120:123], v[0:15]
	ds_read_b128 v[216:219], v240 offset:23552
	s_waitcnt lgkmcnt(14)
	v_mfma_f32_32x32x16_f16 v[220:235], v[124:127], v[28:31], 0
	s_waitcnt lgkmcnt(14)
	v_mfma_f32_32x32x16_f16 v[220:235], v[128:131], v[32:35], v[220:235]
	s_add_i32 s20, s14, 7
	s_cmp_lt_u32 s20, 12
	s_cselect_b32 s26, s8, s10
	s_cselect_b32 s27, s9, s11
	s_waitcnt lgkmcnt(14)
	v_mfma_f32_32x32x16_f16 v[220:235], v[132:135], v[36:39], v[220:235]
	s_cselect_b32 s21, 0, 12
	s_cmp_lt_u32 s20, 24
	s_cselect_b32 s26, s26, s0
	s_cselect_b32 s27, s27, s1
	s_waitcnt lgkmcnt(14)
	v_mfma_f32_32x32x16_f16 v[220:235], v[136:139], v[40:43], v[220:235]
	s_cselect_b32 s21, s21, 24
	s_sub_i32 s20, s20, s21
	s_lshr_b32 s21, s20, 1
	s_and_b32 s20, s20, 1
	s_waitcnt lgkmcnt(14)
	v_mfma_f32_32x32x16_f16 v[220:235], v[140:143], v[44:47], v[220:235]
	s_add_i32 s21, s21, s15
	s_lshl_b32 s21, s21, 15
	s_lshl_b32 s20, s20, 11
	s_add_i32 s21, s21, s20
	s_waitcnt lgkmcnt(14)
	v_mfma_f32_32x32x16_f16 v[220:235], v[144:147], v[48:51], v[220:235]
	s_add_u32 s26, s26, s21
	s_addc_u32 s27, s27, 0
	s_waitcnt lgkmcnt(14)
	v_mfma_f32_32x32x16_f16 v[220:235], v[148:151], v[52:55], v[220:235]
	v_cvt_pk_f16_f32 v244, v0, v1
	v_cvt_pk_f16_f32 v245, v2, v3
	s_waitcnt lgkmcnt(14)
	v_mfma_f32_32x32x16_f16 v[220:235], v[152:155], v[56:59], v[220:235]
	v_cvt_pk_f16_f32 v246, v4, v5
	v_cvt_pk_f16_f32 v247, v6, v7
	s_waitcnt lgkmcnt(14)
	v_mfma_f32_32x32x16_f16 v[220:235], v[156:159], v[60:63], v[220:235]
	v_cvt_pk_f16_f32 v248, v8, v9
	v_cvt_pk_f16_f32 v249, v10, v11
	s_waitcnt lgkmcnt(14)
	v_mfma_f32_32x32x16_f16 v[220:235], v[160:163], v[64:67], v[220:235]
	v_cvt_pk_f16_f32 v250, v12, v13
	v_cvt_pk_f16_f32 v251, v14, v15
	s_waitcnt lgkmcnt(13)
	v_mfma_f32_32x32x16_f16 v[220:235], v[164:167], v[68:71], v[220:235]
	global_store_dwordx4 v241, v[244:247], s[26:27]
	s_waitcnt lgkmcnt(12)
	v_mfma_f32_32x32x16_f16 v[220:235], v[168:171], v[72:75], v[220:235]
	global_store_dwordx4 v241, v[248:251], s[26:27] offset:1024
	s_waitcnt lgkmcnt(11)
	v_mfma_f32_32x32x16_f16 v[220:235], v[172:175], v[76:79], v[220:235]
	s_waitcnt lgkmcnt(10)
	v_mfma_f32_32x32x16_f16 v[220:235], v[176:179], v[80:83], v[220:235]
	s_waitcnt lgkmcnt(9)
	v_mfma_f32_32x32x16_f16 v[220:235], v[180:183], v[84:87], v[220:235]
	s_waitcnt lgkmcnt(8)
	v_mfma_f32_32x32x16_f16 v[220:235], v[184:187], v[88:91], v[220:235]
	s_waitcnt lgkmcnt(7)
	v_mfma_f32_32x32x16_f16 v[220:235], v[188:191], v[92:95], v[220:235]
	s_waitcnt lgkmcnt(6)
	v_mfma_f32_32x32x16_f16 v[220:235], v[192:195], v[96:99], v[220:235]
	s_waitcnt lgkmcnt(5)
	v_mfma_f32_32x32x16_f16 v[220:235], v[196:199], v[100:103], v[220:235]
	s_waitcnt lgkmcnt(4)
	v_mfma_f32_32x32x16_f16 v[220:235], v[200:203], v[104:107], v[220:235]
	s_waitcnt lgkmcnt(3)
	v_mfma_f32_32x32x16_f16 v[220:235], v[204:207], v[108:111], v[220:235]
	s_waitcnt lgkmcnt(2)
	v_mfma_f32_32x32x16_f16 v[220:235], v[208:211], v[112:115], v[220:235]
	s_waitcnt lgkmcnt(1)
	v_mfma_f32_32x32x16_f16 v[220:235], v[212:215], v[116:119], v[220:235]
	s_waitcnt lgkmcnt(0)
	v_mfma_f32_32x32x16_f16 v[220:235], v[216:219], v[120:123], v[220:235]
	s_add_i32 s20, s14, 8
	s_cmp_lt_u32 s20, 12
	s_cselect_b32 s26, s8, s10
	s_cselect_b32 s27, s9, s11
	s_cselect_b32 s21, 0, 12
	s_cmp_lt_u32 s20, 24
	s_cselect_b32 s26, s26, s0
	s_cselect_b32 s27, s27, s1
	s_cselect_b32 s21, s21, 24
	s_sub_i32 s20, s20, s21
	s_lshr_b32 s21, s20, 1
	s_and_b32 s20, s20, 1
	s_add_i32 s21, s21, s15
	s_lshl_b32 s21, s21, 15
	s_lshl_b32 s20, s20, 11
	s_add_i32 s21, s21, s20
	s_add_u32 s26, s26, s21
	s_addc_u32 s27, s27, 0
	s_nop 7
	v_cvt_pk_f16_f32 v244, v220, v221
	v_cvt_pk_f16_f32 v245, v222, v223
	v_cvt_pk_f16_f32 v246, v224, v225
	v_cvt_pk_f16_f32 v247, v226, v227
	v_cvt_pk_f16_f32 v248, v228, v229
	v_cvt_pk_f16_f32 v249, v230, v231
	v_cvt_pk_f16_f32 v250, v232, v233
	v_cvt_pk_f16_f32 v251, v234, v235
	global_store_dwordx4 v241, v[244:247], s[26:27]
	global_store_dwordx4 v241, v[248:251], s[26:27] offset:1024
	s_endpgm
.Lqkv_p1N:
	v_mov_b32_e32 v211, 0
	v_lshlrev_b32_e32 v208, 4, v0
	v_mov_b32_e32 v209, v211
	v_lshl_add_u64 v[2:3], s[6:7], 0, v[208:209]
	s_movk_i32 s3, 0x2000
	v_add_co_u32_e32 v4, vcc, s3, v2
	v_lshrrev_b32_e32 v214, 6, v0
	s_nop 0
	v_addc_co_u32_e32 v5, vcc, 0, v3, vcc
	s_movk_i32 s3, 0x4000
	v_add_co_u32_e32 v6, vcc, s3, v2
	v_lshlrev_b32_e32 v1, 5, v214
	v_addc_co_u32_e32 v7, vcc, 0, v3, vcc
	v_lshl_or_b32 v1, s12, 8, v1
	s_movk_i32 s6, 0x600
	v_mov_b64_e32 v[4:5], s[4:5]
	v_mad_i64_i32 v[72:73], s[4:5], v1, s6, v[4:5]
	v_bfe_u32 v1, v0, 4, 2
	v_and_b32_e32 v80, 15, v0
	v_lshlrev_b32_e32 v210, 4, v80
	v_mul_u32_u24_e32 v4, 0x180, v1
	v_lshl_add_u64 v[40:41], v[72:73], 0, v[210:211]
	v_lshlrev_b32_e32 v48, 2, v4
	v_mov_b32_e32 v49, v211
	v_lshl_add_u64 v[12:13], v[40:41], 0, v[48:49]
	s_movk_i32 s4, 0x1000
	v_add_co_u32_e32 v14, vcc, s4, v12
	s_movk_i32 s4, 0x3000
	s_nop 0
	v_addc_co_u32_e32 v15, vcc, 0, v13, vcc
	v_add_co_u32_e32 v32, vcc, s4, v12
	global_load_dwordx4 v[4:7], v[12:13], off nt
	global_load_dwordx4 v[8:11], v[14:15], off offset:2048 nt
	v_addc_co_u32_e32 v33, vcc, 0, v13, vcc
	v_add_co_u32_e32 v34, vcc, s3, v12
	v_or_b32_e32 v64, 0x6000, v48
	v_mov_b32_e32 v65, v211
	v_addc_co_u32_e32 v35, vcc, 0, v13, vcc
	global_load_dwordx4 v[12:15], v[32:33], off nt
	global_load_dwordx4 v[28:31], v[34:35], off offset:2048 nt
	v_lshl_add_u64 v[42:43], v[40:41], 0, v[64:65]
	v_add_u32_e32 v66, 0x7800, v48
	v_mov_b32_e32 v67, v211
	v_add_u32_e32 v74, 0x9000, v48
	v_mov_b32_e32 v75, v211
	v_lshl_add_u64 v[44:45], v[40:41], 0, v[66:67]
	global_load_dwordx4 v[32:35], v[42:43], off nt
	global_load_dwordx4 v[36:39], v[44:45], off nt
	v_lshl_add_u64 v[50:51], v[40:41], 0, v[74:75]
	v_add_u32_e32 v76, 0xa800, v48
	v_mov_b32_e32 v77, v211
	v_lshl_add_u64 v[52:53], v[40:41], 0, v[76:77]
	global_load_dwordx4 v[40:43], v[50:51], off nt
	global_load_dwordx4 v[44:47], v[52:53], off nt
	v_lshl_add_u64 v[48:49], v[72:73], 0, v[48:49]
	v_lshl_add_u64 v[140:141], v[48:49], 0, v[210:211]
	s_mov_b64 s[4:5], 0x1800
	v_lshl_add_u64 v[142:143], v[140:141], 0, s[4:5]
	s_mov_b64 s[4:5], 0x3000
	v_lshl_add_u64 v[64:65], v[72:73], 0, v[64:65]
	v_lshl_add_u64 v[74:75], v[72:73], 0, v[74:75]
	v_lshl_add_u64 v[144:145], v[140:141], 0, s[4:5]
	s_mov_b64 s[4:5], 0x4800
	v_lshl_add_u64 v[148:149], v[64:65], 0, v[210:211]
	v_lshl_add_u64 v[64:65], v[72:73], 0, v[66:67]
	v_lshl_add_u64 v[152:153], v[74:75], 0, v[210:211]
	v_lshl_add_u64 v[72:73], v[72:73], 0, v[76:77]
	global_load_dwordx4 v[48:51], v[140:141], off offset:256 nt
	global_load_dwordx4 v[52:55], v[142:143], off offset:256 nt
	v_lshl_add_u64 v[146:147], v[140:141], 0, s[4:5]
	global_load_dwordx4 v[56:59], v[144:145], off offset:256 nt
	global_load_dwordx4 v[60:63], v[146:147], off offset:256 nt
	v_lshl_add_u64 v[150:151], v[64:65], 0, v[210:211]
	global_load_dwordx4 v[64:67], v[148:149], off offset:256 nt
	global_load_dwordx4 v[68:71], v[150:151], off offset:256 nt
	v_lshl_add_u64 v[154:155], v[72:73], 0, v[210:211]
	global_load_dwordx4 v[72:75], v[152:153], off offset:256 nt
	global_load_dwordx4 v[76:79], v[154:155], off offset:256 nt
	v_mov_b32_e32 v236, v208
	v_add_u32_e32 v237, 0x2000, v208
	v_add_u32_e32 v238, 0x4000, v208
	global_load_dwordx4 v[160:163], v236, s[22:23]
	global_load_dwordx4 v[164:167], v237, s[22:23]
	global_load_dwordx4 v[168:171], v238, s[22:23]
	s_add_u32 s20, s22, 24576
	s_addc_u32 s21, s23, 0
	global_load_dwordx4 v[172:175], v236, s[20:21]
	global_load_dwordx4 v[176:179], v237, s[20:21]
	global_load_dwordx4 v[180:183], v238, s[20:21]
	s_add_u32 s20, s22, 49152
	s_addc_u32 s21, s23, 0
	global_load_dwordx4 v[184:187], v236, s[20:21]
	global_load_dwordx4 v[188:191], v237, s[20:21]
	global_load_dwordx4 v[192:195], v238, s[20:21]
	s_add_u32 s20, s22, 73728
	s_addc_u32 s21, s23, 0
	global_load_dwordx4 v[196:199], v236, s[20:21]
	global_load_dwordx4 v[200:203], v237, s[20:21]
	global_load_dwordx4 v[204:207], v238, s[20:21]
	s_add_u32 s20, s22, 98304
	s_addc_u32 s21, s23, 0
	global_load_dwordx4 v[216:219], v236, s[20:21]
	global_load_dwordx4 v[220:223], v237, s[20:21]
	global_load_dwordx4 v[224:227], v238, s[20:21]
	v_mul_u32_u24_e32 v82, 0x1200, v214
	v_lshl_or_b32 v80, v80, 3, v82
	s_movk_i32 s3, 0x90
	v_mad_u32_u24 v1, v1, s3, v80
	v_add_u32_e32 v157, 0x1e000, v1
	v_and_b32_e32 v81, 31, v0
	v_lshrrev_b32_e32 v83, 1, v0
	v_add_u32_e32 v1, 0x1e800, v1
	v_mul_u32_u24_e32 v81, 0x90, v81
	v_and_b32_e32 v83, 16, v83
	v_add3_u32 v156, v82, v81, v83
	v_add_u32_e32 v156, 0x12000, v156
	s_load_dwordx2 s[0:1], s[0:1], 0x20
	s_mov_b32 s3, 0
	v_and_b32_e32 v0, 63, v0
	s_waitcnt vmcnt(30)
	v_cvt_pk_f16_f32 v7, v6, v7
	v_cvt_pk_f16_f32 v6, v4, v5
	s_waitcnt vmcnt(29)
	v_cvt_pk_f16_f32 v5, v10, v11
	v_cvt_pk_f16_f32 v4, v8, v9
	ds_write2_b64 v157, v[6:7], v[4:5] offset1:72
	s_waitcnt vmcnt(28)
	v_cvt_pk_f16_f32 v5, v14, v15
	v_cvt_pk_f16_f32 v4, v12, v13
	s_waitcnt vmcnt(27)
	v_cvt_pk_f16_f32 v7, v30, v31
	v_cvt_pk_f16_f32 v6, v28, v29
	ds_write2_b64 v157, v[4:5], v[6:7] offset0:144 offset1:216
	s_waitcnt vmcnt(26)
	v_cvt_pk_f16_f32 v5, v34, v35
	v_cvt_pk_f16_f32 v4, v32, v33
	s_waitcnt vmcnt(25)
	v_cvt_pk_f16_f32 v7, v38, v39
	v_cvt_pk_f16_f32 v6, v36, v37
	ds_write2_b64 v1, v[4:5], v[6:7] offset0:32 offset1:104
	s_waitcnt vmcnt(24)
	v_cvt_pk_f16_f32 v5, v42, v43
	v_cvt_pk_f16_f32 v4, v40, v41
	s_waitcnt vmcnt(23)
	v_cvt_pk_f16_f32 v7, v46, v47
	v_cvt_pk_f16_f32 v6, v44, v45
	ds_write2_b64 v1, v[4:5], v[6:7] offset0:176 offset1:248
	ds_read_b128 v[28:31], v156 offset:49152
	ds_read_b128 v[32:35], v156 offset:49184
	ds_read_b128 v[36:39], v156 offset:49216
	ds_read_b128 v[40:43], v156 offset:49248
	global_load_dwordx4 v[4:7], v[140:141], off offset:512 nt
	global_load_dwordx4 v[8:11], v[142:143], off offset:512 nt
	global_load_dwordx4 v[12:15], v[144:145], off offset:512 nt
	global_load_dwordx4 v[80:83], v[146:147], off offset:512 nt
	global_load_dwordx4 v[84:87], v[148:149], off offset:512 nt
	global_load_dwordx4 v[88:91], v[150:151], off offset:512 nt
	global_load_dwordx4 v[92:95], v[152:153], off offset:512 nt
	global_load_dwordx4 v[96:99], v[154:155], off offset:512 nt
	s_waitcnt vmcnt(15)
	v_cvt_pk_f16_f32 v45, v50, v51
	v_cvt_pk_f16_f32 v44, v48, v49
	s_waitcnt vmcnt(14)
	v_cvt_pk_f16_f32 v47, v54, v55
	v_cvt_pk_f16_f32 v46, v52, v53
	ds_write2_b64 v157, v[44:45], v[46:47] offset1:72
	s_waitcnt vmcnt(13)
	v_cvt_pk_f16_f32 v45, v58, v59
	v_cvt_pk_f16_f32 v44, v56, v57
	s_waitcnt vmcnt(12)
	v_cvt_pk_f16_f32 v47, v62, v63
	v_cvt_pk_f16_f32 v46, v60, v61
	ds_write2_b64 v157, v[44:45], v[46:47] offset0:144 offset1:216
	s_waitcnt vmcnt(11)
	v_cvt_pk_f16_f32 v45, v66, v67
	v_cvt_pk_f16_f32 v44, v64, v65
	s_waitcnt vmcnt(10)
	v_cvt_pk_f16_f32 v47, v70, v71
	v_cvt_pk_f16_f32 v46, v68, v69
	ds_write2_b64 v1, v[44:45], v[46:47] offset0:32 offset1:104
	s_waitcnt vmcnt(9)
	v_cvt_pk_f16_f32 v45, v74, v75
	v_cvt_pk_f16_f32 v44, v72, v73
	s_waitcnt vmcnt(8)
	v_cvt_pk_f16_f32 v47, v78, v79
	v_cvt_pk_f16_f32 v46, v76, v77
	ds_write2_b64 v1, v[44:45], v[46:47] offset0:176 offset1:248
	ds_read_b128 v[44:47], v156 offset:49152
	ds_read_b128 v[48:51], v156 offset:49184
	ds_read_b128 v[52:55], v156 offset:49216
	ds_read_b128 v[56:59], v156 offset:49248
	global_load_dwordx4 v[76:79], v[140:141], off offset:768 nt
	global_load_dwordx4 v[100:103], v[142:143], off offset:768 nt
	global_load_dwordx4 v[104:107], v[144:145], off offset:768 nt
	global_load_dwordx4 v[108:111], v[146:147], off offset:768 nt
	global_load_dwordx4 v[112:115], v[148:149], off offset:768 nt
	global_load_dwordx4 v[116:119], v[150:151], off offset:768 nt
	global_load_dwordx4 v[120:123], v[152:153], off offset:768 nt
	global_load_dwordx4 v[124:127], v[154:155], off offset:768 nt
	s_mul_i32 s14, s2, 9
	s_mul_i32 s15, s12, 6
	v_lshlrev_b32_e32 v239, 4, v0
	v_add_u32_e32 v240, 0xc000, v239
	v_add_u32_e32 v242, 0x18000, v239
	v_lshlrev_b32_e32 v241, 12, v214
	v_or_b32_e32 v241, v241, v239
	v_add_u32_e32 v252, 0x12000, v236
	v_add_u32_e32 v253, 0x12000, v237
	v_add_u32_e32 v254, 0x12000, v238
	ds_write_b128 v236, v[160:163] offset:0
	ds_write_b128 v237, v[164:167] offset:0
	ds_write_b128 v238, v[168:171] offset:0
	ds_write_b128 v236, v[172:175] offset:24576
	ds_write_b128 v237, v[176:179] offset:24576
	ds_write_b128 v238, v[180:183] offset:24576
	ds_write_b128 v236, v[184:187] offset:49152
	ds_write_b128 v237, v[188:191] offset:49152
	ds_write_b128 v238, v[192:195] offset:49152
	ds_write_b128 v252, v[196:199] offset:0
	ds_write_b128 v253, v[200:203] offset:0
	ds_write_b128 v254, v[204:207] offset:0
	ds_write_b128 v252, v[216:219] offset:24576
	ds_write_b128 v253, v[220:223] offset:24576
	ds_write_b128 v254, v[224:227] offset:24576
	s_waitcnt lgkmcnt(0)
	s_barrier
	ds_read_b128 v[216:219], v239 offset:0
	ds_read_b128 v[220:223], v239 offset:24576
	ds_read_b128 v[224:227], v240 offset:0
	ds_read_b128 v[228:231], v239 offset:1024
	s_waitcnt lgkmcnt(3)
	v_mfma_f32_32x32x16_f16 v[160:175], v[28:31], v[216:219], 0
	ds_read_b128 v[216:219], v239 offset:25600
	s_waitcnt lgkmcnt(3)
	v_mfma_f32_32x32x16_f16 v[176:191], v[28:31], v[220:223], 0
	ds_read_b128 v[220:223], v240 offset:1024
	s_waitcnt lgkmcnt(3)
	v_mfma_f32_32x32x16_f16 v[192:207], v[28:31], v[224:227], 0
	ds_read_b128 v[224:227], v239 offset:2048
	s_waitcnt lgkmcnt(3)
	v_mfma_f32_32x32x16_f16 v[160:175], v[32:35], v[228:231], v[160:175]
	ds_read_b128 v[228:231], v239 offset:26624
	s_waitcnt lgkmcnt(3)
	v_mfma_f32_32x32x16_f16 v[176:191], v[32:35], v[216:219], v[176:191]
	ds_read_b128 v[216:219], v240 offset:2048
	s_waitcnt lgkmcnt(3)
	v_mfma_f32_32x32x16_f16 v[192:207], v[32:35], v[220:223], v[192:207]
	ds_read_b128 v[220:223], v239 offset:3072
	s_waitcnt lgkmcnt(3)
	v_mfma_f32_32x32x16_f16 v[160:175], v[36:39], v[224:227], v[160:175]
	ds_read_b128 v[224:227], v239 offset:27648
	s_waitcnt lgkmcnt(3)
	v_mfma_f32_32x32x16_f16 v[176:191], v[36:39], v[228:231], v[176:191]
	ds_read_b128 v[228:231], v240 offset:3072
	s_waitcnt lgkmcnt(3)
	v_mfma_f32_32x32x16_f16 v[192:207], v[36:39], v[216:219], v[192:207]
	s_waitcnt lgkmcnt(2)
	v_mfma_f32_32x32x16_f16 v[160:175], v[40:43], v[220:223], v[160:175]
	s_waitcnt lgkmcnt(1)
	v_mfma_f32_32x32x16_f16 v[176:191], v[40:43], v[224:227], v[176:191]
	s_waitcnt lgkmcnt(0)
	v_mfma_f32_32x32x16_f16 v[192:207], v[40:43], v[228:231], v[192:207]
	ds_read_b128 v[216:219], v239 offset:4096
	ds_read_b128 v[220:223], v239 offset:28672
	ds_read_b128 v[224:227], v240 offset:4096
	ds_read_b128 v[228:231], v239 offset:5120
	s_waitcnt lgkmcnt(3)
	v_mfma_f32_32x32x16_f16 v[160:175], v[44:47], v[216:219], v[160:175]
	ds_read_b128 v[216:219], v239 offset:29696
	s_waitcnt lgkmcnt(3)
	v_mfma_f32_32x32x16_f16 v[176:191], v[44:47], v[220:223], v[176:191]
	ds_read_b128 v[220:223], v240 offset:5120
	s_waitcnt lgkmcnt(3)
	v_mfma_f32_32x32x16_f16 v[192:207], v[44:47], v[224:227], v[192:207]
	ds_read_b128 v[224:227], v239 offset:6144
	s_waitcnt lgkmcnt(3)
	v_mfma_f32_32x32x16_f16 v[160:175], v[48:51], v[228:231], v[160:175]
	ds_read_b128 v[228:231], v239 offset:30720
	s_waitcnt lgkmcnt(3)
	v_mfma_f32_32x32x16_f16 v[176:191], v[48:51], v[216:219], v[176:191]
	ds_read_b128 v[216:219], v240 offset:6144
	s_waitcnt lgkmcnt(3)
	v_mfma_f32_32x32x16_f16 v[192:207], v[48:51], v[220:223], v[192:207]
	ds_read_b128 v[220:223], v239 offset:7168
	s_waitcnt lgkmcnt(3)
	v_mfma_f32_32x32x16_f16 v[160:175], v[52:55], v[224:227], v[160:175]
	ds_read_b128 v[224:227], v239 offset:31744
	s_waitcnt lgkmcnt(3)
	v_mfma_f32_32x32x16_f16 v[176:191], v[52:55], v[228:231], v[176:191]
	ds_read_b128 v[228:231], v240 offset:7168
	s_waitcnt lgkmcnt(3)
	v_mfma_f32_32x32x16_f16 v[192:207], v[52:55], v[216:219], v[192:207]
	s_waitcnt lgkmcnt(2)
	v_mfma_f32_32x32x16_f16 v[160:175], v[56:59], v[220:223], v[160:175]
	s_waitcnt lgkmcnt(1)
	v_mfma_f32_32x32x16_f16 v[176:191], v[56:59], v[224:227], v[176:191]
	s_waitcnt lgkmcnt(0)
	v_mfma_f32_32x32x16_f16 v[192:207], v[56:59], v[228:231], v[192:207]
	s_waitcnt vmcnt(15)
	v_cvt_pk_f16_f32 v7, v6, v7
	v_cvt_pk_f16_f32 v6, v4, v5
	s_waitcnt vmcnt(14)
	v_cvt_pk_f16_f32 v5, v10, v11
	v_cvt_pk_f16_f32 v4, v8, v9
	ds_write2_b64 v157, v[6:7], v[4:5] offset1:72
	s_waitcnt vmcnt(13)
	v_cvt_pk_f16_f32 v5, v14, v15
	v_cvt_pk_f16_f32 v4, v12, v13
	s_waitcnt vmcnt(12)
	v_cvt_pk_f16_f32 v7, v82, v83
	v_cvt_pk_f16_f32 v6, v80, v81
	ds_write2_b64 v157, v[4:5], v[6:7] offset0:144 offset1:216
	s_waitcnt vmcnt(11)
	v_cvt_pk_f16_f32 v5, v86, v87
	v_cvt_pk_f16_f32 v4, v84, v85
	s_waitcnt vmcnt(10)
	v_cvt_pk_f16_f32 v7, v90, v91
	v_cvt_pk_f16_f32 v6, v88, v89
	ds_write2_b64 v1, v[4:5], v[6:7] offset0:32 offset1:104
	s_waitcnt vmcnt(9)
	v_cvt_pk_f16_f32 v5, v94, v95
	v_cvt_pk_f16_f32 v4, v92, v93
	s_waitcnt vmcnt(8)
	v_cvt_pk_f16_f32 v7, v98, v99
	v_cvt_pk_f16_f32 v6, v96, v97
	ds_write2_b64 v1, v[4:5], v[6:7] offset0:176 offset1:248
	ds_read_b128 v[60:63], v156 offset:49152
	ds_read_b128 v[64:67], v156 offset:49184
	ds_read_b128 v[68:71], v156 offset:49216
	ds_read_b128 v[72:75], v156 offset:49248
	global_load_dwordx4 v[4:7], v[140:141], off offset:1024 nt
	global_load_dwordx4 v[8:11], v[142:143], off offset:1024 nt
	global_load_dwordx4 v[12:15], v[144:145], off offset:1024 nt
	global_load_dwordx4 v[92:95], v[146:147], off offset:1024 nt
	global_load_dwordx4 v[96:99], v[148:149], off offset:1024 nt
	global_load_dwordx4 v[128:131], v[150:151], off offset:1024 nt
	global_load_dwordx4 v[132:135], v[152:153], off offset:1024 nt
	global_load_dwordx4 v[136:139], v[154:155], off offset:1024 nt
	ds_read_b128 v[216:219], v239 offset:8192
	ds_read_b128 v[220:223], v239 offset:32768
	ds_read_b128 v[224:227], v240 offset:8192
	ds_read_b128 v[228:231], v239 offset:9216
	s_waitcnt lgkmcnt(3)
	v_mfma_f32_32x32x16_f16 v[160:175], v[60:63], v[216:219], v[160:175]
	ds_read_b128 v[216:219], v239 offset:33792
	s_waitcnt lgkmcnt(3)
	v_mfma_f32_32x32x16_f16 v[176:191], v[60:63], v[220:223], v[176:191]
	ds_read_b128 v[220:223], v240 offset:9216
	s_waitcnt lgkmcnt(3)
	v_mfma_f32_32x32x16_f16 v[192:207], v[60:63], v[224:227], v[192:207]
	ds_read_b128 v[224:227], v239 offset:10240
	s_waitcnt lgkmcnt(3)
	v_mfma_f32_32x32x16_f16 v[160:175], v[64:67], v[228:231], v[160:175]
	ds_read_b128 v[228:231], v239 offset:34816
	s_waitcnt lgkmcnt(3)
	v_mfma_f32_32x32x16_f16 v[176:191], v[64:67], v[216:219], v[176:191]
	ds_read_b128 v[216:219], v240 offset:10240
	s_waitcnt lgkmcnt(3)
	v_mfma_f32_32x32x16_f16 v[192:207], v[64:67], v[220:223], v[192:207]
	ds_read_b128 v[220:223], v239 offset:11264
	s_waitcnt lgkmcnt(3)
	v_mfma_f32_32x32x16_f16 v[160:175], v[68:71], v[224:227], v[160:175]
	ds_read_b128 v[224:227], v239 offset:35840
	s_waitcnt lgkmcnt(3)
	v_mfma_f32_32x32x16_f16 v[176:191], v[68:71], v[228:231], v[176:191]
	ds_read_b128 v[228:231], v240 offset:11264
	s_waitcnt lgkmcnt(3)
	v_mfma_f32_32x32x16_f16 v[192:207], v[68:71], v[216:219], v[192:207]
	s_waitcnt lgkmcnt(2)
	v_mfma_f32_32x32x16_f16 v[160:175], v[72:75], v[220:223], v[160:175]
	s_waitcnt lgkmcnt(1)
	v_mfma_f32_32x32x16_f16 v[176:191], v[72:75], v[224:227], v[176:191]
	s_waitcnt lgkmcnt(0)
	v_mfma_f32_32x32x16_f16 v[192:207], v[72:75], v[228:231], v[192:207]
	s_waitcnt vmcnt(15)
	v_cvt_pk_f16_f32 v79, v78, v79
	v_cvt_pk_f16_f32 v78, v76, v77
	s_waitcnt vmcnt(14)
	v_cvt_pk_f16_f32 v77, v102, v103
	v_cvt_pk_f16_f32 v76, v100, v101
	ds_write2_b64 v157, v[78:79], v[76:77] offset1:72
	s_waitcnt vmcnt(13)
	v_cvt_pk_f16_f32 v77, v106, v107
	v_cvt_pk_f16_f32 v76, v104, v105
	s_waitcnt vmcnt(12)
	v_cvt_pk_f16_f32 v79, v110, v111
	v_cvt_pk_f16_f32 v78, v108, v109
	ds_write2_b64 v157, v[76:77], v[78:79] offset0:144 offset1:216
	s_waitcnt vmcnt(11)
	v_cvt_pk_f16_f32 v77, v114, v115
	v_cvt_pk_f16_f32 v76, v112, v113
	s_waitcnt vmcnt(10)
	v_cvt_pk_f16_f32 v79, v118, v119
	v_cvt_pk_f16_f32 v78, v116, v117
	ds_write2_b64 v1, v[76:77], v[78:79] offset0:32 offset1:104
	s_waitcnt vmcnt(9)
	v_cvt_pk_f16_f32 v77, v122, v123
	v_cvt_pk_f16_f32 v76, v120, v121
	s_waitcnt vmcnt(8)
	v_cvt_pk_f16_f32 v79, v126, v127
	v_cvt_pk_f16_f32 v78, v124, v125
	ds_write2_b64 v1, v[76:77], v[78:79] offset0:176 offset1:248
	ds_read_b128 v[76:79], v156 offset:49152
	ds_read_b128 v[80:83], v156 offset:49184
	ds_read_b128 v[84:87], v156 offset:49216
	ds_read_b128 v[88:91], v156 offset:49248
	global_load_dwordx4 v[108:111], v[140:141], off offset:1280 nt
	global_load_dwordx4 v[112:115], v[142:143], off offset:1280 nt
	global_load_dwordx4 v[116:119], v[144:145], off offset:1280 nt
	global_load_dwordx4 v[120:123], v[146:147], off offset:1280 nt
	global_load_dwordx4 v[124:127], v[148:149], off offset:1280 nt
	s_nop 0
	global_load_dwordx4 v[140:143], v[150:151], off offset:1280 nt
	global_load_dwordx4 v[144:147], v[152:153], off offset:1280 nt
	s_nop 0
	global_load_dwordx4 v[148:151], v[154:155], off offset:1280 nt
	ds_read_b128 v[216:219], v239 offset:12288
	ds_read_b128 v[220:223], v239 offset:36864
	ds_read_b128 v[224:227], v240 offset:12288
	ds_read_b128 v[228:231], v239 offset:13312
	s_waitcnt lgkmcnt(3)
	v_mfma_f32_32x32x16_f16 v[160:175], v[76:79], v[216:219], v[160:175]
	ds_read_b128 v[216:219], v239 offset:37888
	s_waitcnt lgkmcnt(3)
	v_mfma_f32_32x32x16_f16 v[176:191], v[76:79], v[220:223], v[176:191]
	ds_read_b128 v[220:223], v240 offset:13312
	s_waitcnt lgkmcnt(3)
	v_mfma_f32_32x32x16_f16 v[192:207], v[76:79], v[224:227], v[192:207]
	ds_read_b128 v[224:227], v239 offset:14336
	s_waitcnt lgkmcnt(3)
	v_mfma_f32_32x32x16_f16 v[160:175], v[80:83], v[228:231], v[160:175]
	ds_read_b128 v[228:231], v239 offset:38912
	s_waitcnt lgkmcnt(3)
	v_mfma_f32_32x32x16_f16 v[176:191], v[80:83], v[216:219], v[176:191]
	ds_read_b128 v[216:219], v240 offset:14336
	s_waitcnt lgkmcnt(3)
	v_mfma_f32_32x32x16_f16 v[192:207], v[80:83], v[220:223], v[192:207]
	ds_read_b128 v[220:223], v239 offset:15360
	s_waitcnt lgkmcnt(3)
	v_mfma_f32_32x32x16_f16 v[160:175], v[84:87], v[224:227], v[160:175]
	ds_read_b128 v[224:227], v239 offset:39936
	s_waitcnt lgkmcnt(3)
	v_mfma_f32_32x32x16_f16 v[176:191], v[84:87], v[228:231], v[176:191]
	ds_read_b128 v[228:231], v240 offset:15360
	s_waitcnt lgkmcnt(3)
	v_mfma_f32_32x32x16_f16 v[192:207], v[84:87], v[216:219], v[192:207]
	s_waitcnt lgkmcnt(2)
	v_mfma_f32_32x32x16_f16 v[160:175], v[88:91], v[220:223], v[160:175]
	s_waitcnt lgkmcnt(1)
	v_mfma_f32_32x32x16_f16 v[176:191], v[88:91], v[224:227], v[176:191]
	s_waitcnt lgkmcnt(0)
	v_mfma_f32_32x32x16_f16 v[192:207], v[88:91], v[228:231], v[192:207]
	s_waitcnt vmcnt(15)
	v_cvt_pk_f16_f32 v7, v6, v7
	v_cvt_pk_f16_f32 v6, v4, v5
	s_waitcnt vmcnt(14)
	v_cvt_pk_f16_f32 v5, v10, v11
	v_cvt_pk_f16_f32 v4, v8, v9
	ds_write2_b64 v157, v[6:7], v[4:5] offset1:72
	s_waitcnt vmcnt(13)
	v_cvt_pk_f16_f32 v5, v14, v15
	v_cvt_pk_f16_f32 v4, v12, v13
	s_waitcnt vmcnt(12)
	v_cvt_pk_f16_f32 v7, v94, v95
	v_cvt_pk_f16_f32 v6, v92, v93
	ds_write2_b64 v157, v[4:5], v[6:7] offset0:144 offset1:216
	s_waitcnt vmcnt(11)
	v_cvt_pk_f16_f32 v5, v98, v99
	v_cvt_pk_f16_f32 v4, v96, v97
	s_waitcnt vmcnt(10)
	v_cvt_pk_f16_f32 v7, v130, v131
	v_cvt_pk_f16_f32 v6, v128, v129
	ds_write2_b64 v1, v[4:5], v[6:7] offset0:32 offset1:104
	s_waitcnt vmcnt(9)
	v_cvt_pk_f16_f32 v5, v134, v135
	v_cvt_pk_f16_f32 v4, v132, v133
	s_waitcnt vmcnt(8)
	v_cvt_pk_f16_f32 v7, v138, v139
	v_cvt_pk_f16_f32 v6, v136, v137
	ds_write2_b64 v1, v[4:5], v[6:7] offset0:176 offset1:248
	ds_read_b128 v[92:95], v156 offset:49152
	ds_read_b128 v[96:99], v156 offset:49184
	ds_read_b128 v[100:103], v156 offset:49216
	ds_read_b128 v[104:107], v156 offset:49248
	ds_read_b128 v[216:219], v239 offset:16384
	ds_read_b128 v[220:223], v239 offset:40960
	ds_read_b128 v[224:227], v240 offset:16384
	ds_read_b128 v[228:231], v239 offset:17408
	s_waitcnt lgkmcnt(3)
	v_mfma_f32_32x32x16_f16 v[160:175], v[92:95], v[216:219], v[160:175]
	ds_read_b128 v[216:219], v239 offset:41984
	s_waitcnt lgkmcnt(3)
	v_mfma_f32_32x32x16_f16 v[176:191], v[92:95], v[220:223], v[176:191]
	ds_read_b128 v[220:223], v240 offset:17408
	s_waitcnt lgkmcnt(3)
	v_mfma_f32_32x32x16_f16 v[192:207], v[92:95], v[224:227], v[192:207]
	ds_read_b128 v[224:227], v239 offset:18432
	s_waitcnt lgkmcnt(3)
	v_mfma_f32_32x32x16_f16 v[160:175], v[96:99], v[228:231], v[160:175]
	ds_read_b128 v[228:231], v239 offset:43008
	s_waitcnt lgkmcnt(3)
	v_mfma_f32_32x32x16_f16 v[176:191], v[96:99], v[216:219], v[176:191]
	ds_read_b128 v[216:219], v240 offset:18432
	s_waitcnt lgkmcnt(3)
	v_mfma_f32_32x32x16_f16 v[192:207], v[96:99], v[220:223], v[192:207]
	ds_read_b128 v[220:223], v239 offset:19456
	s_waitcnt lgkmcnt(3)
	v_mfma_f32_32x32x16_f16 v[160:175], v[100:103], v[224:227], v[160:175]
	ds_read_b128 v[224:227], v239 offset:44032
	s_waitcnt lgkmcnt(3)
	v_mfma_f32_32x32x16_f16 v[176:191], v[100:103], v[228:231], v[176:191]
	ds_read_b128 v[228:231], v240 offset:19456
	s_waitcnt lgkmcnt(3)
	v_mfma_f32_32x32x16_f16 v[192:207], v[100:103], v[216:219], v[192:207]
	s_waitcnt lgkmcnt(2)
	v_mfma_f32_32x32x16_f16 v[160:175], v[104:107], v[220:223], v[160:175]
	s_waitcnt lgkmcnt(1)
	v_mfma_f32_32x32x16_f16 v[176:191], v[104:107], v[224:227], v[176:191]
	s_waitcnt lgkmcnt(0)
	v_mfma_f32_32x32x16_f16 v[192:207], v[104:107], v[228:231], v[192:207]
	s_waitcnt vmcnt(7)
	v_cvt_pk_f16_f32 v5, v110, v111
	v_cvt_pk_f16_f32 v4, v108, v109
	s_waitcnt vmcnt(6)
	v_cvt_pk_f16_f32 v7, v114, v115
	v_cvt_pk_f16_f32 v6, v112, v113
	ds_write2_b64 v157, v[4:5], v[6:7] offset1:72
	s_waitcnt vmcnt(5)
	v_cvt_pk_f16_f32 v5, v118, v119
	v_cvt_pk_f16_f32 v4, v116, v117
	s_waitcnt vmcnt(4)
	v_cvt_pk_f16_f32 v7, v122, v123
	v_cvt_pk_f16_f32 v6, v120, v121
	ds_write2_b64 v157, v[4:5], v[6:7] offset0:144 offset1:216
	s_waitcnt vmcnt(3)
	v_cvt_pk_f16_f32 v5, v126, v127
	v_cvt_pk_f16_f32 v4, v124, v125
	s_waitcnt vmcnt(2)
	v_cvt_pk_f16_f32 v7, v142, v143
	v_cvt_pk_f16_f32 v6, v140, v141
	ds_write2_b64 v1, v[4:5], v[6:7] offset0:32 offset1:104
	s_waitcnt vmcnt(1)
	v_cvt_pk_f16_f32 v5, v146, v147
	v_cvt_pk_f16_f32 v4, v144, v145
	s_waitcnt vmcnt(0)
	v_cvt_pk_f16_f32 v7, v150, v151
	v_cvt_pk_f16_f32 v6, v148, v149
	ds_write2_b64 v1, v[4:5], v[6:7] offset0:176 offset1:248
	ds_read_b128 v[108:111], v156 offset:49152
	ds_read_b128 v[112:115], v156 offset:49184
	ds_read_b128 v[116:119], v156 offset:49216
	ds_read_b128 v[120:123], v156 offset:49248
	ds_read_b128 v[216:219], v239 offset:20480
	ds_read_b128 v[220:223], v239 offset:45056
	ds_read_b128 v[224:227], v240 offset:20480
	ds_read_b128 v[228:231], v239 offset:21504
	s_waitcnt lgkmcnt(3)
	v_mfma_f32_32x32x16_f16 v[160:175], v[108:111], v[216:219], v[160:175]
	ds_read_b128 v[216:219], v239 offset:46080
	s_waitcnt lgkmcnt(3)
	v_mfma_f32_32x32x16_f16 v[176:191], v[108:111], v[220:223], v[176:191]
	ds_read_b128 v[220:223], v240 offset:21504
	s_waitcnt lgkmcnt(3)
	v_mfma_f32_32x32x16_f16 v[192:207], v[108:111], v[224:227], v[192:207]
	ds_read_b128 v[224:227], v239 offset:22528
	s_waitcnt lgkmcnt(3)
	v_mfma_f32_32x32x16_f16 v[160:175], v[112:115], v[228:231], v[160:175]
	ds_read_b128 v[228:231], v239 offset:47104
	s_waitcnt lgkmcnt(3)
	v_mfma_f32_32x32x16_f16 v[176:191], v[112:115], v[216:219], v[176:191]
	ds_read_b128 v[216:219], v240 offset:22528
	s_waitcnt lgkmcnt(3)
	v_mfma_f32_32x32x16_f16 v[192:207], v[112:115], v[220:223], v[192:207]
	ds_read_b128 v[220:223], v239 offset:23552
	s_waitcnt lgkmcnt(3)
	v_mfma_f32_32x32x16_f16 v[160:175], v[116:119], v[224:227], v[160:175]
	ds_read_b128 v[224:227], v239 offset:48128
	s_waitcnt lgkmcnt(3)
	v_mfma_f32_32x32x16_f16 v[176:191], v[116:119], v[228:231], v[176:191]
	ds_read_b128 v[228:231], v240 offset:23552
	s_waitcnt lgkmcnt(3)
	v_mfma_f32_32x32x16_f16 v[192:207], v[116:119], v[216:219], v[192:207]
	s_waitcnt lgkmcnt(2)
	v_mfma_f32_32x32x16_f16 v[160:175], v[120:123], v[220:223], v[160:175]
	s_waitcnt lgkmcnt(1)
	v_mfma_f32_32x32x16_f16 v[176:191], v[120:123], v[224:227], v[176:191]
	s_waitcnt lgkmcnt(0)
	v_mfma_f32_32x32x16_f16 v[192:207], v[120:123], v[228:231], v[192:207]
	s_add_i32 s20, s14, 0
	s_cmp_lt_u32 s20, 12
	s_cselect_b32 s26, s8, s10
	s_cselect_b32 s27, s9, s11
	s_cselect_b32 s21, 0, 12
	s_cmp_lt_u32 s20, 24
	s_cselect_b32 s26, s26, s0
	s_cselect_b32 s27, s27, s1
	s_cselect_b32 s21, s21, 24
	s_sub_i32 s20, s20, s21
	s_lshr_b32 s21, s20, 1
	s_and_b32 s20, s20, 1
	s_add_i32 s21, s21, s15
	s_lshl_b32 s21, s21, 15
	s_lshl_b32 s20, s20, 11
	s_add_i32 s21, s21, s20
	s_add_u32 s26, s26, s21
	s_addc_u32 s27, s27, 0
	s_mov_b64 s[28:29], s[26:27]
	s_add_i32 s20, s14, 1
	s_cmp_lt_u32 s20, 12
	s_cselect_b32 s26, s8, s10
	s_cselect_b32 s27, s9, s11
	s_cselect_b32 s21, 0, 12
	s_cmp_lt_u32 s20, 24
	s_cselect_b32 s26, s26, s0
	s_cselect_b32 s27, s27, s1
	s_cselect_b32 s21, s21, 24
	s_sub_i32 s20, s20, s21
	s_lshr_b32 s21, s20, 1
	s_and_b32 s20, s20, 1
	s_add_i32 s21, s21, s15
	s_lshl_b32 s21, s21, 15
	s_lshl_b32 s20, s20, 11
	s_add_i32 s21, s21, s20
	s_add_u32 s26, s26, s21
	s_addc_u32 s27, s27, 0
	s_mov_b64 s[30:31], s[26:27]
	s_add_i32 s20, s14, 2
	s_cmp_lt_u32 s20, 12
	s_cselect_b32 s26, s8, s10
	s_cselect_b32 s27, s9, s11
	s_cselect_b32 s21, 0, 12
	s_cmp_lt_u32 s20, 24
	s_cselect_b32 s26, s26, s0
	s_cselect_b32 s27, s27, s1
	s_cselect_b32 s21, s21, 24
	s_sub_i32 s20, s20, s21
	s_lshr_b32 s21, s20, 1
	s_and_b32 s20, s20, 1
	s_add_i32 s21, s21, s15
	s_lshl_b32 s21, s21, 15
	s_lshl_b32 s20, s20, 11
	s_add_i32 s21, s21, s20
	s_add_u32 s26, s26, s21
	s_addc_u32 s27, s27, 0
	v_cvt_pk_f16_f32 v244, v160, v161
	v_cvt_pk_f16_f32 v245, v162, v163
	v_cvt_pk_f16_f32 v246, v164, v165
	v_cvt_pk_f16_f32 v247, v166, v167
	v_cvt_pk_f16_f32 v248, v168, v169
	v_cvt_pk_f16_f32 v249, v170, v171
	v_cvt_pk_f16_f32 v250, v172, v173
	v_cvt_pk_f16_f32 v251, v174, v175
	global_store_dwordx4 v241, v[244:247], s[28:29]
	global_store_dwordx4 v241, v[248:251], s[28:29] offset:1024
	v_cvt_pk_f16_f32 v124, v176, v177
	v_cvt_pk_f16_f32 v125, v178, v179
	v_cvt_pk_f16_f32 v126, v180, v181
	v_cvt_pk_f16_f32 v127, v182, v183
	v_cvt_pk_f16_f32 v128, v184, v185
	v_cvt_pk_f16_f32 v129, v186, v187
	v_cvt_pk_f16_f32 v130, v188, v189
	v_cvt_pk_f16_f32 v131, v190, v191
	global_store_dwordx4 v241, v[124:127], s[30:31]
	global_store_dwordx4 v241, v[128:131], s[30:31] offset:1024
	v_cvt_pk_f16_f32 v132, v192, v193
	v_cvt_pk_f16_f32 v133, v194, v195
	v_cvt_pk_f16_f32 v134, v196, v197
	v_cvt_pk_f16_f32 v135, v198, v199
	v_cvt_pk_f16_f32 v136, v200, v201
	v_cvt_pk_f16_f32 v137, v202, v203
	v_cvt_pk_f16_f32 v138, v204, v205
	v_cvt_pk_f16_f32 v139, v206, v207
	global_store_dwordx4 v241, v[132:135], s[26:27]
	global_store_dwordx4 v241, v[136:139], s[26:27] offset:1024
	s_waitcnt lgkmcnt(0)
	s_barrier
.Lqkv_p2N:
	ds_read_b128 v[124:127], v240 offset:24576
	ds_read_b128 v[128:131], v240 offset:25600
	ds_read_b128 v[132:135], v240 offset:26624
	ds_read_b128 v[136:139], v240 offset:27648
	ds_read_b128 v[140:143], v240 offset:28672
	ds_read_b128 v[144:147], v240 offset:29696
	ds_read_b128 v[148:151], v240 offset:30720
	ds_read_b128 v[152:155], v240 offset:31744
	ds_read_b128 v[156:159], v240 offset:32768
	ds_read_b128 v[160:163], v240 offset:33792
	ds_read_b128 v[164:167], v240 offset:34816
	ds_read_b128 v[168:171], v240 offset:35840
	ds_read_b128 v[172:175], v240 offset:36864
	ds_read_b128 v[176:179], v240 offset:37888
	ds_read_b128 v[180:183], v240 offset:38912
	ds_read_b128 v[184:187], v240 offset:39936
	ds_read_b128 v[188:191], v240 offset:40960
	ds_read_b128 v[192:195], v240 offset:41984
	ds_read_b128 v[196:199], v240 offset:43008
	ds_read_b128 v[200:203], v240 offset:44032
	ds_read_b128 v[204:207], v240 offset:45056
	ds_read_b128 v[208:211], v240 offset:46080
	ds_read_b128 v[212:215], v240 offset:47104
	ds_read_b128 v[216:219], v240 offset:48128
	s_add_u32 s24, s22, 122880
	s_addc_u32 s25, s23, 0
	s_waitcnt lgkmcnt(14)
	v_mfma_f32_32x32x16_f16 v[0:15], v[28:31], v[124:127], 0
	ds_read_b128 v[124:127], v242 offset:0
	global_load_dwordx4 v[16:19], v236, s[24:25]
	global_load_dwordx4 v[20:23], v237, s[24:25]
	global_load_dwordx4 v[24:27], v238, s[24:25]
	s_waitcnt lgkmcnt(14)
	v_mfma_f32_32x32x16_f16 v[0:15], v[32:35], v[128:131], v[0:15]
	ds_read_b128 v[128:131], v242 offset:1024
	s_waitcnt lgkmcnt(14)
	v_mfma_f32_32x32x16_f16 v[0:15], v[36:39], v[132:135], v[0:15]
	ds_read_b128 v[132:135], v242 offset:2048
	s_waitcnt lgkmcnt(14)
	v_mfma_f32_32x32x16_f16 v[0:15], v[40:43], v[136:139], v[0:15]
	ds_read_b128 v[136:139], v242 offset:3072
	s_waitcnt lgkmcnt(14)
	v_mfma_f32_32x32x16_f16 v[0:15], v[44:47], v[140:143], v[0:15]
	ds_read_b128 v[140:143], v242 offset:4096
	s_waitcnt lgkmcnt(14)
	v_mfma_f32_32x32x16_f16 v[0:15], v[48:51], v[144:147], v[0:15]
	ds_read_b128 v[144:147], v242 offset:5120
	s_waitcnt lgkmcnt(14)
	v_mfma_f32_32x32x16_f16 v[0:15], v[52:55], v[148:151], v[0:15]
	ds_read_b128 v[148:151], v242 offset:6144
	s_waitcnt lgkmcnt(14)
	v_mfma_f32_32x32x16_f16 v[0:15], v[56:59], v[152:155], v[0:15]
	ds_read_b128 v[152:155], v242 offset:7168
	s_waitcnt lgkmcnt(14)
	v_mfma_f32_32x32x16_f16 v[0:15], v[60:63], v[156:159], v[0:15]
	ds_read_b128 v[156:159], v242 offset:8192
	s_waitcnt lgkmcnt(14)
	v_mfma_f32_32x32x16_f16 v[0:15], v[64:67], v[160:163], v[0:15]
	ds_read_b128 v[160:163], v242 offset:9216
	s_waitcnt lgkmcnt(14)
	v_mfma_f32_32x32x16_f16 v[0:15], v[68:71], v[164:167], v[0:15]
	ds_read_b128 v[164:167], v242 offset:10240
	s_waitcnt lgkmcnt(14)
	v_mfma_f32_32x32x16_f16 v[0:15], v[72:75], v[168:171], v[0:15]
	ds_read_b128 v[168:171], v242 offset:11264
	s_waitcnt lgkmcnt(14)
	v_mfma_f32_32x32x16_f16 v[0:15], v[76:79], v[172:175], v[0:15]
	ds_read_b128 v[172:175], v242 offset:12288
	s_waitcnt lgkmcnt(14)
	v_mfma_f32_32x32x16_f16 v[0:15], v[80:83], v[176:179], v[0:15]
	ds_read_b128 v[176:179], v242 offset:13312
	s_waitcnt lgkmcnt(14)
	v_mfma_f32_32x32x16_f16 v[0:15], v[84:87], v[180:183], v[0:15]
	ds_read_b128 v[180:183], v242 offset:14336
	s_waitcnt lgkmcnt(14)
	v_mfma_f32_32x32x16_f16 v[0:15], v[88:91], v[184:187], v[0:15]
	ds_read_b128 v[184:187], v242 offset:15360
	s_waitcnt lgkmcnt(14)
	v_mfma_f32_32x32x16_f16 v[0:15], v[92:95], v[188:191], v[0:15]
	ds_read_b128 v[188:191], v242 offset:16384
	s_waitcnt lgkmcnt(14)
	v_mfma_f32_32x32x16_f16 v[0:15], v[96:99], v[192:195], v[0:15]
	ds_read_b128 v[192:195], v242 offset:17408
	s_waitcnt lgkmcnt(14)
	v_mfma_f32_32x32x16_f16 v[0:15], v[100:103], v[196:199], v[0:15]
	ds_read_b128 v[196:199], v242 offset:18432
	s_waitcnt vmcnt(0)
	ds_write_b128 v252, v[16:19] offset:49152
	ds_write_b128 v253, v[20:23] offset:49152
	ds_write_b128 v254, v[24:27] offset:49152
	s_waitcnt lgkmcnt(14)
	v_mfma_f32_32x32x16_f16 v[0:15], v[104:107], v[200:203], v[0:15]
	ds_read_b128 v[200:203], v242 offset:19456
	s_waitcnt lgkmcnt(14)
	v_mfma_f32_32x32x16_f16 v[0:15], v[108:111], v[204:207], v[0:15]
	ds_read_b128 v[204:207], v242 offset:20480
	s_waitcnt lgkmcnt(14)
	v_mfma_f32_32x32x16_f16 v[0:15], v[112:115], v[208:211], v[0:15]
	ds_read_b128 v[208:211], v242 offset:21504
	s_waitcnt lgkmcnt(14)
	v_mfma_f32_32x32x16_f16 v[0:15], v[116:119], v[212:215], v[0:15]
	ds_read_b128 v[212:215], v242 offset:22528
	s_waitcnt lgkmcnt(14)
	v_mfma_f32_32x32x16_f16 v[0:15], v[120:123], v[216:219], v[0:15]
	ds_read_b128 v[216:219], v242 offset:23552
	s_waitcnt lgkmcnt(5)
	s_barrier
	s_add_u32 s24, s22, 147456
	s_addc_u32 s25, s23, 0
	s_waitcnt lgkmcnt(14)
	v_mfma_f32_32x32x16_f16 v[220:235], v[28:31], v[124:127], 0
	ds_read_b128 v[124:127], v242 offset:24576
	global_load_dwordx4 v[16:19], v236, s[24:25]
	global_load_dwordx4 v[20:23], v237, s[24:25]
	global_load_dwordx4 v[24:27], v238, s[24:25]
	s_waitcnt lgkmcnt(14)
	v_mfma_f32_32x32x16_f16 v[220:235], v[32:35], v[128:131], v[220:235]
	ds_read_b128 v[128:131], v242 offset:25600
	s_add_i32 s20, s14, 3
	s_cmp_lt_u32 s20, 12
	s_cselect_b32 s26, s8, s10
	s_cselect_b32 s27, s9, s11
	s_waitcnt lgkmcnt(14)
	v_mfma_f32_32x32x16_f16 v[220:235], v[36:39], v[132:135], v[220:235]
	ds_read_b128 v[132:135], v242 offset:26624
	s_cselect_b32 s21, 0, 12
	s_cmp_lt_u32 s20, 24
	s_cselect_b32 s26, s26, s0
	s_cselect_b32 s27, s27, s1
	s_waitcnt lgkmcnt(14)
	v_mfma_f32_32x32x16_f16 v[220:235], v[40:43], v[136:139], v[220:235]
	ds_read_b128 v[136:139], v242 offset:27648
	s_cselect_b32 s21, s21, 24
	s_sub_i32 s20, s20, s21
	s_lshr_b32 s21, s20, 1
	s_and_b32 s20, s20, 1
	s_waitcnt lgkmcnt(14)
	v_mfma_f32_32x32x16_f16 v[220:235], v[44:47], v[140:143], v[220:235]
	ds_read_b128 v[140:143], v242 offset:28672
	s_add_i32 s21, s21, s15
	s_lshl_b32 s21, s21, 15
	s_lshl_b32 s20, s20, 11
	s_add_i32 s21, s21, s20
	s_waitcnt lgkmcnt(14)
	v_mfma_f32_32x32x16_f16 v[220:235], v[48:51], v[144:147], v[220:235]
	ds_read_b128 v[144:147], v242 offset:29696
	s_add_u32 s26, s26, s21
	s_addc_u32 s27, s27, 0
	s_waitcnt lgkmcnt(14)
	v_mfma_f32_32x32x16_f16 v[220:235], v[52:55], v[148:151], v[220:235]
	ds_read_b128 v[148:151], v242 offset:30720
	v_cvt_pk_f16_f32 v244, v0, v1
	v_cvt_pk_f16_f32 v245, v2, v3
	s_waitcnt lgkmcnt(14)
	v_mfma_f32_32x32x16_f16 v[220:235], v[56:59], v[152:155], v[220:235]
	ds_read_b128 v[152:155], v242 offset:31744
	v_cvt_pk_f16_f32 v246, v4, v5
	v_cvt_pk_f16_f32 v247, v6, v7
	s_waitcnt lgkmcnt(14)
	v_mfma_f32_32x32x16_f16 v[220:235], v[60:63], v[156:159], v[220:235]
	ds_read_b128 v[156:159], v242 offset:32768
	v_cvt_pk_f16_f32 v248, v8, v9
	v_cvt_pk_f16_f32 v249, v10, v11
	s_waitcnt lgkmcnt(14)
	v_mfma_f32_32x32x16_f16 v[220:235], v[64:67], v[160:163], v[220:235]
	ds_read_b128 v[160:163], v242 offset:33792
	v_cvt_pk_f16_f32 v250, v12, v13
	v_cvt_pk_f16_f32 v251, v14, v15
	s_waitcnt lgkmcnt(14)
	v_mfma_f32_32x32x16_f16 v[220:235], v[68:71], v[164:167], v[220:235]
	ds_read_b128 v[164:167], v242 offset:34816
	global_store_dwordx4 v241, v[244:247], s[26:27]
	s_waitcnt lgkmcnt(14)
	v_mfma_f32_32x32x16_f16 v[220:235], v[72:75], v[168:171], v[220:235]
	ds_read_b128 v[168:171], v242 offset:35840
	global_store_dwordx4 v241, v[248:251], s[26:27] offset:1024
	s_waitcnt lgkmcnt(14)
	v_mfma_f32_32x32x16_f16 v[220:235], v[76:79], v[172:175], v[220:235]
	ds_read_b128 v[172:175], v242 offset:36864
	s_waitcnt lgkmcnt(14)
	v_mfma_f32_32x32x16_f16 v[220:235], v[80:83], v[176:179], v[220:235]
	ds_read_b128 v[176:179], v242 offset:37888
	s_waitcnt lgkmcnt(14)
	v_mfma_f32_32x32x16_f16 v[220:235], v[84:87], v[180:183], v[220:235]
	ds_read_b128 v[180:183], v242 offset:38912
	s_waitcnt lgkmcnt(14)
	v_mfma_f32_32x32x16_f16 v[220:235], v[88:91], v[184:187], v[220:235]
	ds_read_b128 v[184:187], v242 offset:39936
	s_waitcnt lgkmcnt(14)
	v_mfma_f32_32x32x16_f16 v[220:235], v[92:95], v[188:191], v[220:235]
	ds_read_b128 v[188:191], v242 offset:40960
	s_waitcnt lgkmcnt(14)
	v_mfma_f32_32x32x16_f16 v[220:235], v[96:99], v[192:195], v[220:235]
	ds_read_b128 v[192:195], v242 offset:41984
	s_waitcnt lgkmcnt(14)
	v_mfma_f32_32x32x16_f16 v[220:235], v[100:103], v[196:199], v[220:235]
	ds_read_b128 v[196:199], v242 offset:43008
	s_waitcnt vmcnt(2)
	ds_write_b128 v236, v[16:19] offset:0
	ds_write_b128 v237, v[20:23] offset:0
	ds_write_b128 v238, v[24:27] offset:0
	s_waitcnt lgkmcnt(14)
	v_mfma_f32_32x32x16_f16 v[220:235], v[104:107], v[200:203], v[220:235]
	ds_read_b128 v[200:203], v242 offset:44032
	s_waitcnt lgkmcnt(14)
	v_mfma_f32_32x32x16_f16 v[220:235], v[108:111], v[204:207], v[220:235]
	ds_read_b128 v[204:207], v242 offset:45056
	s_waitcnt lgkmcnt(14)
	v_mfma_f32_32x32x16_f16 v[220:235], v[112:115], v[208:211], v[220:235]
	ds_read_b128 v[208:211], v242 offset:46080
	s_waitcnt lgkmcnt(14)
	v_mfma_f32_32x32x16_f16 v[220:235], v[116:119], v[212:215], v[220:235]
	ds_read_b128 v[212:215], v242 offset:47104
	s_waitcnt lgkmcnt(14)
	v_mfma_f32_32x32x16_f16 v[220:235], v[120:123], v[216:219], v[220:235]
	ds_read_b128 v[216:219], v242 offset:48128
	s_waitcnt lgkmcnt(5)
	s_barrier
	s_add_u32 s24, s22, 172032
	s_addc_u32 s25, s23, 0
	s_waitcnt lgkmcnt(14)
	v_mfma_f32_32x32x16_f16 v[0:15], v[28:31], v[124:127], 0
	ds_read_b128 v[124:127], v239 offset:0
	global_load_dwordx4 v[16:19], v236, s[24:25]
	global_load_dwordx4 v[20:23], v237, s[24:25]
	global_load_dwordx4 v[24:27], v238, s[24:25]
	s_waitcnt lgkmcnt(14)
	v_mfma_f32_32x32x16_f16 v[0:15], v[32:35], v[128:131], v[0:15]
	ds_read_b128 v[128:131], v239 offset:1024
	s_add_i32 s20, s14, 4
	s_cmp_lt_u32 s20, 12
	s_cselect_b32 s26, s8, s10
	s_cselect_b32 s27, s9, s11
	s_waitcnt lgkmcnt(14)
	v_mfma_f32_32x32x16_f16 v[0:15], v[36:39], v[132:135], v[0:15]
	ds_read_b128 v[132:135], v239 offset:2048
	s_cselect_b32 s21, 0, 12
	s_cmp_lt_u32 s20, 24
	s_cselect_b32 s26, s26, s0
	s_cselect_b32 s27, s27, s1
	s_waitcnt lgkmcnt(14)
	v_mfma_f32_32x32x16_f16 v[0:15], v[40:43], v[136:139], v[0:15]
	ds_read_b128 v[136:139], v239 offset:3072
	s_cselect_b32 s21, s21, 24
	s_sub_i32 s20, s20, s21
	s_lshr_b32 s21, s20, 1
	s_and_b32 s20, s20, 1
	s_waitcnt lgkmcnt(14)
	v_mfma_f32_32x32x16_f16 v[0:15], v[44:47], v[140:143], v[0:15]
	ds_read_b128 v[140:143], v239 offset:4096
	s_add_i32 s21, s21, s15
	s_lshl_b32 s21, s21, 15
	s_lshl_b32 s20, s20, 11
	s_add_i32 s21, s21, s20
	s_waitcnt lgkmcnt(14)
	v_mfma_f32_32x32x16_f16 v[0:15], v[48:51], v[144:147], v[0:15]
	ds_read_b128 v[144:147], v239 offset:5120
	s_add_u32 s26, s26, s21
	s_addc_u32 s27, s27, 0
	s_waitcnt lgkmcnt(14)
	v_mfma_f32_32x32x16_f16 v[0:15], v[52:55], v[148:151], v[0:15]
	ds_read_b128 v[148:151], v239 offset:6144
	v_cvt_pk_f16_f32 v244, v220, v221
	v_cvt_pk_f16_f32 v245, v222, v223
	s_waitcnt lgkmcnt(14)
	v_mfma_f32_32x32x16_f16 v[0:15], v[56:59], v[152:155], v[0:15]
	ds_read_b128 v[152:155], v239 offset:7168
	v_cvt_pk_f16_f32 v246, v224, v225
	v_cvt_pk_f16_f32 v247, v226, v227
	s_waitcnt lgkmcnt(14)
	v_mfma_f32_32x32x16_f16 v[0:15], v[60:63], v[156:159], v[0:15]
	ds_read_b128 v[156:159], v239 offset:8192
	v_cvt_pk_f16_f32 v248, v228, v229
	v_cvt_pk_f16_f32 v249, v230, v231
	s_waitcnt lgkmcnt(14)
	v_mfma_f32_32x32x16_f16 v[0:15], v[64:67], v[160:163], v[0:15]
	ds_read_b128 v[160:163], v239 offset:9216
	v_cvt_pk_f16_f32 v250, v232, v233
	v_cvt_pk_f16_f32 v251, v234, v235
	s_waitcnt lgkmcnt(14)
	v_mfma_f32_32x32x16_f16 v[0:15], v[68:71], v[164:167], v[0:15]
	ds_read_b128 v[164:167], v239 offset:10240
	global_store_dwordx4 v241, v[244:247], s[26:27]
	s_waitcnt lgkmcnt(14)
	v_mfma_f32_32x32x16_f16 v[0:15], v[72:75], v[168:171], v[0:15]
	ds_read_b128 v[168:171], v239 offset:11264
	global_store_dwordx4 v241, v[248:251], s[26:27] offset:1024
	s_waitcnt lgkmcnt(14)
	v_mfma_f32_32x32x16_f16 v[0:15], v[76:79], v[172:175], v[0:15]
	ds_read_b128 v[172:175], v239 offset:12288
	s_waitcnt lgkmcnt(14)
	v_mfma_f32_32x32x16_f16 v[0:15], v[80:83], v[176:179], v[0:15]
	ds_read_b128 v[176:179], v239 offset:13312
	s_waitcnt lgkmcnt(14)
	v_mfma_f32_32x32x16_f16 v[0:15], v[84:87], v[180:183], v[0:15]
	ds_read_b128 v[180:183], v239 offset:14336
	s_waitcnt lgkmcnt(14)
	v_mfma_f32_32x32x16_f16 v[0:15], v[88:91], v[184:187], v[0:15]
	ds_read_b128 v[184:187], v239 offset:15360
	s_waitcnt lgkmcnt(14)
	v_mfma_f32_32x32x16_f16 v[0:15], v[92:95], v[188:191], v[0:15]
	ds_read_b128 v[188:191], v239 offset:16384
	s_waitcnt lgkmcnt(14)
	v_mfma_f32_32x32x16_f16 v[0:15], v[96:99], v[192:195], v[0:15]
	ds_read_b128 v[192:195], v239 offset:17408
	s_waitcnt lgkmcnt(14)
	v_mfma_f32_32x32x16_f16 v[0:15], v[100:103], v[196:199], v[0:15]
	ds_read_b128 v[196:199], v239 offset:18432
	s_waitcnt vmcnt(2)
	ds_write_b128 v236, v[16:19] offset:24576
	ds_write_b128 v237, v[20:23] offset:24576
	ds_write_b128 v238, v[24:27] offset:24576
	s_waitcnt lgkmcnt(14)
	v_mfma_f32_32x32x16_f16 v[0:15], v[104:107], v[200:203], v[0:15]
	ds_read_b128 v[200:203], v239 offset:19456
	s_waitcnt lgkmcnt(14)
	v_mfma_f32_32x32x16_f16 v[0:15], v[108:111], v[204:207], v[0:15]
	ds_read_b128 v[204:207], v239 offset:20480
	s_waitcnt lgkmcnt(14)
	v_mfma_f32_32x32x16_f16 v[0:15], v[112:115], v[208:211], v[0:15]
	ds_read_b128 v[208:211], v239 offset:21504
	s_waitcnt lgkmcnt(14)
	v_mfma_f32_32x32x16_f16 v[0:15], v[116:119], v[212:215], v[0:15]
	ds_read_b128 v[212:215], v239 offset:22528
	s_waitcnt lgkmcnt(14)
	v_mfma_f32_32x32x16_f16 v[0:15], v[120:123], v[216:219], v[0:15]
	ds_read_b128 v[216:219], v239 offset:23552
	s_waitcnt lgkmcnt(5)
	s_barrier
	s_add_u32 s24, s22, 196608
	s_addc_u32 s25, s23, 0
	s_waitcnt lgkmcnt(14)
	v_mfma_f32_32x32x16_f16 v[220:235], v[28:31], v[124:127], 0
	ds_read_b128 v[124:127], v239 offset:24576
	global_load_dwordx4 v[16:19], v236, s[24:25]
	global_load_dwordx4 v[20:23], v237, s[24:25]
	global_load_dwordx4 v[24:27], v238, s[24:25]
	s_waitcnt lgkmcnt(14)
	v_mfma_f32_32x32x16_f16 v[220:235], v[32:35], v[128:131], v[220:235]
	ds_read_b128 v[128:131], v239 offset:25600
	s_add_i32 s20, s14, 5
	s_cmp_lt_u32 s20, 12
	s_cselect_b32 s26, s8, s10
	s_cselect_b32 s27, s9, s11
	s_waitcnt lgkmcnt(14)
	v_mfma_f32_32x32x16_f16 v[220:235], v[36:39], v[132:135], v[220:235]
	ds_read_b128 v[132:135], v239 offset:26624
	s_cselect_b32 s21, 0, 12
	s_cmp_lt_u32 s20, 24
	s_cselect_b32 s26, s26, s0
	s_cselect_b32 s27, s27, s1
	s_waitcnt lgkmcnt(14)
	v_mfma_f32_32x32x16_f16 v[220:235], v[40:43], v[136:139], v[220:235]
	ds_read_b128 v[136:139], v239 offset:27648
	s_cselect_b32 s21, s21, 24
	s_sub_i32 s20, s20, s21
	s_lshr_b32 s21, s20, 1
	s_and_b32 s20, s20, 1
	s_waitcnt lgkmcnt(14)
	v_mfma_f32_32x32x16_f16 v[220:235], v[44:47], v[140:143], v[220:235]
	ds_read_b128 v[140:143], v239 offset:28672
	s_add_i32 s21, s21, s15
	s_lshl_b32 s21, s21, 15
	s_lshl_b32 s20, s20, 11
	s_add_i32 s21, s21, s20
	s_waitcnt lgkmcnt(14)
	v_mfma_f32_32x32x16_f16 v[220:235], v[48:51], v[144:147], v[220:235]
	ds_read_b128 v[144:147], v239 offset:29696
	s_add_u32 s26, s26, s21
	s_addc_u32 s27, s27, 0
	s_waitcnt lgkmcnt(14)
	v_mfma_f32_32x32x16_f16 v[220:235], v[52:55], v[148:151], v[220:235]
	ds_read_b128 v[148:151], v239 offset:30720
	v_cvt_pk_f16_f32 v244, v0, v1
	v_cvt_pk_f16_f32 v245, v2, v3
	s_waitcnt lgkmcnt(14)
	v_mfma_f32_32x32x16_f16 v[220:235], v[56:59], v[152:155], v[220:235]
	ds_read_b128 v[152:155], v239 offset:31744
	v_cvt_pk_f16_f32 v246, v4, v5
	v_cvt_pk_f16_f32 v247, v6, v7
	s_waitcnt lgkmcnt(14)
	v_mfma_f32_32x32x16_f16 v[220:235], v[60:63], v[156:159], v[220:235]
	ds_read_b128 v[156:159], v239 offset:32768
	v_cvt_pk_f16_f32 v248, v8, v9
	v_cvt_pk_f16_f32 v249, v10, v11
	s_waitcnt lgkmcnt(14)
	v_mfma_f32_32x32x16_f16 v[220:235], v[64:67], v[160:163], v[220:235]
	ds_read_b128 v[160:163], v239 offset:33792
	v_cvt_pk_f16_f32 v250, v12, v13
	v_cvt_pk_f16_f32 v251, v14, v15
	s_waitcnt lgkmcnt(14)
	v_mfma_f32_32x32x16_f16 v[220:235], v[68:71], v[164:167], v[220:235]
	ds_read_b128 v[164:167], v239 offset:34816
	global_store_dwordx4 v241, v[244:247], s[26:27]
	s_waitcnt lgkmcnt(14)
	v_mfma_f32_32x32x16_f16 v[220:235], v[72:75], v[168:171], v[220:235]
	ds_read_b128 v[168:171], v239 offset:35840
	global_store_dwordx4 v241, v[248:251], s[26:27] offset:1024
	s_waitcnt lgkmcnt(14)
	v_mfma_f32_32x32x16_f16 v[220:235], v[76:79], v[172:175], v[220:235]
	ds_read_b128 v[172:175], v239 offset:36864
	s_waitcnt lgkmcnt(14)
	v_mfma_f32_32x32x16_f16 v[220:235], v[80:83], v[176:179], v[220:235]
	ds_read_b128 v[176:179], v239 offset:37888
	s_waitcnt lgkmcnt(14)
	v_mfma_f32_32x32x16_f16 v[220:235], v[84:87], v[180:183], v[220:235]
	ds_read_b128 v[180:183], v239 offset:38912
	s_waitcnt lgkmcnt(14)
	v_mfma_f32_32x32x16_f16 v[220:235], v[88:91], v[184:187], v[220:235]
	ds_read_b128 v[184:187], v239 offset:39936
	s_waitcnt lgkmcnt(14)
	v_mfma_f32_32x32x16_f16 v[220:235], v[92:95], v[188:191], v[220:235]
	ds_read_b128 v[188:191], v239 offset:40960
	s_waitcnt lgkmcnt(14)
	v_mfma_f32_32x32x16_f16 v[220:235], v[96:99], v[192:195], v[220:235]
	ds_read_b128 v[192:195], v239 offset:41984
	s_waitcnt lgkmcnt(14)
	v_mfma_f32_32x32x16_f16 v[220:235], v[100:103], v[196:199], v[220:235]
	ds_read_b128 v[196:199], v239 offset:43008
	s_waitcnt vmcnt(2)
	ds_write_b128 v236, v[16:19] offset:49152
	ds_write_b128 v237, v[20:23] offset:49152
	ds_write_b128 v238, v[24:27] offset:49152
	s_waitcnt lgkmcnt(14)
	v_mfma_f32_32x32x16_f16 v[220:235], v[104:107], v[200:203], v[220:235]
	ds_read_b128 v[200:203], v239 offset:44032
	s_waitcnt lgkmcnt(14)
	v_mfma_f32_32x32x16_f16 v[220:235], v[108:111], v[204:207], v[220:235]
	ds_read_b128 v[204:207], v239 offset:45056
	s_waitcnt lgkmcnt(14)
	v_mfma_f32_32x32x16_f16 v[220:235], v[112:115], v[208:211], v[220:235]
	ds_read_b128 v[208:211], v239 offset:46080
	s_waitcnt lgkmcnt(14)
	v_mfma_f32_32x32x16_f16 v[220:235], v[116:119], v[212:215], v[220:235]
	ds_read_b128 v[212:215], v239 offset:47104
	s_waitcnt lgkmcnt(14)
	v_mfma_f32_32x32x16_f16 v[220:235], v[120:123], v[216:219], v[220:235]
	ds_read_b128 v[216:219], v239 offset:48128
	s_waitcnt lgkmcnt(5)
	s_barrier
	s_waitcnt lgkmcnt(14)
	v_mfma_f32_32x32x16_f16 v[0:15], v[28:31], v[124:127], 0
	ds_read_b128 v[124:127], v240 offset:0
	s_waitcnt lgkmcnt(14)
	v_mfma_f32_32x32x16_f16 v[0:15], v[32:35], v[128:131], v[0:15]
	ds_read_b128 v[128:131], v240 offset:1024
	s_add_i32 s20, s14, 6
	s_cmp_lt_u32 s20, 12
	s_cselect_b32 s26, s8, s10
	s_cselect_b32 s27, s9, s11
	s_waitcnt lgkmcnt(14)
	v_mfma_f32_32x32x16_f16 v[0:15], v[36:39], v[132:135], v[0:15]
	ds_read_b128 v[132:135], v240 offset:2048
	s_cselect_b32 s21, 0, 12
	s_cmp_lt_u32 s20, 24
	s_cselect_b32 s26, s26, s0
	s_cselect_b32 s27, s27, s1
	s_waitcnt lgkmcnt(14)
	v_mfma_f32_32x32x16_f16 v[0:15], v[40:43], v[136:139], v[0:15]
	ds_read_b128 v[136:139], v240 offset:3072
	s_cselect_b32 s21, s21, 24
	s_sub_i32 s20, s20, s21
	s_lshr_b32 s21, s20, 1
	s_and_b32 s20, s20, 1
	s_waitcnt lgkmcnt(14)
	v_mfma_f32_32x32x16_f16 v[0:15], v[44:47], v[140:143], v[0:15]
	ds_read_b128 v[140:143], v240 offset:4096
	s_add_i32 s21, s21, s15
	s_lshl_b32 s21, s21, 15
	s_lshl_b32 s20, s20, 11
	s_add_i32 s21, s21, s20
	s_waitcnt lgkmcnt(14)
	v_mfma_f32_32x32x16_f16 v[0:15], v[48:51], v[144:147], v[0:15]
	ds_read_b128 v[144:147], v240 offset:5120
	s_add_u32 s26, s26, s21
	s_addc_u32 s27, s27, 0
	s_waitcnt lgkmcnt(14)
	v_mfma_f32_32x32x16_f16 v[0:15], v[52:55], v[148:151], v[0:15]
	ds_read_b128 v[148:151], v240 offset:6144
	v_cvt_pk_f16_f32 v244, v220, v221
	v_cvt_pk_f16_f32 v245, v222, v223
	s_waitcnt lgkmcnt(14)
	v_mfma_f32_32x32x16_f16 v[0:15], v[56:59], v[152:155], v[0:15]
	ds_read_b128 v[152:155], v240 offset:7168
	v_cvt_pk_f16_f32 v246, v224, v225
	v_cvt_pk_f16_f32 v247, v226, v227
	s_waitcnt lgkmcnt(14)
	v_mfma_f32_32x32x16_f16 v[0:15], v[60:63], v[156:159], v[0:15]
	ds_read_b128 v[156:159], v240 offset:8192
	v_cvt_pk_f16_f32 v248, v228, v229
	v_cvt_pk_f16_f32 v249, v230, v231
	s_waitcnt lgkmcnt(14)
	v_mfma_f32_32x32x16_f16 v[0:15], v[64:67], v[160:163], v[0:15]
	ds_read_b128 v[160:163], v240 offset:9216
	v_cvt_pk_f16_f32 v250, v232, v233
	v_cvt_pk_f16_f32 v251, v234, v235
	s_waitcnt lgkmcnt(14)
	v_mfma_f32_32x32x16_f16 v[0:15], v[68:71], v[164:167], v[0:15]
	ds_read_b128 v[164:167], v240 offset:10240
	global_store_dwordx4 v241, v[244:247], s[26:27]
	s_waitcnt lgkmcnt(14)
	v_mfma_f32_32x32x16_f16 v[0:15], v[72:75], v[168:171], v[0:15]
	ds_read_b128 v[168:171], v240 offset:11264
	global_store_dwordx4 v241, v[248:251], s[26:27] offset:1024
	s_waitcnt lgkmcnt(14)
	v_mfma_f32_32x32x16_f16 v[0:15], v[76:79], v[172:175], v[0:15]
	ds_read_b128 v[172:175], v240 offset:12288
	s_waitcnt lgkmcnt(14)
	v_mfma_f32_32x32x16_f16 v[0:15], v[80:83], v[176:179], v[0:15]
	ds_read_b128 v[176:179], v240 offset:13312
	s_waitcnt lgkmcnt(14)
	v_mfma_f32_32x32x16_f16 v[0:15], v[84:87], v[180:183], v[0:15]
	ds_read_b128 v[180:183], v240 offset:14336
	s_waitcnt lgkmcnt(14)
	v_mfma_f32_32x32x16_f16 v[0:15], v[88:91], v[184:187], v[0:15]
	ds_read_b128 v[184:187], v240 offset:15360
	s_waitcnt lgkmcnt(14)
	v_mfma_f32_32x32x16_f16 v[0:15], v[92:95], v[188:191], v[0:15]
	ds_read_b128 v[188:191], v240 offset:16384
	s_waitcnt lgkmcnt(14)
	v_mfma_f32_32x32x16_f16 v[0:15], v[96:99], v[192:195], v[0:15]
	ds_read_b128 v[192:195], v240 offset:17408
	s_waitcnt lgkmcnt(14)
	v_mfma_f32_32x32x16_f16 v[0:15], v[100:103], v[196:199], v[0:15]
	ds_read_b128 v[196:199], v240 offset:18432
	s_waitcnt lgkmcnt(14)
	v_mfma_f32_32x32x16_f16 v[0:15], v[104:107], v[200:203], v[0:15]
	ds_read_b128 v[200:203], v240 offset:19456
	s_waitcnt lgkmcnt(14)
	v_mfma_f32_32x32x16_f16 v[0:15], v[108:111], v[204:207], v[0:15]
	ds_read_b128 v[204:207], v240 offset:20480
	s_waitcnt lgkmcnt(14)
	v_mfma_f32_32x32x16_f16 v[0:15], v[112:115], v[208:211], v[0:15]
	ds_read_b128 v[208:211], v240 offset:21504
	s_waitcnt lgkmcnt(14)
	v_mfma_f32_32x32x16_f16 v[0:15], v[116:119], v[212:215], v[0:15]
	ds_read_b128 v[212:215], v240 offset:22528
	s_waitcnt lgkmcnt(14)
	v_mfma_f32_32x32x16_f16 v[0:15], v[120:123], v[216:219], v[0:15]
	ds_read_b128 v[216:219], v240 offset:23552
	s_waitcnt lgkmcnt(14)
	v_mfma_f32_32x32x16_f16 v[220:235], v[28:31], v[124:127], 0
	s_waitcnt lgkmcnt(14)
	v_mfma_f32_32x32x16_f16 v[220:235], v[32:35], v[128:131], v[220:235]
	s_add_i32 s20, s14, 7
	s_cmp_lt_u32 s20, 12
	s_cselect_b32 s26, s8, s10
	s_cselect_b32 s27, s9, s11
	s_waitcnt lgkmcnt(14)
	v_mfma_f32_32x32x16_f16 v[220:235], v[36:39], v[132:135], v[220:235]
	s_cselect_b32 s21, 0, 12
	s_cmp_lt_u32 s20, 24
	s_cselect_b32 s26, s26, s0
	s_cselect_b32 s27, s27, s1
	s_waitcnt lgkmcnt(14)
	v_mfma_f32_32x32x16_f16 v[220:235], v[40:43], v[136:139], v[220:235]
	s_cselect_b32 s21, s21, 24
	s_sub_i32 s20, s20, s21
	s_lshr_b32 s21, s20, 1
	s_and_b32 s20, s20, 1
	s_waitcnt lgkmcnt(14)
	v_mfma_f32_32x32x16_f16 v[220:235], v[44:47], v[140:143], v[220:235]
	s_add_i32 s21, s21, s15
	s_lshl_b32 s21, s21, 15
	s_lshl_b32 s20, s20, 11
	s_add_i32 s21, s21, s20
	s_waitcnt lgkmcnt(14)
	v_mfma_f32_32x32x16_f16 v[220:235], v[48:51], v[144:147], v[220:235]
	s_add_u32 s26, s26, s21
	s_addc_u32 s27, s27, 0
	s_waitcnt lgkmcnt(14)
	v_mfma_f32_32x32x16_f16 v[220:235], v[52:55], v[148:151], v[220:235]
	v_cvt_pk_f16_f32 v244, v0, v1
	v_cvt_pk_f16_f32 v245, v2, v3
	s_waitcnt lgkmcnt(14)
	v_mfma_f32_32x32x16_f16 v[220:235], v[56:59], v[152:155], v[220:235]
	v_cvt_pk_f16_f32 v246, v4, v5
	v_cvt_pk_f16_f32 v247, v6, v7
	s_waitcnt lgkmcnt(14)
	v_mfma_f32_32x32x16_f16 v[220:235], v[60:63], v[156:159], v[220:235]
	v_cvt_pk_f16_f32 v248, v8, v9
	v_cvt_pk_f16_f32 v249, v10, v11
	s_waitcnt lgkmcnt(14)
	v_mfma_f32_32x32x16_f16 v[220:235], v[64:67], v[160:163], v[220:235]
	v_cvt_pk_f16_f32 v250, v12, v13
	v_cvt_pk_f16_f32 v251, v14, v15
	s_waitcnt lgkmcnt(13)
	v_mfma_f32_32x32x16_f16 v[220:235], v[68:71], v[164:167], v[220:235]
	global_store_dwordx4 v241, v[244:247], s[26:27]
	s_waitcnt lgkmcnt(12)
	v_mfma_f32_32x32x16_f16 v[220:235], v[72:75], v[168:171], v[220:235]
	global_store_dwordx4 v241, v[248:251], s[26:27] offset:1024
	s_waitcnt lgkmcnt(11)
	v_mfma_f32_32x32x16_f16 v[220:235], v[76:79], v[172:175], v[220:235]
	s_waitcnt lgkmcnt(10)
	v_mfma_f32_32x32x16_f16 v[220:235], v[80:83], v[176:179], v[220:235]
	s_waitcnt lgkmcnt(9)
	v_mfma_f32_32x32x16_f16 v[220:235], v[84:87], v[180:183], v[220:235]
	s_waitcnt lgkmcnt(8)
	v_mfma_f32_32x32x16_f16 v[220:235], v[88:91], v[184:187], v[220:235]
	s_waitcnt lgkmcnt(7)
	v_mfma_f32_32x32x16_f16 v[220:235], v[92:95], v[188:191], v[220:235]
	s_waitcnt lgkmcnt(6)
	v_mfma_f32_32x32x16_f16 v[220:235], v[96:99], v[192:195], v[220:235]
	s_waitcnt lgkmcnt(5)
	v_mfma_f32_32x32x16_f16 v[220:235], v[100:103], v[196:199], v[220:235]
	s_waitcnt lgkmcnt(4)
	v_mfma_f32_32x32x16_f16 v[220:235], v[104:107], v[200:203], v[220:235]
	s_waitcnt lgkmcnt(3)
	v_mfma_f32_32x32x16_f16 v[220:235], v[108:111], v[204:207], v[220:235]
	s_waitcnt lgkmcnt(2)
	v_mfma_f32_32x32x16_f16 v[220:235], v[112:115], v[208:211], v[220:235]
	s_waitcnt lgkmcnt(1)
	v_mfma_f32_32x32x16_f16 v[220:235], v[116:119], v[212:215], v[220:235]
	s_waitcnt lgkmcnt(0)
	v_mfma_f32_32x32x16_f16 v[220:235], v[120:123], v[216:219], v[220:235]
	s_add_i32 s20, s14, 8
	s_cmp_lt_u32 s20, 12
	s_cselect_b32 s26, s8, s10
	s_cselect_b32 s27, s9, s11
	s_cselect_b32 s21, 0, 12
	s_cmp_lt_u32 s20, 24
	s_cselect_b32 s26, s26, s0
	s_cselect_b32 s27, s27, s1
	s_cselect_b32 s21, s21, 24
	s_sub_i32 s20, s20, s21
	s_lshr_b32 s21, s20, 1
	s_and_b32 s20, s20, 1
	s_add_i32 s21, s21, s15
	s_lshl_b32 s21, s21, 15
	s_lshl_b32 s20, s20, 11
	s_add_i32 s21, s21, s20
	s_add_u32 s26, s26, s21
	s_addc_u32 s27, s27, 0
	s_nop 7
	v_cvt_pk_f16_f32 v244, v220, v221
	v_cvt_pk_f16_f32 v245, v222, v223
	v_cvt_pk_f16_f32 v246, v224, v225
	v_cvt_pk_f16_f32 v247, v226, v227
	v_cvt_pk_f16_f32 v248, v228, v229
	v_cvt_pk_f16_f32 v249, v230, v231
	v_cvt_pk_f16_f32 v250, v232, v233
	v_cvt_pk_f16_f32 v251, v234, v235
	global_store_dwordx4 v241, v[244:247], s[26:27]
	global_store_dwordx4 v241, v[248:251], s[26:27] offset:1024
	s_endpgm

	.amdhsa_kernel _Z10qkv_kernelPKfPK15HIP_vector_typeIjLj4EEPDv8_DF16_S6_S6_
		.amdhsa_group_segment_fixed_size 159744
		.amdhsa_private_segment_fixed_size 0
		.amdhsa_kernarg_size 40
		.amdhsa_user_sgpr_count 2
		.amdhsa_user_sgpr_dispatch_ptr 0
		.amdhsa_user_sgpr_queue_ptr 0
		.amdhsa_user_sgpr_kernarg_segment_ptr 1
		.amdhsa_user_sgpr_dispatch_id 0
		.amdhsa_user_sgpr_kernarg_preload_length 0
		.amdhsa_user_sgpr_kernarg_preload_offset 0
		.amdhsa_user_sgpr_private_segment_size 0
		.amdhsa_uses_dynamic_stack 0
		.amdhsa_enable_private_segment 0
		.amdhsa_system_sgpr_workgroup_id_x 1
		.amdhsa_system_sgpr_workgroup_id_y 0
		.amdhsa_system_sgpr_workgroup_id_z 0
		.amdhsa_system_sgpr_workgroup_info 0
		.amdhsa_system_vgpr_workitem_id 0
		.amdhsa_next_free_vgpr 256
		.amdhsa_next_free_sgpr 96
		.amdhsa_accum_offset 256
		.amdhsa_reserve_vcc 1
		.amdhsa_float_round_mode_32 0
		.amdhsa_float_round_mode_16_64 0
		.amdhsa_float_denorm_mode_32 3
		.amdhsa_float_denorm_mode_16_64 3
		.amdhsa_dx10_clamp 1
		.amdhsa_ieee_mode 1
		.amdhsa_fp16_overflow 0
		.amdhsa_tg_split 0
		.amdhsa_exception_fp_ieee_invalid_op 0
		.amdhsa_exception_fp_denorm_src 0
		.amdhsa_exception_fp_ieee_div_zero 0
		.amdhsa_exception_fp_ieee_overflow 0
		.amdhsa_exception_fp_ieee_underflow 0
		.amdhsa_exception_fp_ieee_inexact 0
		.amdhsa_exception_int_div_zero 0
	.end_amdhsa_kernel

amdhsa.kernels:
  - .agpr_count:     0
    .args:
      - .actual_access:  read_only
        .address_space:  global
        .offset:         0
        .size:           8
        .value_kind:     global_buffer
      - .actual_access:  read_only
        .address_space:  global
        .offset:         8
        .size:           8
        .value_kind:     global_buffer
      - .actual_access:  read_only
        .address_space:  global
        .offset:         16
        .size:           8
        .value_kind:     global_buffer
      - .actual_access:  read_only
        .address_space:  global
        .offset:         24
        .size:           8
        .value_kind:     global_buffer
      - .actual_access:  write_only
        .address_space:  global
        .offset:         32
        .size:           8
        .value_kind:     global_buffer
      - .actual_access:  write_only
        .address_space:  global
        .offset:         40
        .size:           8
        .value_kind:     global_buffer
    .group_segment_fixed_size: 0
    .kernarg_segment_align: 8
    .kernarg_segment_size: 48
    .language:       OpenCL C
    .language_version:
      - 2
      - 0
    .max_flat_workgroup_size: 64
    .name:           _Z11prep_kernelPKfS0_S0_S0_PDv8_DF16_S2_
    .private_segment_fixed_size: 0
    .sgpr_count:     19
    .sgpr_spill_count: 0
    .symbol:         _Z11prep_kernelPKfS0_S0_S0_PDv8_DF16_S2_.kd
    .uniform_work_group_size: 1
    .uses_dynamic_stack: false
    .vgpr_count:     26
    .vgpr_spill_count: 0
    .wavefront_size: 64
  - .agpr_count:     0
    .args:
      - .actual_access:  read_only
        .address_space:  global
        .offset:         0
        .size:           8
        .value_kind:     global_buffer
      - .actual_access:  read_only
        .address_space:  global
        .offset:         8
        .size:           8
        .value_kind:     global_buffer
      - .actual_access:  write_only
        .address_space:  global
        .offset:         16
        .size:           8
        .value_kind:     global_buffer
      - .actual_access:  write_only
        .address_space:  global
        .offset:         24
        .size:           8
        .value_kind:     global_buffer
      - .actual_access:  write_only
        .address_space:  global
        .offset:         32
        .size:           8
        .value_kind:     global_buffer
    .group_segment_fixed_size: 159744
    .kernarg_segment_align: 8
    .kernarg_segment_size: 40
    .language:       OpenCL C
    .language_version:
      - 2
      - 0
    .max_flat_workgroup_size: 512
    .name:           _Z10qkv_kernelPKfPK15HIP_vector_typeIjLj4EEPDv8_DF16_S6_S6_
    .private_segment_fixed_size: 0
    .sgpr_count:     28
    .sgpr_spill_count: 0
    .symbol:         _Z10qkv_kernelPKfPK15HIP_vector_typeIjLj4EEPDv8_DF16_S6_S6_.kd
    .uniform_work_group_size: 1
    .uses_dynamic_stack: false
    .vgpr_count:     256
    .vgpr_spill_count: 0
    .wavefront_size: 64
  - .agpr_count:     0
    .args:
      - .actual_access:  read_only
        .address_space:  global
        .offset:         0
        .size:           8
        .value_kind:     global_buffer
      - .actual_access:  read_only
        .address_space:  global
        .offset:         8
        .size:           8
        .value_kind:     global_buffer
      - .actual_access:  read_only
        .address_space:  global
        .offset:         16
        .size:           8
        .value_kind:     global_buffer
      - .actual_access:  read_only
        .address_space:  global
        .offset:         24
        .size:           8
        .value_kind:     global_buffer
      - .actual_access:  read_only
        .address_space:  global
        .offset:         32
        .size:           8
        .value_kind:     global_buffer
      - .actual_access:  write_only
        .address_space:  global
        .offset:         40
        .size:           8
        .value_kind:     global_buffer
    .group_segment_fixed_size: 101376
    .kernarg_segment_align: 8
    .kernarg_segment_size: 48
    .language:       OpenCL C
    .language_version:
      - 2
      - 0
    .max_flat_workgroup_size: 768
    .name:           _Z15attn_out_kernelPKDv8_DF16_S1_S1_S1_PKfPf
    .private_segment_fixed_size: 0
    .sgpr_count:     62
    .sgpr_spill_count: 0
    .symbol:         _Z15attn_out_kernelPKDv8_DF16_S1_S1_S1_PKfPf.kd
    .uniform_work_group_size: 1
    .uses_dynamic_stack: false
    .vgpr_count:     158
    .vgpr_spill_count: 0
    .wavefront_size: 64
